# attention inner loop: softmax VALU stream merged into the QK^T MFMA gaps (QK^T temporaries renamed to free VGPRs), second QK^T block rebuilt without the 23 splat moves, trailing 16 exps issued inside
# speedup vs baseline: 1.0039x; 1.0039x over previous
; #define LAS __attribute__((address_space(3)))
; __device__ __forceinline__ void finishSM(f32x16& p0, f32x16& p1, float& l_reg, bf16x8& pa0, bf16x8& pa1, bf16x8& pa2, bf16x8& pa3) {
;   for (int r = 0; r < 16; ++r) p1[r] = __builtin_amdgcn_exp2f(p1[r]);
;   float ps = 0; for (int r = 0; r < 16; ++r) ps += p0[r]; for (int r = 0; r < 16; ++r) ps += p1[r];
;   { auto rr = __builtin_amdgcn_permlane32_swap(__float_as_uint(ps), __float_as_uint(ps), false, false);
;     ps = __uint_as_float(rr[0]) + __uint_as_float(rr[1]); }
;   l_reg += ps;
;     ...
;   PK4(p0, 0, pa0); PK4(p0, 8, pa1); PK4(p1, 0, pa2); PK4(p1, 8, pa3);
;     ...
; }
; __device__ __forceinline__ void qkt(f32x16& p0, f32x16& p1, const LAS char* Ks, const bf16x8* qr, int r32, int hi, float nm) {
; #pragma unroll
;   for (int r = 0; r < 16; ++r) { p0[r] = nm; p1[r] = nm; }
; #pragma unroll
;   for (int d0 = 0; d0 < DQK / 16; ++d0) { int cb = (d0 * 16 + hi * 8) * 2;
;     bf16x8 b0 = *reinterpret_cast<const LAS bf16x8*>(Ks + KSWZ(r32, cb));
;     bf16x8 b1 = *reinterpret_cast<const LAS bf16x8*>(Ks + KSWZ(32 + r32, cb));
;     __builtin_amdgcn_s_setprio(1);
;     p0 = __builtin_amdgcn_mfma_f32_32x32x16_bf16(b0, qr[d0], p0, 0, 0, 0);
;     p1 = __builtin_amdgcn_mfma_f32_32x32x16_bf16(b1, qr[d0], p1, 0, 0, 0);
;     __builtin_amdgcn_s_setprio(0); }
.LBB0_603:
	s_mov_b32 s72, s4
	s_lshl_b32 s4, s70, 14
	s_add_i32 s73, s4, 0
	v_add_u32_e32 v242, s73, v192
	v_add_u32_e32 v238, v242, v198
	ds_read_b128 v[234:237], v238 offset:24576
	ds_read_b128 v[238:241], v238 offset:32768
	v_add_f32_e32 v33, 0, v80
	v_add_f32_e32 v33, v81, v33
	v_add_f32_e32 v33, v82, v33
	v_add_f32_e32 v33, v83, v33
	v_add_f32_e32 v33, v84, v33
	s_setprio 1
	s_waitcnt lgkmcnt(1)
	v_mfma_f32_32x32x16_bf16 v[112:127], v[234:237], v[128:131], v[48:63]
	v_add_f32_e32 v33, v85, v33
	v_add_f32_e32 v33, v86, v33
	v_add_f32_e32 v33, v87, v33
	v_add_f32_e32 v33, v88, v33
	s_waitcnt lgkmcnt(0)
	v_mfma_f32_32x32x16_bf16 v[96:111], v[238:241], v[128:131], v[48:63]
	s_setprio 0
	v_add_f32_e32 v33, v89, v33
	v_add_f32_e32 v33, v90, v33
	v_add_f32_e32 v33, v91, v33
	v_add_u32_e32 v238, v242, v199
	ds_read_b128 v[234:237], v238 offset:24576
	ds_read_b128 v[238:241], v238 offset:32768
	v_exp_f32_e32 v64, v64
	v_add_f32_e32 v33, v92, v33
	v_exp_f32_e32 v65, v65
	v_add_f32_e32 v33, v93, v33
	v_exp_f32_e32 v66, v66
	s_setprio 1
	s_waitcnt lgkmcnt(1)
	v_mfma_f32_32x32x16_bf16 v[112:127], v[234:237], v[132:135], v[112:127]
	v_add_f32_e32 v33, v94, v33
	v_exp_f32_e32 v67, v67
	v_add_f32_e32 v33, v95, v33
	v_exp_f32_e32 v68, v68
	s_waitcnt lgkmcnt(0)
	v_mfma_f32_32x32x16_bf16 v[96:111], v[238:241], v[132:135], v[96:111]
	s_setprio 0
	v_add_f32_e32 v33, v64, v33
	v_exp_f32_e32 v69, v69
	v_add_f32_e32 v33, v65, v33
	v_add_u32_e32 v238, v242, v200
	ds_read_b128 v[234:237], v238 offset:24576
	ds_read_b128 v[238:241], v238 offset:32768
	v_exp_f32_e32 v70, v70
	v_add_f32_e32 v33, v66, v33
	v_exp_f32_e32 v71, v71
	v_add_f32_e32 v33, v67, v33
	v_exp_f32_e32 v72, v72
	s_setprio 1
	s_waitcnt lgkmcnt(1)
	v_mfma_f32_32x32x16_bf16 v[112:127], v[234:237], v[136:139], v[112:127]
	v_add_f32_e32 v33, v68, v33
	v_exp_f32_e32 v73, v73
	v_add_f32_e32 v33, v69, v33
	v_exp_f32_e32 v74, v74
	s_waitcnt lgkmcnt(0)
	v_mfma_f32_32x32x16_bf16 v[96:111], v[238:241], v[136:139], v[96:111]
	s_setprio 0
	v_add_f32_e32 v33, v70, v33
	v_exp_f32_e32 v75, v75
	v_add_f32_e32 v33, v71, v33
	v_add_u32_e32 v238, v242, v201
	ds_read_b128 v[234:237], v238 offset:24576
	ds_read_b128 v[238:241], v238 offset:32768
	v_exp_f32_e32 v76, v76
	v_add_f32_e32 v33, v72, v33
	v_exp_f32_e32 v77, v77
	v_add_f32_e32 v33, v73, v33
	v_exp_f32_e32 v78, v78
	s_setprio 1
	s_waitcnt lgkmcnt(1)
	v_mfma_f32_32x32x16_bf16 v[112:127], v[234:237], v[140:143], v[112:127]
	v_add_f32_e32 v33, v74, v33
	v_exp_f32_e32 v79, v79
	v_add_f32_e32 v33, v75, v33
	v_add_f32_e32 v33, v76, v33
	s_waitcnt lgkmcnt(0)
	v_mfma_f32_32x32x16_bf16 v[96:111], v[238:241], v[140:143], v[96:111]
	s_setprio 0
	v_add_f32_e32 v33, v77, v33
	v_add_f32_e32 v33, v78, v33
	v_add_f32_e32 v204, v79, v33
	v_add_u32_e32 v238, v242, v202
	ds_read_b128 v[234:237], v238 offset:24576
	ds_read_b128 v[238:241], v238 offset:32768
	v_mov_b32_e32 v205, v204
	v_cvt_pk_bf16_f32 v34, v80, v81
	v_cvt_pk_bf16_f32 v35, v82, v83
	v_cvt_pk_bf16_f32 v36, v84, v85
	v_cvt_pk_bf16_f32 v37, v86, v87
	s_setprio 1
	s_waitcnt lgkmcnt(1)
	v_mfma_f32_32x32x16_bf16 v[112:127], v[234:237], v[148:151], v[112:127]
	v_cvt_pk_bf16_f32 v38, v88, v89
	v_cvt_pk_bf16_f32 v39, v90, v91
	v_cvt_pk_bf16_f32 v40, v92, v93
	v_cvt_pk_bf16_f32 v41, v94, v95
	s_waitcnt lgkmcnt(0)
	v_mfma_f32_32x32x16_bf16 v[96:111], v[238:241], v[148:151], v[96:111]
	s_setprio 0
	v_cvt_pk_bf16_f32 v42, v64, v65
	v_cvt_pk_bf16_f32 v43, v66, v67
	v_cvt_pk_bf16_f32 v44, v68, v69
	v_add_u32_e32 v242, v242, v203
	ds_read_b128 v[234:237], v242 offset:24576
	ds_read_b128 v[238:241], v242 offset:32768
	v_cvt_pk_bf16_f32 v45, v70, v71
	v_cvt_pk_bf16_f32 v164, v72, v73
	v_cvt_pk_bf16_f32 v165, v74, v75
	v_cvt_pk_bf16_f32 v166, v76, v77
	v_cvt_pk_bf16_f32 v167, v78, v79
	s_setprio 1
	s_waitcnt lgkmcnt(1)
	v_mfma_f32_32x32x16_bf16 v[112:127], v[234:237], v[144:147], v[112:127]
	s_nop 1
	v_permlane32_swap_b32_e32 v204, v205
	v_permlane32_swap_b32_e32 v34, v36
	v_permlane32_swap_b32_e32 v35, v37
	s_waitcnt lgkmcnt(0)
	v_mfma_f32_32x32x16_bf16 v[96:111], v[238:241], v[144:147], v[96:111]
	s_setprio 0
	v_permlane32_swap_b32_e32 v38, v40
	v_permlane32_swap_b32_e32 v39, v41
	v_permlane32_swap_b32_e32 v42, v44
	v_permlane32_swap_b32_e32 v43, v45
	v_permlane32_swap_b32_e32 v164, v166
	v_permlane32_swap_b32_e32 v165, v167
	s_cmp_lt_u32 s71, 61
	s_cselect_b64 s[4:5], -1, 0
	s_cmp_gt_u32 s71, 60
	v_lshl_add_u64 v[180:181], s[22:23], 0, v[176:177]
	v_lshl_add_u64 v[178:179], s[22:23], 0, v[174:175]
	s_cbranch_scc1 .LBB0_605
	v_add_co_u32_e32 v46, vcc, 0x66006000, v180
	s_nop 1
	v_addc_co_u32_e32 v47, vcc, 0, v181, vcc
	s_waitcnt vmcnt(1)
	v_add_co_u32_e32 v156, vcc, 0x6200c000, v178
	s_nop 1
	v_addc_co_u32_e32 v157, vcc, 0, v179, vcc
	global_load_dwordx4 v[152:155], v[46:47], off
	s_nop 0
	global_load_dwordx4 v[156:159], v[156:157], off
	v_add_co_u32_e32 v46, vcc, 0x6200e000, v178
	s_nop 1
	v_addc_co_u32_e32 v47, vcc, 0, v179, vcc
	global_load_dwordx4 v[160:163], v[46:47], off

; #define LAS __attribute__((address_space(3)))
; __device__ __forceinline__ void finishSM(f32x16& p0, f32x16& p1, float& l_reg, bf16x8& pa0, bf16x8& pa1, bf16x8& pa2, bf16x8& pa3) {
;   for (int r = 0; r < 16; ++r) p1[r] = __builtin_amdgcn_exp2f(p1[r]);
;   float ps = 0; for (int r = 0; r < 16; ++r) ps += p0[r]; for (int r = 0; r < 16; ++r) ps += p1[r];
;   { auto rr = __builtin_amdgcn_permlane32_swap(__float_as_uint(ps), __float_as_uint(ps), false, false);
;     ps = __uint_as_float(rr[0]) + __uint_as_float(rr[1]); }
;   l_reg += ps;
;     ...
;   PK4(p0, 0, pa0); PK4(p0, 8, pa1); PK4(p1, 0, pa2); PK4(p1, 8, pa3);
;     ...
; }
; __device__ __forceinline__ void qkt(f32x16& p0, f32x16& p1, const LAS char* Ks, const bf16x8* qr, int r32, int hi, float nm) {
; #pragma unroll
;   for (int r = 0; r < 16; ++r) { p0[r] = nm; p1[r] = nm; }
; #pragma unroll
;   for (int d0 = 0; d0 < DQK / 16; ++d0) { int cb = (d0 * 16 + hi * 8) * 2;
;     bf16x8 b0 = *reinterpret_cast<const LAS bf16x8*>(Ks + KSWZ(r32, cb));
;     bf16x8 b1 = *reinterpret_cast<const LAS bf16x8*>(Ks + KSWZ(32 + r32, cb));
;     __builtin_amdgcn_s_setprio(1);
;     p0 = __builtin_amdgcn_mfma_f32_32x32x16_bf16(b0, qr[d0], p0, 0, 0, 0);
;     p1 = __builtin_amdgcn_mfma_f32_32x32x16_bf16(b1, qr[d0], p1, 0, 0, 0);
;     __builtin_amdgcn_s_setprio(0); }
.LBB0_607:
	s_cmp_lt_u32 s71, 62
	s_cselect_b64 s[14:15], -1, 0
	s_cmp_gt_u32 s71, 61
	s_cselect_b64 s[4:5], -1, 0
	s_and_b64 vcc, exec, s[4:5]
	s_cbranch_vccnz .Lattn0_s2only
	v_lshl_add_u32 v243, s72, 14, v193
	v_add_u32_e32 v238, v243, v198
	ds_read_b128 v[234:237], v238 offset:24576
	ds_read_b128 v[238:241], v238 offset:32768
	v_exp_f32_e32 v34, v112
	v_exp_f32_e32 v35, v113
	v_exp_f32_e32 v36, v114
	v_exp_f32_e32 v37, v115
	v_exp_f32_e32 v38, v116
	v_add_f32_e32 v33, 0, v34
	v_exp_f32_e32 v39, v117
	s_setprio 1
	s_waitcnt lgkmcnt(1)
	v_mfma_f32_32x32x16_bf16 v[80:95], v[234:237], v[128:131], v[48:63]
	v_add_f32_e32 v33, v35, v33
	v_exp_f32_e32 v40, v118
	v_add_f32_e32 v33, v36, v33
	v_exp_f32_e32 v41, v119
	v_add_f32_e32 v33, v37, v33
	s_waitcnt lgkmcnt(0)
	v_mfma_f32_32x32x16_bf16 v[64:79], v[238:241], v[128:131], v[48:63]
	s_setprio 0
	v_exp_f32_e32 v42, v120
	v_add_f32_e32 v33, v38, v33
	v_exp_f32_e32 v43, v121
	v_add_f32_e32 v33, v39, v33
	v_add_u32_e32 v238, v243, v199
	ds_read_b128 v[234:237], v238 offset:24576
	ds_read_b128 v[238:241], v238 offset:32768
	v_exp_f32_e32 v44, v122
	v_add_f32_e32 v33, v40, v33
	v_exp_f32_e32 v45, v123
	v_add_f32_e32 v33, v41, v33
	v_exp_f32_e32 v47, v124
	v_add_f32_e32 v33, v42, v33
	v_exp_f32_e32 v112, v125
	s_setprio 1
	s_waitcnt lgkmcnt(1)
	v_mfma_f32_32x32x16_bf16 v[80:95], v[234:237], v[132:135], v[80:95]
	v_add_f32_e32 v33, v43, v33
	v_exp_f32_e32 v113, v126
	v_add_f32_e32 v33, v44, v33
	v_exp_f32_e32 v114, v127
	v_add_f32_e32 v33, v45, v33
	s_waitcnt lgkmcnt(0)
	v_mfma_f32_32x32x16_bf16 v[64:79], v[238:241], v[132:135], v[64:79]
	s_setprio 0
	v_exp_f32_e32 v96, v96
	v_add_f32_e32 v33, v47, v33
	v_exp_f32_e32 v97, v97
	v_add_f32_e32 v33, v112, v33
	v_add_u32_e32 v238, v243, v200
	ds_read_b128 v[234:237], v238 offset:24576
	ds_read_b128 v[238:241], v238 offset:32768
	v_exp_f32_e32 v98, v98
	v_add_f32_e32 v33, v113, v33
	v_exp_f32_e32 v99, v99
	v_add_f32_e32 v33, v114, v33
	v_exp_f32_e32 v100, v100
	v_add_f32_e32 v33, v96, v33
	v_exp_f32_e32 v101, v101
	s_setprio 1
	s_waitcnt lgkmcnt(1)
	v_mfma_f32_32x32x16_bf16 v[80:95], v[234:237], v[136:139], v[80:95]
	v_add_f32_e32 v33, v97, v33
	v_exp_f32_e32 v102, v102
	v_add_f32_e32 v33, v98, v33
	v_exp_f32_e32 v103, v103
	v_add_f32_e32 v33, v99, v33
	s_waitcnt lgkmcnt(0)
	v_mfma_f32_32x32x16_bf16 v[64:79], v[238:241], v[136:139], v[64:79]
	s_setprio 0
	v_exp_f32_e32 v104, v104
	v_add_f32_e32 v33, v100, v33
	v_exp_f32_e32 v105, v105
	v_add_f32_e32 v33, v101, v33
	v_add_u32_e32 v238, v243, v201
	ds_read_b128 v[234:237], v238 offset:24576
	ds_read_b128 v[238:241], v238 offset:32768
	v_exp_f32_e32 v106, v106
	v_add_f32_e32 v33, v102, v33
	v_exp_f32_e32 v107, v107
	v_add_f32_e32 v33, v103, v33
	v_exp_f32_e32 v108, v108
	v_add_f32_e32 v33, v104, v33
	v_exp_f32_e32 v109, v109
	s_setprio 1
	s_waitcnt lgkmcnt(1)
	v_mfma_f32_32x32x16_bf16 v[80:95], v[234:237], v[140:143], v[80:95]
	v_add_f32_e32 v33, v105, v33
	v_exp_f32_e32 v110, v110
	v_add_f32_e32 v33, v106, v33
	v_exp_f32_e32 v111, v111
	v_add_f32_e32 v33, v107, v33
	s_waitcnt lgkmcnt(0)
	v_mfma_f32_32x32x16_bf16 v[64:79], v[238:241], v[140:143], v[64:79]
	s_setprio 0
	v_add_f32_e32 v33, v108, v33
	v_add_f32_e32 v33, v109, v33
	v_add_f32_e32 v33, v110, v33
	v_add_f32_e32 v33, v111, v33
	v_add_u32_e32 v238, v243, v202
	ds_read_b128 v[234:237], v238 offset:24576
	ds_read_b128 v[238:241], v238 offset:32768
	v_mov_b32_e32 v46, v33
	v_cvt_pk_bf16_f32 v34, v34, v35
	v_cvt_pk_bf16_f32 v35, v36, v37
	v_cvt_pk_bf16_f32 v36, v38, v39
	v_cvt_pk_bf16_f32 v37, v40, v41
	v_cvt_pk_bf16_f32 v38, v42, v43
	v_cvt_pk_bf16_f32 v39, v44, v45
	s_setprio 1
	s_waitcnt lgkmcnt(1)
	v_mfma_f32_32x32x16_bf16 v[80:95], v[234:237], v[148:151], v[80:95]
	v_cvt_pk_bf16_f32 v40, v47, v112
	v_cvt_pk_bf16_f32 v41, v113, v114
	v_cvt_pk_bf16_f32 v42, v96, v97
	v_cvt_pk_bf16_f32 v43, v98, v99
	v_cvt_pk_bf16_f32 v44, v100, v101
	s_waitcnt lgkmcnt(0)
	v_mfma_f32_32x32x16_bf16 v[64:79], v[238:241], v[148:151], v[64:79]
	s_setprio 0
	v_cvt_pk_bf16_f32 v45, v102, v103
	v_cvt_pk_bf16_f32 v96, v104, v105
	v_cvt_pk_bf16_f32 v97, v106, v107
	v_cvt_pk_bf16_f32 v98, v108, v109
	v_add_u32_e32 v238, v243, v203
	ds_read_b128 v[234:237], v238 offset:24576
	ds_read_b128 v[238:241], v238 offset:32768
	v_cvt_pk_bf16_f32 v99, v110, v111
	s_nop 1
	v_permlane32_swap_b32_e32 v33, v46
	v_permlane32_swap_b32_e32 v34, v36
	v_permlane32_swap_b32_e32 v35, v37
	v_permlane32_swap_b32_e32 v38, v40
	v_permlane32_swap_b32_e32 v39, v41
	s_setprio 1
	s_waitcnt lgkmcnt(1)
	v_mfma_f32_32x32x16_bf16 v[80:95], v[234:237], v[144:147], v[80:95]
	v_permlane32_swap_b32_e32 v42, v44
	v_permlane32_swap_b32_e32 v43, v45
	v_permlane32_swap_b32_e32 v96, v98
	v_permlane32_swap_b32_e32 v97, v99
	s_waitcnt lgkmcnt(0)
	v_mfma_f32_32x32x16_bf16 v[64:79], v[238:241], v[144:147], v[64:79]
	s_setprio 0
	s_branch .Lattn0_join

; #define SBAR() __builtin_amdgcn_sched_barrier(0)
; #define SLOAD(k0) do { sr_.vs0 = *reinterpret_cast<const bf16x8*>(&Vh[(long)((k0) + vr) * DVV + vc]); \
;     sr_.ks0 = *reinterpret_cast<const bf16x8*>(&Kh[(long)((k0) + sr) * KROW + sc]); sr_.ks1 = *reinterpret_cast<const bf16x8*>(&Kh[(long)((k0) + 32 + sr) * KROW + sc]); } while (0)
; template <int D0> __device__ __forceinline__ void pv_one(f32x16& od, int vb, bf16x8 pa0, bf16x8 pa1, bf16x8 pa2, bf16x8 pa3) {
;   const s16x4 l0 = tr_read<v_rd_off(D0, 0, 0)>(vb), h0 = tr_read<v_rd_off(D0, 0, 1)>(vb), l1 = tr_read<v_rd_off(D0, 1, 0)>(vb), h1 = tr_read<v_rd_off(D0, 1, 1)>(vb);
;   const s16x4 l2 = tr_read<v_rd_off(D0, 2, 0)>(vb), h2 = tr_read<v_rd_off(D0, 2, 1)>(vb), l3 = tr_read<v_rd_off(D0, 3, 0)>(vb), h3 = tr_read<v_rd_off(D0, 3, 1)>(vb);
;   asm volatile("s_waitcnt lgkmcnt(0)" ::: "memory"); SBAR();
;     ...
;   __builtin_amdgcn_s_setprio(1);
;   od = __builtin_amdgcn_mfma_f32_32x32x16_bf16(pa0, PK(l0, h0), od, 0, 0, 0);
;   od = __builtin_amdgcn_mfma_f32_32x32x16_bf16(pa1, PK(l1, h1), od, 0, 0, 0);
;   od = __builtin_amdgcn_mfma_f32_32x32x16_bf16(pa2, PK(l2, h2), od, 0, 0, 0);
;   od = __builtin_amdgcn_mfma_f32_32x32x16_bf16(pa3, PK(l3, h3), od, 0, 0, 0);
;   __builtin_amdgcn_s_setprio(0);
;     ...
; }
; __device__ __forceinline__ void pv_d0(f32x16* o, int vb, bf16x8 pa0, bf16x8 pa1, bf16x8 pa2, bf16x8 pa3) {
;   pv_one<0>(o[0], vb, pa0, pa1, pa2, pa3); pv_one<1>(o[1], vb, pa0, pa1, pa2, pa3);
; }
; __device__ __forceinline__ void attn_body(const bf16_t* __restrict__ Qb, const bf16_t* __restrict__ Kh, const bf16_t* __restrict__ Vh, unsigned char* __restrict__ Ob, int ldo, int seq, LAS char* lds, const int wv, const float kbound, const float oscale) {
;     ...
;     if (j + 4 < NT) SLOAD((j + 4) * KVBLK); SBAR();
;     pv_d0(o, vb0 + b1 * (int)SHM_V, pa0, pa1, pa2, pa3); if (j + 2 < NT) partialSM(pA0, pA1);
.Lattn0_join:
	s_cmp_lt_u32 s71, 60
	s_cselect_b64 s[16:17], -1, 0
	s_cmp_gt_u32 s71, 59
	s_cbranch_scc1 .LBB0_611
	v_add_co_u32_e32 v100, vcc, 0x66008000, v180
	s_nop 1
	v_addc_co_u32_e32 v101, vcc, 0, v181, vcc
	v_add_co_u32_e32 v102, vcc, 0x62010000, v178
	s_nop 1
	v_addc_co_u32_e32 v103, vcc, 0, v179, vcc
	global_load_dwordx4 v[152:155], v[100:101], off
	global_load_dwordx4 v[156:159], v[102:103], off
	v_add_co_u32_e32 v100, vcc, 0x62012000, v178
	s_nop 1
	v_addc_co_u32_e32 v101, vcc, 0, v179, vcc
	global_load_dwordx4 v[160:163], v[100:101], off
.LBB0_611:
	s_lshl_b32 s74, s70, 13
	v_add_u32_e32 v47, s74, v188
	ds_read_b64_tr_b16 v[100:101], v47 offset:0
	ds_read_b64_tr_b16 v[102:103], v47 offset:0x400
	ds_read_b64_tr_b16 v[104:105], v47 offset:0x800
	ds_read_b64_tr_b16 v[106:107], v47 offset:0xc00
	ds_read_b64_tr_b16 v[108:109], v47 offset:0x1000
	ds_read_b64_tr_b16 v[110:111], v47 offset:0x1400
	ds_read_b64_tr_b16 v[112:113], v47 offset:0x1800
	ds_read_b64_tr_b16 v[114:115], v47 offset:0x1c00
	s_waitcnt lgkmcnt(0)
	s_setprio 1
	v_mfma_f32_32x32x16_bf16 v[0:15], v[34:37], v[100:103], v[0:15]
	v_exp_f32_e32 v80, v80
	v_exp_f32_e32 v81, v81
	v_mfma_f32_32x32x16_bf16 v[0:15], v[38:41], v[104:107], v[0:15]
	v_exp_f32_e32 v82, v82
	v_exp_f32_e32 v83, v83
	v_mfma_f32_32x32x16_bf16 v[0:15], v[42:45], v[108:111], v[0:15]
	v_exp_f32_e32 v84, v84
	v_exp_f32_e32 v85, v85
	v_mfma_f32_32x32x16_bf16 v[0:15], v[96:99], v[112:115], v[0:15]
	v_exp_f32_e32 v86, v86
	v_exp_f32_e32 v87, v87
	s_setprio 0
	ds_read_b64_tr_b16 v[100:101], v47 offset:0x200
	ds_read_b64_tr_b16 v[102:103], v47 offset:0x600
	ds_read_b64_tr_b16 v[104:105], v47 offset:0xa00
	ds_read_b64_tr_b16 v[106:107], v47 offset:0xe00
	ds_read_b64_tr_b16 v[108:109], v47 offset:0x1200
	ds_read_b64_tr_b16 v[110:111], v47 offset:0x1600
	ds_read_b64_tr_b16 v[112:113], v47 offset:0x1a00
	ds_read_b64_tr_b16 v[114:115], v47 offset:0x1e00
	s_waitcnt lgkmcnt(0)
	s_setprio 1
	v_mfma_f32_32x32x16_bf16 v[16:31], v[34:37], v[100:103], v[16:31]
	v_exp_f32_e32 v88, v88
	v_exp_f32_e32 v89, v89
	v_mfma_f32_32x32x16_bf16 v[16:31], v[38:41], v[104:107], v[16:31]
	v_exp_f32_e32 v90, v90
	v_exp_f32_e32 v91, v91
	v_mfma_f32_32x32x16_bf16 v[16:31], v[42:45], v[108:111], v[16:31]
	v_exp_f32_e32 v92, v92
	v_exp_f32_e32 v93, v93
	v_mfma_f32_32x32x16_bf16 v[16:31], v[96:99], v[112:115], v[16:31]
	v_exp_f32_e32 v94, v94
	v_exp_f32_e32 v95, v95
	s_setprio 0

; #define LAS __attribute__((address_space(3)))
; __device__ __forceinline__ bf16_t f2bf(float f) { unsigned u = __builtin_bit_cast(unsigned, f); return (bf16_t)((u + 0x7fffu + ((u >> 16) & 1u)) >> 16); }
; __device__ __forceinline__ int crow(int r, int hi) { return (r & 3) + 8 * (r >> 2) + 4 * hi; }
; __device__ __forceinline__ int crow(int r, int hi) { return (r & 3) + 8 * (r >> 2) + 4 * hi; }
; template <int DK, int DV, bool MLSTM>
; __device__ __forceinline__ void out_unit2(LAS unsigned char* lds, LAS unsigned char* ldstab, const OutArgs a, const int wv) {
;     ...
;     for (int r = 0; r < 16; ++r) {
;         const int row = 32 * rb + crow(r, hi);
;         const float t1 = s1[r] + exch[((1 - dh) * 128 + row) * 2], t2 = s2[r] + exch[((1 - dh) * 128 + row) * 2 + 1];
;         float mean, inv;
;         if (MLSTM) { mean = 0.f; inv = rsqrtf(t2 * (1.f / DV) + EPS); }
;         else { mean = t1 * (1.f / DV); inv = rsqrtf(fmaxf(t2 * (1.f / DV) - mean * mean, 0.f) + EPS); }
; #pragma unroll
;         for (int nb = 0; nb < NB; ++nb) { const int col = dh * (DV / 2) + 32 * nb + r32;
;             *(LAS bf16_t*)(lds + row * TP + col * 2) = f2bf((o[nb][r] - mean) * inv); }
.LBB0_1838:
	s_or_b64 exec, exec, s[4:5]
	v_lshlrev_b32_e32 v164, 1, v219
	v_subrev_u32_e32 v164, s6, v164
	s_add_i32 s4, 0, 0x22100
	v_lshl_add_u32 v164, v164, 2, s4
	s_waitcnt vmcnt(0) lgkmcnt(0)
	s_barrier
	ds_read_b128 v[164:167], v164 offset:1024
	v_lshlrev_b32_e32 v168, 1, v217
	v_subrev_u32_e32 v168, s6, v168
	v_lshl_add_u32 v168, v168, 2, s4
	ds_read2_b64 v[168:171], v168 offset0:128 offset1:129
	s_waitcnt lgkmcnt(1)
	v_pk_add_f32 v[156:157], v[156:157], v[164:165]
	s_nop 0
	v_pk_mul_f32 v[156:157], v[156:157], s[36:37] op_sel_hi:[1,0]
	s_nop 0
	v_fma_f32 v157, -v156, v156, v157
	v_max_f32_e32 v157, 0, v157
	v_add_f32_e32 v157, 0x358637bd, v157
	v_mul_f32_e32 v164, 0x4b800000, v157
	v_cmp_gt_f32_e32 vcc, s89, v157
	v_sub_f32_e32 v16, v16, v156
	v_sub_f32_e32 v0, v0, v156
	v_cndmask_b32_e32 v157, v157, v164, vcc
	v_rsq_f32_e32 v157, v157
	v_or_b32_e32 v164, s6, v233
	v_mul_f32_e32 v165, 0x45800000, v157
	v_cndmask_b32_e32 v157, v157, v165, vcc
	v_mul_f32_e32 v16, v16, v157
	v_bfe_u32 v172, v16, 16, 1
	v_lshlrev_b32_e32 v165, 10, v219
	v_add3_u32 v172, v16, v172, s90
	v_lshlrev_b32_e32 v16, 1, v164
	v_mul_f32_e32 v0, v0, v157
	v_add3_u32 v164, 0, v165, v16
	v_bfe_u32 v165, v0, 16, 1
	v_add3_u32 v0, v0, v165, s90
	ds_write_b16_d16_hi v164, v0 offset:64
	v_sub_f32_e32 v0, v32, v156
	v_mul_f32_e32 v0, v0, v157
	v_bfe_u32 v32, v0, 16, 1
	v_add3_u32 v0, v0, v32, s90
	ds_write_b16_d16_hi v164, v0 offset:128
	v_sub_f32_e32 v0, v48, v156
	v_mul_f32_e32 v0, v0, v157
	v_bfe_u32 v32, v0, 16, 1
	v_add3_u32 v0, v0, v32, s90
	ds_write_b16_d16_hi v164, v0 offset:192
	v_sub_f32_e32 v0, v96, v156
	v_mul_f32_e32 v0, v0, v157
	v_bfe_u32 v32, v0, 16, 1
	v_add3_u32 v0, v0, v32, s90
	ds_write_b16_d16_hi v164, v0 offset:256
	v_sub_f32_e32 v0, v112, v156
	v_mul_f32_e32 v0, v0, v157
	v_bfe_u32 v32, v0, 16, 1
	v_add3_u32 v0, v0, v32, s90
	ds_write_b16_d16_hi v164, v0 offset:320
	v_sub_f32_e32 v0, v80, v156
	v_mul_f32_e32 v0, v0, v157
	v_bfe_u32 v32, v0, 16, 1
	v_add3_u32 v0, v0, v32, s90
	ds_write_b16_d16_hi v164, v0 offset:384
	v_sub_f32_e32 v0, v64, v156
	v_mul_f32_e32 v0, v0, v157
	v_pk_add_f32 v[156:157], v[158:159], v[166:167]
	ds_write_b16_d16_hi v164, v172
	v_pk_mul_f32 v[156:157], v[156:157], s[36:37] op_sel_hi:[1,0]
	s_nop 0
	v_fma_f32 v32, -v156, v156, v157
	v_max_f32_e32 v32, 0, v32
	v_add_f32_e32 v32, 0x358637bd, v32
	v_mul_f32_e32 v48, 0x4b800000, v32
	v_cmp_gt_f32_e32 vcc, s89, v32
	v_sub_f32_e32 v17, v17, v156
	v_sub_f32_e32 v1, v1, v156
	v_cndmask_b32_e32 v32, v32, v48, vcc
	v_rsq_f32_e32 v32, v32
	v_bfe_u32 v48, v0, 16, 1
	v_add3_u32 v0, v0, v48, s90
	ds_write_b16_d16_hi v164, v0 offset:448
	v_mul_f32_e32 v0, 0x45800000, v32
	v_cndmask_b32_e32 v0, v32, v0, vcc
	v_mul_f32_e32 v17, v17, v0
	v_lshlrev_b32_e32 v32, 10, v218
	v_bfe_u32 v48, v17, 16, 1
	v_add3_u32 v17, v17, v48, s90
	v_add3_u32 v32, 0, v32, v16
	v_mul_f32_e32 v1, v1, v0
	ds_write_b16_d16_hi v32, v17
	v_bfe_u32 v17, v1, 16, 1
	v_add3_u32 v1, v1, v17, s90
	ds_write_b16_d16_hi v32, v1 offset:64
	v_sub_f32_e32 v1, v33, v156
	v_mul_f32_e32 v1, v1, v0
	v_bfe_u32 v17, v1, 16, 1
	v_add3_u32 v1, v1, v17, s90
	ds_write_b16_d16_hi v32, v1 offset:128
	v_sub_f32_e32 v1, v49, v156
	v_mul_f32_e32 v1, v1, v0
	v_bfe_u32 v17, v1, 16, 1
	v_add3_u32 v1, v1, v17, s90
	ds_write_b16_d16_hi v32, v1 offset:192
	v_sub_f32_e32 v1, v97, v156
	v_mul_f32_e32 v1, v1, v0
	v_bfe_u32 v17, v1, 16, 1
	v_add3_u32 v1, v1, v17, s90
	ds_write_b16_d16_hi v32, v1 offset:256
	v_sub_f32_e32 v1, v113, v156
	v_mul_f32_e32 v1, v1, v0
	v_bfe_u32 v17, v1, 16, 1
	v_add3_u32 v1, v1, v17, s90
	ds_write_b16_d16_hi v32, v1 offset:320
	v_sub_f32_e32 v1, v81, v156
	v_mul_f32_e32 v1, v1, v0
	v_bfe_u32 v17, v1, 16, 1
	v_add3_u32 v1, v1, v17, s90
	ds_write_b16_d16_hi v32, v1 offset:384
	v_sub_f32_e32 v1, v65, v156
	v_mul_f32_e32 v17, v1, v0
	s_waitcnt lgkmcnt(14)
	v_pk_add_f32 v[0:1], v[152:153], v[168:169]
	s_nop 0
	v_pk_mul_f32 v[0:1], v[0:1], s[36:37] op_sel_hi:[1,0]
	s_nop 0
	v_fma_f32 v1, -v0, v0, v1
	v_max_f32_e32 v1, 0, v1
	v_add_f32_e32 v1, 0x358637bd, v1
	v_mul_f32_e32 v33, 0x4b800000, v1
	v_cmp_gt_f32_e32 vcc, s89, v1
	v_sub_f32_e32 v18, v18, v0
	v_sub_f32_e32 v2, v2, v0
	v_cndmask_b32_e32 v1, v1, v33, vcc
	v_rsq_f32_e32 v1, v1
	v_bfe_u32 v33, v17, 16, 1
	v_add3_u32 v17, v17, v33, s90
	ds_write_b16_d16_hi v32, v17 offset:448
	v_mul_f32_e32 v17, 0x45800000, v1
	v_cndmask_b32_e32 v1, v1, v17, vcc
	v_mul_f32_e32 v18, v18, v1
	v_lshlrev_b32_e32 v17, 10, v217
	v_bfe_u32 v32, v18, 16, 1
	v_add3_u32 v18, v18, v32, s90
	v_add3_u32 v17, 0, v17, v16
	v_mul_f32_e32 v2, v2, v1
	ds_write_b16_d16_hi v17, v18
	v_bfe_u32 v18, v2, 16, 1
	v_add3_u32 v2, v2, v18, s90
	ds_write_b16_d16_hi v17, v2 offset:64
	v_sub_f32_e32 v2, v34, v0
	v_mul_f32_e32 v2, v2, v1
	v_bfe_u32 v18, v2, 16, 1
	v_add3_u32 v2, v2, v18, s90
	ds_write_b16_d16_hi v17, v2 offset:128
	v_sub_f32_e32 v2, v50, v0
	v_mul_f32_e32 v2, v2, v1
	v_bfe_u32 v18, v2, 16, 1
	v_add3_u32 v2, v2, v18, s90
	ds_write_b16_d16_hi v17, v2 offset:192
	v_sub_f32_e32 v2, v98, v0
	v_mul_f32_e32 v2, v2, v1
	v_bfe_u32 v18, v2, 16, 1
	v_add3_u32 v2, v2, v18, s90
	ds_write_b16_d16_hi v17, v2 offset:256
	v_sub_f32_e32 v2, v114, v0
	v_mul_f32_e32 v2, v2, v1
	v_bfe_u32 v18, v2, 16, 1
	v_add3_u32 v2, v2, v18, s90
	ds_write_b16_d16_hi v17, v2 offset:320
	v_sub_f32_e32 v2, v82, v0
	v_mul_f32_e32 v2, v2, v1
	v_bfe_u32 v18, v2, 16, 1
	v_add3_u32 v2, v2, v18, s90
	v_sub_f32_e32 v0, v66, v0
	ds_write_b16_d16_hi v17, v2 offset:384
	v_mul_f32_e32 v2, v0, v1
	v_pk_add_f32 v[0:1], v[154:155], v[170:171]
	s_nop 0
	v_pk_mul_f32 v[0:1], v[0:1], s[36:37] op_sel_hi:[1,0]
	s_nop 0
	v_fma_f32 v1, -v0, v0, v1
	v_max_f32_e32 v1, 0, v1
; #define LAS __attribute__((address_space(3)))
; __device__ __forceinline__ bf16_t f2bf(float f) { unsigned u = __builtin_bit_cast(unsigned, f); return (bf16_t)((u + 0x7fffu + ((u >> 16) & 1u)) >> 16); }
; __device__ __forceinline__ int crow(int r, int hi) { return (r & 3) + 8 * (r >> 2) + 4 * hi; }
; __device__ __forceinline__ int crow(int r, int hi) { return (r & 3) + 8 * (r >> 2) + 4 * hi; }
; template <int DK, int DV, bool MLSTM>
; __device__ __forceinline__ void out_unit2(LAS unsigned char* lds, LAS unsigned char* ldstab, const OutArgs a, const int wv) {
;     ...
;     for (int r = 0; r < 16; ++r) {
;         const int row = 32 * rb + crow(r, hi);
;         const float t1 = s1[r] + exch[((1 - dh) * 128 + row) * 2], t2 = s2[r] + exch[((1 - dh) * 128 + row) * 2 + 1];
;         float mean, inv;
;         if (MLSTM) { mean = 0.f; inv = rsqrtf(t2 * (1.f / DV) + EPS); }
;         else { mean = t1 * (1.f / DV); inv = rsqrtf(fmaxf(t2 * (1.f / DV) - mean * mean, 0.f) + EPS); }
; #pragma unroll
;         for (int nb = 0; nb < NB; ++nb) { const int col = dh * (DV / 2) + 32 * nb + r32;
;             *(LAS bf16_t*)(lds + row * TP + col * 2) = f2bf((o[nb][r] - mean) * inv); }
	v_add_f32_e32 v1, 0x358637bd, v1
	v_mul_f32_e32 v18, 0x4b800000, v1
	v_cmp_gt_f32_e32 vcc, s89, v1
	s_nop 1
	v_cndmask_b32_e32 v1, v1, v18, vcc
	v_rsq_f32_e32 v1, v1
	v_bfe_u32 v18, v2, 16, 1
	v_add3_u32 v2, v2, v18, s90
	ds_write_b16_d16_hi v17, v2 offset:448
	v_mul_f32_e32 v2, 0x45800000, v1
	v_cndmask_b32_e32 v1, v1, v2, vcc
	v_sub_f32_e32 v17, v19, v0
	v_mul_f32_e32 v17, v17, v1
	v_lshlrev_b32_e32 v2, 10, v216
	v_bfe_u32 v18, v17, 16, 1
	v_add3_u32 v17, v17, v18, s90
	v_add3_u32 v18, 0, v2, v16
	v_sub_f32_e32 v2, v3, v0
	v_mul_f32_e32 v2, v2, v1
	v_bfe_u32 v3, v2, 16, 1
	v_add3_u32 v2, v2, v3, s90
	ds_write_b16_d16_hi v18, v2 offset:64
	v_sub_f32_e32 v2, v35, v0
	v_mul_f32_e32 v2, v2, v1
	v_bfe_u32 v3, v2, 16, 1
	v_add3_u32 v2, v2, v3, s90
	ds_write_b16_d16_hi v18, v2 offset:128
	v_sub_f32_e32 v2, v51, v0
	v_mul_f32_e32 v2, v2, v1
	v_bfe_u32 v3, v2, 16, 1
	v_add3_u32 v2, v2, v3, s90
	ds_write_b16_d16_hi v18, v2 offset:192
	v_sub_f32_e32 v2, v99, v0
	v_mul_f32_e32 v2, v2, v1
	v_bfe_u32 v3, v2, 16, 1
	v_add3_u32 v2, v2, v3, s90
	ds_write_b16_d16_hi v18, v2 offset:256
	v_sub_f32_e32 v2, v115, v0
	v_mul_f32_e32 v2, v2, v1
	v_bfe_u32 v3, v2, 16, 1
	v_add3_u32 v2, v2, v3, s90
	ds_write_b16_d16_hi v18, v2 offset:320
	v_sub_f32_e32 v2, v83, v0
	v_sub_f32_e32 v0, v67, v0
	ds_write_b16_d16_hi v18, v17
	v_mul_f32_e32 v2, v2, v1
	v_mul_f32_e32 v17, v0, v1
	v_lshlrev_b32_e32 v0, 1, v215
	v_bfe_u32 v3, v2, 16, 1
	v_subrev_u32_e32 v0, s6, v0
	v_add3_u32 v2, v2, v3, s90
	v_lshl_add_u32 v0, v0, 2, s4
	ds_write_b16_d16_hi v18, v2 offset:384
	ds_read2_b64 v[0:3], v0 offset0:128 offset1:129
	v_lshlrev_b32_e32 v19, 1, v213
	v_subrev_u32_e32 v19, s6, v19
	v_lshl_add_u32 v19, v19, 2, s4
	ds_read2_b64 v[32:35], v19 offset0:128 offset1:129
	s_waitcnt lgkmcnt(1)
	v_pk_add_f32 v[0:1], v[148:149], v[0:1]
	s_nop 0
	v_pk_mul_f32 v[0:1], v[0:1], s[36:37] op_sel_hi:[1,0]
	s_nop 0
	v_fma_f32 v1, -v0, v0, v1
	v_max_f32_e32 v1, 0, v1
	v_add_f32_e32 v1, 0x358637bd, v1
	v_mul_f32_e32 v19, 0x4b800000, v1
	v_cmp_gt_f32_e32 vcc, s89, v1
	v_sub_f32_e32 v4, v4, v0
	s_nop 0
	v_cndmask_b32_e32 v1, v1, v19, vcc
	v_rsq_f32_e32 v1, v1
	v_bfe_u32 v19, v17, 16, 1
	v_add3_u32 v17, v17, v19, s90
	ds_write_b16_d16_hi v18, v17 offset:448
	v_mul_f32_e32 v17, 0x45800000, v1
	v_cndmask_b32_e32 v1, v1, v17, vcc
	v_sub_f32_e32 v18, v20, v0
	v_mul_f32_e32 v18, v18, v1
	v_lshlrev_b32_e32 v17, 10, v215
	v_bfe_u32 v19, v18, 16, 1
	v_add3_u32 v18, v18, v19, s90
	v_add3_u32 v17, 0, v17, v16
	v_mul_f32_e32 v4, v4, v1
	ds_write_b16_d16_hi v17, v18
	v_bfe_u32 v18, v4, 16, 1
	v_add3_u32 v4, v4, v18, s90
	ds_write_b16_d16_hi v17, v4 offset:64
	v_sub_f32_e32 v4, v36, v0
	v_mul_f32_e32 v4, v4, v1
	v_bfe_u32 v18, v4, 16, 1
	v_add3_u32 v4, v4, v18, s90
	ds_write_b16_d16_hi v17, v4 offset:128
	v_sub_f32_e32 v4, v52, v0
	v_mul_f32_e32 v4, v4, v1
	v_bfe_u32 v18, v4, 16, 1
	v_add3_u32 v4, v4, v18, s90
	ds_write_b16_d16_hi v17, v4 offset:192
	v_sub_f32_e32 v4, v100, v0
	v_mul_f32_e32 v4, v4, v1
	v_bfe_u32 v18, v4, 16, 1
	v_add3_u32 v4, v4, v18, s90
	ds_write_b16_d16_hi v17, v4 offset:256
	v_sub_f32_e32 v4, v116, v0
	v_mul_f32_e32 v4, v4, v1
	v_bfe_u32 v18, v4, 16, 1
	v_add3_u32 v4, v4, v18, s90
	ds_write_b16_d16_hi v17, v4 offset:320
	v_sub_f32_e32 v4, v84, v0
	v_mul_f32_e32 v4, v4, v1
	v_bfe_u32 v18, v4, 16, 1
	v_add3_u32 v4, v4, v18, s90
	v_sub_f32_e32 v0, v68, v0
	ds_write_b16_d16_hi v17, v4 offset:384
	v_mul_f32_e32 v4, v0, v1
	v_pk_add_f32 v[0:1], v[150:151], v[2:3]
	s_nop 0
	v_pk_mul_f32 v[0:1], v[0:1], s[36:37] op_sel_hi:[1,0]
	s_nop 0
	v_fma_f32 v1, -v0, v0, v1
	v_max_f32_e32 v1, 0, v1
	v_add_f32_e32 v1, 0x358637bd, v1
	v_mul_f32_e32 v2, 0x4b800000, v1
	v_cmp_gt_f32_e32 vcc, s89, v1
	v_sub_f32_e32 v3, v21, v0
	s_nop 0
	v_cndmask_b32_e32 v1, v1, v2, vcc
	v_rsq_f32_e32 v1, v1
	v_bfe_u32 v2, v4, 16, 1
	v_add3_u32 v2, v4, v2, s90
	ds_write_b16_d16_hi v17, v2 offset:448
	v_mul_f32_e32 v2, 0x45800000, v1
	v_cndmask_b32_e32 v1, v1, v2, vcc
	v_mul_f32_e32 v3, v3, v1
	v_lshlrev_b32_e32 v2, 10, v214
	v_bfe_u32 v4, v3, 16, 1
	v_add3_u32 v3, v3, v4, s90
	v_add3_u32 v2, 0, v2, v16
	ds_write_b16_d16_hi v2, v3
	v_sub_f32_e32 v3, v5, v0
	v_mul_f32_e32 v3, v3, v1
	v_bfe_u32 v4, v3, 16, 1
	v_add3_u32 v3, v3, v4, s90
	ds_write_b16_d16_hi v2, v3 offset:64
	v_sub_f32_e32 v3, v37, v0
	v_mul_f32_e32 v3, v3, v1
	v_bfe_u32 v4, v3, 16, 1
	v_add3_u32 v3, v3, v4, s90
	ds_write_b16_d16_hi v2, v3 offset:128
	v_sub_f32_e32 v3, v53, v0
	v_mul_f32_e32 v3, v3, v1
	v_bfe_u32 v4, v3, 16, 1
	v_add3_u32 v3, v3, v4, s90
	ds_write_b16_d16_hi v2, v3 offset:192
	v_sub_f32_e32 v3, v101, v0
	v_mul_f32_e32 v3, v3, v1
	v_bfe_u32 v4, v3, 16, 1
	v_add3_u32 v3, v3, v4, s90
	ds_write_b16_d16_hi v2, v3 offset:256
	v_sub_f32_e32 v3, v117, v0
	v_mul_f32_e32 v3, v3, v1
	v_bfe_u32 v4, v3, 16, 1
	v_add3_u32 v3, v3, v4, s90
	ds_write_b16_d16_hi v2, v3 offset:320
	v_sub_f32_e32 v3, v85, v0
	v_mul_f32_e32 v3, v3, v1
	v_bfe_u32 v4, v3, 16, 1
	v_add3_u32 v3, v3, v4, s90
	v_sub_f32_e32 v0, v69, v0
	ds_write_b16_d16_hi v2, v3 offset:384
	v_mul_f32_e32 v3, v0, v1
	s_waitcnt lgkmcnt(14)
; #define LAS __attribute__((address_space(3)))
; __device__ __forceinline__ bf16_t f2bf(float f) { unsigned u = __builtin_bit_cast(unsigned, f); return (bf16_t)((u + 0x7fffu + ((u >> 16) & 1u)) >> 16); }
; __device__ __forceinline__ int crow(int r, int hi) { return (r & 3) + 8 * (r >> 2) + 4 * hi; }
; __device__ __forceinline__ int crow(int r, int hi) { return (r & 3) + 8 * (r >> 2) + 4 * hi; }
; template <int DK, int DV, bool MLSTM>
; __device__ __forceinline__ void out_unit2(LAS unsigned char* lds, LAS unsigned char* ldstab, const OutArgs a, const int wv) {
;     ...
;     for (int r = 0; r < 16; ++r) {
;         const int row = 32 * rb + crow(r, hi);
;         const float t1 = s1[r] + exch[((1 - dh) * 128 + row) * 2], t2 = s2[r] + exch[((1 - dh) * 128 + row) * 2 + 1];
;         float mean, inv;
;         if (MLSTM) { mean = 0.f; inv = rsqrtf(t2 * (1.f / DV) + EPS); }
;         else { mean = t1 * (1.f / DV); inv = rsqrtf(fmaxf(t2 * (1.f / DV) - mean * mean, 0.f) + EPS); }
; #pragma unroll
;         for (int nb = 0; nb < NB; ++nb) { const int col = dh * (DV / 2) + 32 * nb + r32;
;             *(LAS bf16_t*)(lds + row * TP + col * 2) = f2bf((o[nb][r] - mean) * inv); }
	v_pk_add_f32 v[0:1], v[144:145], v[32:33]
	s_nop 0
	v_pk_mul_f32 v[0:1], v[0:1], s[36:37] op_sel_hi:[1,0]
	s_nop 0
	v_fma_f32 v1, -v0, v0, v1
	v_max_f32_e32 v1, 0, v1
	v_add_f32_e32 v1, 0x358637bd, v1
	v_mul_f32_e32 v4, 0x4b800000, v1
	v_cmp_gt_f32_e32 vcc, s89, v1
	s_nop 1
	v_cndmask_b32_e32 v1, v1, v4, vcc
	v_rsq_f32_e32 v1, v1
	v_bfe_u32 v4, v3, 16, 1
	v_add3_u32 v3, v3, v4, s90
	ds_write_b16_d16_hi v2, v3 offset:448
	v_mul_f32_e32 v2, 0x45800000, v1
	v_cndmask_b32_e32 v1, v1, v2, vcc
	v_sub_f32_e32 v3, v22, v0
	v_mul_f32_e32 v3, v3, v1
	v_lshlrev_b32_e32 v2, 10, v213
	v_bfe_u32 v4, v3, 16, 1
	v_add3_u32 v3, v3, v4, s90
	v_add3_u32 v2, 0, v2, v16
	ds_write_b16_d16_hi v2, v3
	v_sub_f32_e32 v3, v6, v0
	v_mul_f32_e32 v3, v3, v1
	v_bfe_u32 v4, v3, 16, 1
	v_add3_u32 v3, v3, v4, s90
	ds_write_b16_d16_hi v2, v3 offset:64
	v_sub_f32_e32 v3, v38, v0
	v_mul_f32_e32 v3, v3, v1
	v_bfe_u32 v4, v3, 16, 1
	v_add3_u32 v3, v3, v4, s90
	ds_write_b16_d16_hi v2, v3 offset:128
	v_sub_f32_e32 v3, v54, v0
	v_mul_f32_e32 v3, v3, v1
	v_bfe_u32 v4, v3, 16, 1
	v_add3_u32 v3, v3, v4, s90
	ds_write_b16_d16_hi v2, v3 offset:192
	v_sub_f32_e32 v3, v102, v0
	v_mul_f32_e32 v3, v3, v1
	v_bfe_u32 v4, v3, 16, 1
	v_add3_u32 v3, v3, v4, s90
	ds_write_b16_d16_hi v2, v3 offset:256
	v_sub_f32_e32 v3, v118, v0
	v_mul_f32_e32 v3, v3, v1
	v_bfe_u32 v4, v3, 16, 1
	v_add3_u32 v3, v3, v4, s90
	ds_write_b16_d16_hi v2, v3 offset:320
	v_sub_f32_e32 v3, v86, v0
	v_mul_f32_e32 v3, v3, v1
	v_bfe_u32 v4, v3, 16, 1
	v_add3_u32 v3, v3, v4, s90
	v_sub_f32_e32 v0, v70, v0
	ds_write_b16_d16_hi v2, v3 offset:384
	v_mul_f32_e32 v3, v0, v1
	v_pk_add_f32 v[0:1], v[146:147], v[34:35]
	s_nop 0
	v_pk_mul_f32 v[0:1], v[0:1], s[36:37] op_sel_hi:[1,0]
	s_nop 0
	v_fma_f32 v1, -v0, v0, v1
	v_max_f32_e32 v1, 0, v1
	v_add_f32_e32 v1, 0x358637bd, v1
	v_mul_f32_e32 v4, 0x4b800000, v1
	v_cmp_gt_f32_e32 vcc, s89, v1
	s_nop 1
	v_cndmask_b32_e32 v1, v1, v4, vcc
	v_rsq_f32_e32 v1, v1
	v_bfe_u32 v4, v3, 16, 1
	v_add3_u32 v3, v3, v4, s90
	ds_write_b16_d16_hi v2, v3 offset:448
	v_mul_f32_e32 v2, 0x45800000, v1
	v_cndmask_b32_e32 v1, v1, v2, vcc
	v_sub_f32_e32 v3, v23, v0
	v_lshlrev_b32_e32 v2, 10, v212
	v_mul_f32_e32 v3, v3, v1
	v_bfe_u32 v4, v3, 16, 1
	v_add3_u32 v17, 0, v2, v16
	v_sub_f32_e32 v2, v7, v0
	v_add3_u32 v3, v3, v4, s90
	v_mul_f32_e32 v2, v2, v1
	ds_write_b16_d16_hi v17, v3
	v_bfe_u32 v3, v2, 16, 1
	v_add3_u32 v2, v2, v3, s90
	ds_write_b16_d16_hi v17, v2 offset:64
	v_sub_f32_e32 v2, v39, v0
	v_mul_f32_e32 v2, v2, v1
	v_bfe_u32 v3, v2, 16, 1
	v_add3_u32 v2, v2, v3, s90
	ds_write_b16_d16_hi v17, v2 offset:128
	v_sub_f32_e32 v2, v55, v0
	v_mul_f32_e32 v2, v2, v1
	v_bfe_u32 v3, v2, 16, 1
	v_add3_u32 v2, v2, v3, s90
	ds_write_b16_d16_hi v17, v2 offset:192
	v_sub_f32_e32 v2, v103, v0
	v_mul_f32_e32 v2, v2, v1
	v_bfe_u32 v3, v2, 16, 1
	v_add3_u32 v2, v2, v3, s90
	ds_write_b16_d16_hi v17, v2 offset:256
	v_sub_f32_e32 v2, v119, v0
	v_mul_f32_e32 v2, v2, v1
	v_bfe_u32 v3, v2, 16, 1
	v_add3_u32 v2, v2, v3, s90
	ds_write_b16_d16_hi v17, v2 offset:320
	v_sub_f32_e32 v2, v87, v0
	v_sub_f32_e32 v0, v71, v0
	v_mul_f32_e32 v2, v2, v1
	v_mul_f32_e32 v18, v0, v1
	v_lshlrev_b32_e32 v0, 1, v211
	v_bfe_u32 v3, v2, 16, 1
	v_subrev_u32_e32 v0, s6, v0
	v_add3_u32 v2, v2, v3, s90
	v_lshl_add_u32 v0, v0, 2, s4
	ds_write_b16_d16_hi v17, v2 offset:384
	ds_read2_b64 v[0:3], v0 offset0:128 offset1:129
	v_lshlrev_b32_e32 v4, 1, v209
	v_subrev_u32_e32 v4, s6, v4
	v_lshl_add_u32 v4, v4, 2, s4
	ds_read2_b64 v[4:7], v4 offset0:128 offset1:129
	s_waitcnt lgkmcnt(1)
	v_pk_add_f32 v[0:1], v[140:141], v[0:1]
	s_nop 0
	v_pk_mul_f32 v[0:1], v[0:1], s[36:37] op_sel_hi:[1,0]
	s_nop 0
	v_fma_f32 v1, -v0, v0, v1
	v_max_f32_e32 v1, 0, v1
	v_add_f32_e32 v1, 0x358637bd, v1
	v_mul_f32_e32 v19, 0x4b800000, v1
	v_cmp_gt_f32_e32 vcc, s89, v1
	v_sub_f32_e32 v8, v8, v0
	s_nop 0
	v_cndmask_b32_e32 v1, v1, v19, vcc
	v_rsq_f32_e32 v1, v1
	v_bfe_u32 v19, v18, 16, 1
	v_add3_u32 v18, v18, v19, s90
	ds_write_b16_d16_hi v17, v18 offset:448
	v_mul_f32_e32 v17, 0x45800000, v1
	v_cndmask_b32_e32 v1, v1, v17, vcc
	v_sub_f32_e32 v18, v24, v0
	v_mul_f32_e32 v18, v18, v1
	v_lshlrev_b32_e32 v17, 10, v211
	v_bfe_u32 v19, v18, 16, 1
	v_add3_u32 v18, v18, v19, s90
	v_add3_u32 v17, 0, v17, v16
	v_mul_f32_e32 v8, v8, v1
	ds_write_b16_d16_hi v17, v18
	v_bfe_u32 v18, v8, 16, 1
	v_add3_u32 v8, v8, v18, s90
	ds_write_b16_d16_hi v17, v8 offset:64
	v_sub_f32_e32 v8, v40, v0
	v_mul_f32_e32 v8, v8, v1
	v_bfe_u32 v18, v8, 16, 1
	v_add3_u32 v8, v8, v18, s90
	ds_write_b16_d16_hi v17, v8 offset:128
	v_sub_f32_e32 v8, v56, v0
	v_mul_f32_e32 v8, v8, v1
	v_bfe_u32 v18, v8, 16, 1
	v_add3_u32 v8, v8, v18, s90
	ds_write_b16_d16_hi v17, v8 offset:192
	v_sub_f32_e32 v8, v104, v0
	v_mul_f32_e32 v8, v8, v1
	v_bfe_u32 v18, v8, 16, 1
	v_add3_u32 v8, v8, v18, s90
	ds_write_b16_d16_hi v17, v8 offset:256
	v_sub_f32_e32 v8, v120, v0
	v_mul_f32_e32 v8, v8, v1
	v_bfe_u32 v18, v8, 16, 1
	v_add3_u32 v8, v8, v18, s90
	ds_write_b16_d16_hi v17, v8 offset:320
	v_sub_f32_e32 v8, v88, v0
	v_mul_f32_e32 v8, v8, v1
	v_bfe_u32 v18, v8, 16, 1
	v_add3_u32 v8, v8, v18, s90
	v_sub_f32_e32 v0, v72, v0
	ds_write_b16_d16_hi v17, v8 offset:384
	v_mul_f32_e32 v8, v0, v1
	v_pk_add_f32 v[0:1], v[142:143], v[2:3]
	s_nop 0
	v_pk_mul_f32 v[0:1], v[0:1], s[36:37] op_sel_hi:[1,0]
	s_nop 0
	v_fma_f32 v1, -v0, v0, v1
	v_max_f32_e32 v1, 0, v1
	v_add_f32_e32 v1, 0x358637bd, v1
	v_mul_f32_e32 v2, 0x4b800000, v1
	v_cmp_gt_f32_e32 vcc, s89, v1
	v_sub_f32_e32 v3, v25, v0
	s_nop 0
	v_cndmask_b32_e32 v1, v1, v2, vcc
	v_rsq_f32_e32 v1, v1
	v_bfe_u32 v2, v8, 16, 1
	v_add3_u32 v2, v8, v2, s90
	ds_write_b16_d16_hi v17, v2 offset:448
	v_mul_f32_e32 v2, 0x45800000, v1
	v_cndmask_b32_e32 v1, v1, v2, vcc
	v_mul_f32_e32 v3, v3, v1
	v_lshlrev_b32_e32 v2, 10, v210
	v_bfe_u32 v8, v3, 16, 1
	v_add3_u32 v3, v3, v8, s90
	v_add3_u32 v2, 0, v2, v16
	ds_write_b16_d16_hi v2, v3
	v_sub_f32_e32 v3, v9, v0
	v_mul_f32_e32 v3, v3, v1
	v_bfe_u32 v8, v3, 16, 1
	v_add3_u32 v3, v3, v8, s90
	ds_write_b16_d16_hi v2, v3 offset:64
	v_sub_f32_e32 v3, v41, v0
	v_mul_f32_e32 v3, v3, v1
	v_bfe_u32 v8, v3, 16, 1
	v_add3_u32 v3, v3, v8, s90
	ds_write_b16_d16_hi v2, v3 offset:128
	v_sub_f32_e32 v3, v57, v0
	v_mul_f32_e32 v3, v3, v1
	v_bfe_u32 v8, v3, 16, 1
	v_add3_u32 v3, v3, v8, s90
	ds_write_b16_d16_hi v2, v3 offset:192
	v_sub_f32_e32 v3, v105, v0
	v_mul_f32_e32 v3, v3, v1
	v_bfe_u32 v8, v3, 16, 1
	v_add3_u32 v3, v3, v8, s90
	ds_write_b16_d16_hi v2, v3 offset:256
	v_sub_f32_e32 v3, v121, v0
	v_mul_f32_e32 v3, v3, v1
	v_bfe_u32 v8, v3, 16, 1
	v_add3_u32 v3, v3, v8, s90
	ds_write_b16_d16_hi v2, v3 offset:320
	v_sub_f32_e32 v3, v89, v0
	v_mul_f32_e32 v3, v3, v1
	v_bfe_u32 v8, v3, 16, 1
	v_add3_u32 v3, v3, v8, s90
	v_sub_f32_e32 v0, v73, v0
	ds_write_b16_d16_hi v2, v3 offset:384
	v_mul_f32_e32 v3, v0, v1
	s_waitcnt lgkmcnt(14)
; #define LAS __attribute__((address_space(3)))
; __device__ __forceinline__ bf16_t f2bf(float f) { unsigned u = __builtin_bit_cast(unsigned, f); return (bf16_t)((u + 0x7fffu + ((u >> 16) & 1u)) >> 16); }
; __device__ __forceinline__ int crow(int r, int hi) { return (r & 3) + 8 * (r >> 2) + 4 * hi; }
; __device__ __forceinline__ int crow(int r, int hi) { return (r & 3) + 8 * (r >> 2) + 4 * hi; }
; template <int DK, int DV, bool MLSTM>
; __device__ __forceinline__ void out_unit2(LAS unsigned char* lds, LAS unsigned char* ldstab, const OutArgs a, const int wv) {
;     ...
;     for (int r = 0; r < 16; ++r) {
;         const int row = 32 * rb + crow(r, hi);
;         const float t1 = s1[r] + exch[((1 - dh) * 128 + row) * 2], t2 = s2[r] + exch[((1 - dh) * 128 + row) * 2 + 1];
;         float mean, inv;
;         if (MLSTM) { mean = 0.f; inv = rsqrtf(t2 * (1.f / DV) + EPS); }
;         else { mean = t1 * (1.f / DV); inv = rsqrtf(fmaxf(t2 * (1.f / DV) - mean * mean, 0.f) + EPS); }
; #pragma unroll
;         for (int nb = 0; nb < NB; ++nb) { const int col = dh * (DV / 2) + 32 * nb + r32;
;             *(LAS bf16_t*)(lds + row * TP + col * 2) = f2bf((o[nb][r] - mean) * inv); }
	v_pk_add_f32 v[0:1], v[136:137], v[4:5]
	s_nop 0
	v_pk_mul_f32 v[0:1], v[0:1], s[36:37] op_sel_hi:[1,0]
	s_nop 0
	v_fma_f32 v1, -v0, v0, v1
	v_max_f32_e32 v1, 0, v1
	v_add_f32_e32 v1, 0x358637bd, v1
	v_mul_f32_e32 v4, 0x4b800000, v1
	v_cmp_gt_f32_e32 vcc, s89, v1
	s_nop 1
	v_cndmask_b32_e32 v1, v1, v4, vcc
	v_rsq_f32_e32 v1, v1
	v_bfe_u32 v4, v3, 16, 1
	v_add3_u32 v3, v3, v4, s90
	ds_write_b16_d16_hi v2, v3 offset:448
	v_mul_f32_e32 v2, 0x45800000, v1
	v_cndmask_b32_e32 v1, v1, v2, vcc
	v_sub_f32_e32 v3, v26, v0
	v_mul_f32_e32 v3, v3, v1
	v_lshlrev_b32_e32 v2, 10, v209
	v_bfe_u32 v4, v3, 16, 1
	v_add3_u32 v3, v3, v4, s90
	v_add3_u32 v2, 0, v2, v16
	ds_write_b16_d16_hi v2, v3
	v_sub_f32_e32 v3, v10, v0
	v_mul_f32_e32 v3, v3, v1
	v_bfe_u32 v4, v3, 16, 1
	v_add3_u32 v3, v3, v4, s90
	ds_write_b16_d16_hi v2, v3 offset:64
	v_sub_f32_e32 v3, v42, v0
	v_mul_f32_e32 v3, v3, v1
	v_bfe_u32 v4, v3, 16, 1
	v_add3_u32 v3, v3, v4, s90
	ds_write_b16_d16_hi v2, v3 offset:128
	v_sub_f32_e32 v3, v58, v0
	v_mul_f32_e32 v3, v3, v1
	v_bfe_u32 v4, v3, 16, 1
	v_add3_u32 v3, v3, v4, s90
	ds_write_b16_d16_hi v2, v3 offset:192
	v_sub_f32_e32 v3, v106, v0
	v_mul_f32_e32 v3, v3, v1
	v_bfe_u32 v4, v3, 16, 1
	v_add3_u32 v3, v3, v4, s90
	ds_write_b16_d16_hi v2, v3 offset:256
	v_sub_f32_e32 v3, v122, v0
	v_mul_f32_e32 v3, v3, v1
	v_bfe_u32 v4, v3, 16, 1
	v_add3_u32 v3, v3, v4, s90
	ds_write_b16_d16_hi v2, v3 offset:320
	v_sub_f32_e32 v3, v90, v0
	v_mul_f32_e32 v3, v3, v1
	v_bfe_u32 v4, v3, 16, 1
	v_add3_u32 v3, v3, v4, s90
	v_sub_f32_e32 v0, v74, v0
	ds_write_b16_d16_hi v2, v3 offset:384
	v_mul_f32_e32 v3, v0, v1
	v_pk_add_f32 v[0:1], v[138:139], v[6:7]
	s_nop 0
	v_pk_mul_f32 v[0:1], v[0:1], s[36:37] op_sel_hi:[1,0]
	s_nop 0
	v_fma_f32 v1, -v0, v0, v1
	v_max_f32_e32 v1, 0, v1
	v_add_f32_e32 v1, 0x358637bd, v1
	v_mul_f32_e32 v4, 0x4b800000, v1
	v_cmp_gt_f32_e32 vcc, s89, v1
	s_nop 1
	v_cndmask_b32_e32 v1, v1, v4, vcc
	v_rsq_f32_e32 v1, v1
	v_bfe_u32 v4, v3, 16, 1
	v_add3_u32 v3, v3, v4, s90
	ds_write_b16_d16_hi v2, v3 offset:448
	v_mul_f32_e32 v2, 0x45800000, v1
	v_cndmask_b32_e32 v1, v1, v2, vcc
	v_sub_f32_e32 v3, v27, v0
	v_lshlrev_b32_e32 v2, 10, v208
	v_mul_f32_e32 v3, v3, v1
	v_bfe_u32 v4, v3, 16, 1
	v_add3_u32 v8, 0, v2, v16
	v_sub_f32_e32 v2, v11, v0
	v_add3_u32 v3, v3, v4, s90
	v_mul_f32_e32 v2, v2, v1
	ds_write_b16_d16_hi v8, v3
	v_bfe_u32 v3, v2, 16, 1
	v_add3_u32 v2, v2, v3, s90
	ds_write_b16_d16_hi v8, v2 offset:64
	v_sub_f32_e32 v2, v43, v0
	v_mul_f32_e32 v2, v2, v1
	v_bfe_u32 v3, v2, 16, 1
	v_add3_u32 v2, v2, v3, s90
	ds_write_b16_d16_hi v8, v2 offset:128
	v_sub_f32_e32 v2, v59, v0
	v_mul_f32_e32 v2, v2, v1
	v_bfe_u32 v3, v2, 16, 1
	v_add3_u32 v2, v2, v3, s90
	ds_write_b16_d16_hi v8, v2 offset:192
	v_sub_f32_e32 v2, v107, v0
	v_mul_f32_e32 v2, v2, v1
	v_bfe_u32 v3, v2, 16, 1
	v_add3_u32 v2, v2, v3, s90
	ds_write_b16_d16_hi v8, v2 offset:256
	v_sub_f32_e32 v2, v123, v0
	v_mul_f32_e32 v2, v2, v1
	v_bfe_u32 v3, v2, 16, 1
	v_add3_u32 v2, v2, v3, s90
	ds_write_b16_d16_hi v8, v2 offset:320
	v_sub_f32_e32 v2, v91, v0
	v_sub_f32_e32 v0, v75, v0
	v_mul_f32_e32 v2, v2, v1
	v_mul_f32_e32 v9, v0, v1
	v_lshlrev_b32_e32 v0, 1, v207
	v_bfe_u32 v3, v2, 16, 1
	v_subrev_u32_e32 v0, s6, v0
	v_add3_u32 v2, v2, v3, s90
	v_lshl_add_u32 v0, v0, 2, s4
	ds_write_b16_d16_hi v8, v2 offset:384
	ds_read2_b64 v[0:3], v0 offset0:128 offset1:129
	v_lshlrev_b32_e32 v4, 1, v162
	v_subrev_u32_e32 v4, s6, v4
	v_lshl_add_u32 v4, v4, 2, s4
	ds_read2_b64 v[4:7], v4 offset0:128 offset1:129
	s_waitcnt lgkmcnt(1)
	v_pk_add_f32 v[0:1], v[132:133], v[0:1]
	s_nop 0
	v_pk_mul_f32 v[0:1], v[0:1], s[36:37] op_sel_hi:[1,0]
	s_nop 0
	v_fma_f32 v1, -v0, v0, v1
	v_max_f32_e32 v1, 0, v1
	v_add_f32_e32 v1, 0x358637bd, v1
	v_mul_f32_e32 v10, 0x4b800000, v1
	v_cmp_gt_f32_e32 vcc, s89, v1
	s_nop 1
	v_cndmask_b32_e32 v1, v1, v10, vcc
	v_rsq_f32_e32 v1, v1
	v_bfe_u32 v10, v9, 16, 1
	v_add3_u32 v9, v9, v10, s90
	ds_write_b16_d16_hi v8, v9 offset:448
	v_mul_f32_e32 v8, 0x45800000, v1
	v_cndmask_b32_e32 v1, v1, v8, vcc
	v_sub_f32_e32 v9, v28, v0
	v_mul_f32_e32 v9, v9, v1
	v_lshlrev_b32_e32 v8, 10, v207
	v_bfe_u32 v10, v9, 16, 1
	v_add3_u32 v9, v9, v10, s90
	v_add3_u32 v8, 0, v8, v16
	ds_write_b16_d16_hi v8, v9
	v_sub_f32_e32 v9, v12, v0
	v_mul_f32_e32 v9, v9, v1
	v_bfe_u32 v10, v9, 16, 1
	v_add3_u32 v9, v9, v10, s90
	ds_write_b16_d16_hi v8, v9 offset:64
	v_sub_f32_e32 v9, v44, v0
	v_mul_f32_e32 v9, v9, v1
	v_bfe_u32 v10, v9, 16, 1
	v_add3_u32 v9, v9, v10, s90
	ds_write_b16_d16_hi v8, v9 offset:128
	v_sub_f32_e32 v9, v60, v0
	v_mul_f32_e32 v9, v9, v1
	v_bfe_u32 v10, v9, 16, 1
	v_add3_u32 v9, v9, v10, s90
	ds_write_b16_d16_hi v8, v9 offset:192
	v_sub_f32_e32 v9, v108, v0
	v_mul_f32_e32 v9, v9, v1
	v_bfe_u32 v10, v9, 16, 1
	v_add3_u32 v9, v9, v10, s90
	ds_write_b16_d16_hi v8, v9 offset:256
	v_sub_f32_e32 v9, v124, v0
	v_mul_f32_e32 v9, v9, v1
	v_bfe_u32 v10, v9, 16, 1
	v_add3_u32 v9, v9, v10, s90
	ds_write_b16_d16_hi v8, v9 offset:320
	v_sub_f32_e32 v9, v92, v0
	v_mul_f32_e32 v9, v9, v1
	v_bfe_u32 v10, v9, 16, 1
	v_add3_u32 v9, v9, v10, s90
	v_sub_f32_e32 v0, v76, v0
	ds_write_b16_d16_hi v8, v9 offset:384
	v_mul_f32_e32 v9, v0, v1
	v_pk_add_f32 v[0:1], v[134:135], v[2:3]
	s_nop 0
	v_pk_mul_f32 v[0:1], v[0:1], s[36:37] op_sel_hi:[1,0]
	s_nop 0
	v_fma_f32 v1, -v0, v0, v1
	v_max_f32_e32 v1, 0, v1
	v_add_f32_e32 v1, 0x358637bd, v1
	v_mul_f32_e32 v2, 0x4b800000, v1
	v_cmp_gt_f32_e32 vcc, s89, v1
	v_sub_f32_e32 v3, v29, v0
	s_nop 0
	v_cndmask_b32_e32 v1, v1, v2, vcc
	v_rsq_f32_e32 v1, v1
	v_bfe_u32 v2, v9, 16, 1
	v_add3_u32 v2, v9, v2, s90
	ds_write_b16_d16_hi v8, v2 offset:448
	v_mul_f32_e32 v2, 0x45800000, v1
	v_cndmask_b32_e32 v1, v1, v2, vcc
	v_mul_f32_e32 v3, v3, v1
	v_lshlrev_b32_e32 v2, 10, v206
	v_bfe_u32 v8, v3, 16, 1
	v_add3_u32 v3, v3, v8, s90
	v_add3_u32 v2, 0, v2, v16
	ds_write_b16_d16_hi v2, v3
	v_sub_f32_e32 v3, v13, v0
	v_mul_f32_e32 v3, v3, v1
	v_bfe_u32 v8, v3, 16, 1
	v_add3_u32 v3, v3, v8, s90
	ds_write_b16_d16_hi v2, v3 offset:64
	v_sub_f32_e32 v3, v45, v0
	v_mul_f32_e32 v3, v3, v1
	v_bfe_u32 v8, v3, 16, 1
	v_add3_u32 v3, v3, v8, s90
	ds_write_b16_d16_hi v2, v3 offset:128
	v_sub_f32_e32 v3, v61, v0
	v_mul_f32_e32 v3, v3, v1
	v_bfe_u32 v8, v3, 16, 1
	v_add3_u32 v3, v3, v8, s90
	ds_write_b16_d16_hi v2, v3 offset:192
	v_sub_f32_e32 v3, v109, v0
	v_mul_f32_e32 v3, v3, v1
	v_bfe_u32 v8, v3, 16, 1
	v_add3_u32 v3, v3, v8, s90
	ds_write_b16_d16_hi v2, v3 offset:256
	v_sub_f32_e32 v3, v125, v0
	v_mul_f32_e32 v3, v3, v1
	v_bfe_u32 v8, v3, 16, 1
	v_add3_u32 v3, v3, v8, s90
	ds_write_b16_d16_hi v2, v3 offset:320
	v_sub_f32_e32 v3, v93, v0
	v_mul_f32_e32 v3, v3, v1
	v_bfe_u32 v8, v3, 16, 1
	v_add3_u32 v3, v3, v8, s90
	v_sub_f32_e32 v0, v77, v0
	ds_write_b16_d16_hi v2, v3 offset:384
	v_mul_f32_e32 v3, v0, v1
	s_waitcnt lgkmcnt(14)
; #define LAS __attribute__((address_space(3)))
; __device__ __forceinline__ bf16_t f2bf(float f) { unsigned u = __builtin_bit_cast(unsigned, f); return (bf16_t)((u + 0x7fffu + ((u >> 16) & 1u)) >> 16); }
; __device__ __forceinline__ int crow(int r, int hi) { return (r & 3) + 8 * (r >> 2) + 4 * hi; }
; __device__ __forceinline__ int crow(int r, int hi) { return (r & 3) + 8 * (r >> 2) + 4 * hi; }
; template <int DK, int DV, bool MLSTM>
; __device__ __forceinline__ void out_unit2(LAS unsigned char* lds, LAS unsigned char* ldstab, const OutArgs a, const int wv) {
;     ...
;     for (int r = 0; r < 16; ++r) {
;         const int row = 32 * rb + crow(r, hi);
;         const float t1 = s1[r] + exch[((1 - dh) * 128 + row) * 2], t2 = s2[r] + exch[((1 - dh) * 128 + row) * 2 + 1];
;         float mean, inv;
;         if (MLSTM) { mean = 0.f; inv = rsqrtf(t2 * (1.f / DV) + EPS); }
;         else { mean = t1 * (1.f / DV); inv = rsqrtf(fmaxf(t2 * (1.f / DV) - mean * mean, 0.f) + EPS); }
; #pragma unroll
;         for (int nb = 0; nb < NB; ++nb) { const int col = dh * (DV / 2) + 32 * nb + r32;
;             *(LAS bf16_t*)(lds + row * TP + col * 2) = f2bf((o[nb][r] - mean) * inv); }
;     }
;     __syncthreads();
;     constexpr int CPR = DV / 8;
; #pragma unroll 1
;     for (int id = tid; id < 128 * CPR; id += 512) { const int row = id / CPR, ch = id % CPR;
;         const u32x4 y = *(const LAS u32x4*)(lds + row * TP + ch * 16);
;         const f32x4 g0 = *(const f32x4*)(a.gain + 8 * ch), g1 = *(const f32x4*)(a.gain + 8 * ch + 4);
	v_pk_add_f32 v[0:1], v[128:129], v[4:5]
	s_nop 0
	v_pk_mul_f32 v[0:1], v[0:1], s[36:37] op_sel_hi:[1,0]
	s_nop 0
	v_fma_f32 v1, -v0, v0, v1
	v_max_f32_e32 v1, 0, v1
	v_add_f32_e32 v1, 0x358637bd, v1
	v_mul_f32_e32 v4, 0x4b800000, v1
	v_cmp_gt_f32_e32 vcc, s89, v1
	s_nop 1
	v_cndmask_b32_e32 v1, v1, v4, vcc
	v_rsq_f32_e32 v1, v1
	v_bfe_u32 v4, v3, 16, 1
	v_add3_u32 v3, v3, v4, s90
	ds_write_b16_d16_hi v2, v3 offset:448
	v_mul_f32_e32 v2, 0x45800000, v1
	v_cndmask_b32_e32 v1, v1, v2, vcc
	v_sub_f32_e32 v3, v30, v0
	v_mul_f32_e32 v3, v3, v1
	v_lshlrev_b32_e32 v2, 10, v162
	v_bfe_u32 v4, v3, 16, 1
	v_add3_u32 v3, v3, v4, s90
	v_add3_u32 v2, 0, v2, v16
	ds_write_b16_d16_hi v2, v3
	v_sub_f32_e32 v3, v14, v0
	v_mul_f32_e32 v3, v3, v1
	v_bfe_u32 v4, v3, 16, 1
	v_add3_u32 v3, v3, v4, s90
	ds_write_b16_d16_hi v2, v3 offset:64
	v_sub_f32_e32 v3, v46, v0
	v_mul_f32_e32 v3, v3, v1
	v_bfe_u32 v4, v3, 16, 1
	v_add3_u32 v3, v3, v4, s90
	ds_write_b16_d16_hi v2, v3 offset:128
	v_sub_f32_e32 v3, v62, v0
	v_mul_f32_e32 v3, v3, v1
	v_bfe_u32 v4, v3, 16, 1
	v_add3_u32 v3, v3, v4, s90
	ds_write_b16_d16_hi v2, v3 offset:192
	v_sub_f32_e32 v3, v110, v0
	v_mul_f32_e32 v3, v3, v1
	v_bfe_u32 v4, v3, 16, 1
	v_add3_u32 v3, v3, v4, s90
	ds_write_b16_d16_hi v2, v3 offset:256
	v_sub_f32_e32 v3, v126, v0
	v_mul_f32_e32 v3, v3, v1
	v_bfe_u32 v4, v3, 16, 1
	v_add3_u32 v3, v3, v4, s90
	ds_write_b16_d16_hi v2, v3 offset:320
	v_sub_f32_e32 v3, v94, v0
	v_mul_f32_e32 v3, v3, v1
	v_bfe_u32 v4, v3, 16, 1
	v_add3_u32 v3, v3, v4, s90
	v_sub_f32_e32 v0, v78, v0
	ds_write_b16_d16_hi v2, v3 offset:384
	v_mul_f32_e32 v3, v0, v1
	v_pk_add_f32 v[0:1], v[130:131], v[6:7]
	s_nop 0
	v_pk_mul_f32 v[0:1], v[0:1], s[36:37] op_sel_hi:[1,0]
	s_nop 0
	v_fma_f32 v1, -v0, v0, v1
	v_max_f32_e32 v1, 0, v1
	v_add_f32_e32 v1, 0x358637bd, v1
	v_mul_f32_e32 v4, 0x4b800000, v1
	v_cmp_gt_f32_e32 vcc, s89, v1
	s_nop 1
	v_cndmask_b32_e32 v1, v1, v4, vcc
	v_rsq_f32_e32 v1, v1
	v_bfe_u32 v4, v3, 16, 1
	v_add3_u32 v3, v3, v4, s90
	ds_write_b16_d16_hi v2, v3 offset:448
	v_mul_f32_e32 v2, 0x45800000, v1
	v_cndmask_b32_e32 v1, v1, v2, vcc
	v_sub_f32_e32 v3, v31, v0
	v_mul_f32_e32 v3, v3, v1
	v_lshlrev_b32_e32 v2, 10, v160
	v_bfe_u32 v4, v3, 16, 1
	v_add3_u32 v3, v3, v4, s90
	v_add3_u32 v2, 0, v2, v16
	ds_write_b16_d16_hi v2, v3
	v_sub_f32_e32 v3, v15, v0
	v_mul_f32_e32 v3, v3, v1
	v_bfe_u32 v4, v3, 16, 1
	v_add3_u32 v3, v3, v4, s90
	ds_write_b16_d16_hi v2, v3 offset:64
	v_sub_f32_e32 v3, v47, v0
	v_mul_f32_e32 v3, v3, v1
	v_bfe_u32 v4, v3, 16, 1
	v_add3_u32 v3, v3, v4, s90
	ds_write_b16_d16_hi v2, v3 offset:128
	v_sub_f32_e32 v3, v63, v0
	v_mul_f32_e32 v3, v3, v1
	v_bfe_u32 v4, v3, 16, 1
	v_add3_u32 v3, v3, v4, s90
	ds_write_b16_d16_hi v2, v3 offset:192
	v_sub_f32_e32 v3, v111, v0
	v_mul_f32_e32 v3, v3, v1
	v_bfe_u32 v4, v3, 16, 1
	v_add3_u32 v3, v3, v4, s90
	ds_write_b16_d16_hi v2, v3 offset:256
	v_sub_f32_e32 v3, v127, v0
	v_mul_f32_e32 v3, v3, v1
	v_bfe_u32 v4, v3, 16, 1
	v_add3_u32 v3, v3, v4, s90
	ds_write_b16_d16_hi v2, v3 offset:320
	v_sub_f32_e32 v3, v95, v0
	v_sub_f32_e32 v0, v79, v0
	v_mul_f32_e32 v3, v3, v1
	v_mul_f32_e32 v0, v0, v1
	v_bfe_u32 v4, v3, 16, 1
	v_bfe_u32 v1, v0, 16, 1
	v_add3_u32 v3, v3, v4, s90
	v_add3_u32 v0, v0, v1, s90
	v_cmp_gt_i32_e32 vcc, s88, v232
	ds_write_b16_d16_hi v2, v3 offset:384
	ds_write_b16_d16_hi v2, v0 offset:448
	s_waitcnt lgkmcnt(0)
	s_barrier
	s_and_saveexec_b64 s[38:39], vcc
	s_cbranch_execz .LBB0_1826
	s_lshl_b32 s4, s8, 2
	s_add_u32 s40, s24, s4
	s_addc_u32 s41, s25, 0
	s_lshl_b64 s[2:3], s[2:3], 11
	s_add_u32 s4, s53, s2
	s_addc_u32 s5, s54, s3
	s_add_u32 s42, s4, s8
	s_addc_u32 s43, s5, 0
	s_add_u32 s2, s55, s2
	s_addc_u32 s3, s56, s3
	s_add_u32 s44, s2, s8
	s_addc_u32 s45, s3, 0
	v_lshl_add_u32 v4, v232, 4, 0
	v_lshlrev_b32_e32 v5, 3, v232
	s_mov_b64 s[46:47], 0
; #define LAS __attribute__((address_space(3)))
; __device__ __forceinline__ float sigmoidf_(float x) { return 1.f / (1.f + __expf(-x)); }
; __device__ __forceinline__ float siluf_(float x) { return x / (1.f + __expf(-x)); }
; __device__ __forceinline__ unsigned pk4_fp8c(float a, float b, float c, float d) { return pk4_fp8(__builtin_amdgcn_fmed3f(a, -448.f, 448.f), __builtin_amdgcn_fmed3f(b, -448.f, 448.f), __builtin_amdgcn_fmed3f(c, -448.f, 448.f), __builtin_amdgcn_fmed3f(d, -448.f, 448.f)); }
; template <int DK, int DV, bool MLSTM>
; __device__ __forceinline__ void out_unit2(LAS unsigned char* lds, LAS unsigned char* ldstab, const OutArgs a, const int wv) {
;     ...
;     for (int id = tid; id < 128 * CPR; id += 512) { const int row = id / CPR, ch = id % CPR;
;         const u32x4 y = *(const LAS u32x4*)(lds + row * TP + ch * 16);
;         const f32x4 g0 = *(const f32x4*)(a.gain + 8 * ch), g1 = *(const f32x4*)(a.gain + 8 * ch + 4);
;         float yv[8] = {bf_lo(y.x), bf_hi(y.x), bf_lo(y.y), bf_hi(y.y), bf_lo(y.z), bf_hi(y.z), bf_lo(y.w), bf_hi(y.w)};
;         float gv[8];
;         if (MLSTM) { const u32x4 g = *(const u32x4*)(a.G + (size_t)row * a.ldg + 8 * ch);
;             gv[0] = bf_lo(g.x); gv[1] = bf_hi(g.x); gv[2] = bf_lo(g.y); gv[3] = bf_hi(g.y); gv[4] = bf_lo(g.z); gv[5] = bf_hi(g.z); gv[6] = bf_lo(g.w); gv[7] = bf_hi(g.w); }
;         else { const u32x2 g = *(const u32x2*)(a.G8 + (size_t)row * a.ldg8 + 8 * ch);
;             const f32x2 e0 = __builtin_amdgcn_cvt_pk_f32_fp8((int)g.x, false), e1 = __builtin_amdgcn_cvt_pk_f32_fp8((int)g.x, true), e2 = __builtin_amdgcn_cvt_pk_f32_fp8((int)g.y, false), e3 = __builtin_amdgcn_cvt_pk_f32_fp8((int)g.y, true);
;             gv[0] = e0[0] * a.g8inv; gv[1] = e0[1] * a.g8inv; gv[2] = e1[0] * a.g8inv; gv[3] = e1[1] * a.g8inv; gv[4] = e2[0] * a.g8inv; gv[5] = e2[1] * a.g8inv; gv[6] = e3[0] * a.g8inv; gv[7] = e3[1] * a.g8inv; }
;         float gn[8] = {g0[0], g0[1], g0[2], g0[3], g1[0], g1[1], g1[2], g1[3]};
;         float ov[8];
; #pragma unroll
;         for (int i = 0; i < 8; ++i) ov[i] = yv[i] * gn[i] * (MLSTM ? sigmoidf_(gv[i]) : siluf_(gv[i]));
;         u32x2 w; w.x = pg8::pk4_fp8c(ov[0] * a.oscale, ov[1] * a.oscale, ov[2] * a.oscale, ov[3] * a.oscale); w.y = pg8::pk4_fp8c(ov[4] * a.oscale, ov[5] * a.oscale, ov[6] * a.oscale, ov[7] * a.oscale);
;         *(u32x2*)(a.Out + (size_t)row * a.ldo + 8 * ch) = w; }
.LBB0_1840:
	v_ashrrev_i32_e32 v6, 31, v232
	ds_read_b128 v[0:3], v4
	v_lshrrev_b32_e32 v6, 26, v6
	v_add_u32_e32 v6, v232, v6
	v_add_u32_e32 v7, 0x200, v232
	v_ashrrev_i32_e32 v6, 6, v6
	v_cmp_lt_i32_e32 vcc, s92, v232
	v_mov_b32_e32 v232, v7
	v_lshlrev_b32_e32 v8, 9, v6
	v_ashrrev_i32_e32 v7, 31, v6
	v_sub_u32_e32 v26, v5, v8
	v_lshlrev_b64 v[28:29], 11, v[6:7]
	s_waitcnt lgkmcnt(0)
	v_lshlrev_b32_e32 v162, 16, v0
	v_and_b32_e32 v10, 0xffff0000, v0
	v_lshlrev_b32_e32 v12, 16, v1
	v_and_b32_e32 v14, 0xffff0000, v1
	v_ashrrev_i32_e32 v27, 31, v26
	v_lshl_add_u64 v[0:1], s[42:43], 0, v[28:29]
	v_lshl_add_u64 v[6:7], v[26:27], 2, s[40:41]
	v_lshl_add_u64 v[0:1], v[0:1], 0, v[26:27]
	v_lshlrev_b32_e32 v16, 16, v2
	v_and_b32_e32 v18, 0xffff0000, v2
	v_lshlrev_b32_e32 v20, 16, v3
	v_and_b32_e32 v22, 0xffff0000, v3
	global_load_dwordx2 v[30:31], v[0:1], off
	s_nop 0
	global_load_dwordx4 v[0:3], v[6:7], off
	s_nop 0
	global_load_dwordx4 v[6:9], v[6:7], off offset:16
	v_mov_b32_e32 v11, v163
	v_mov_b32_e32 v13, v163
	v_mov_b32_e32 v15, v163
	v_mov_b32_e32 v19, v163
	v_mov_b32_e32 v21, v163
	v_mov_b32_e32 v17, v163
	v_mov_b32_e32 v23, v163
	s_or_b64 s[46:47], vcc, s[46:47]
	v_mov_b32_e32 v24, 0
	v_mov_b32_e32 v25, 0
	v_add_u32_e32 v4, 0x2000, v4
	v_add_u32_e32 v5, 0x1000, v5
	s_waitcnt vmcnt(2)
	v_cvt_pk_f32_fp8_e32 v[32:33], v30
	v_cvt_pk_f32_fp8_sdwa v[34:35], v30 src0_sel:WORD_1
	v_cvt_pk_f32_fp8_e32 v[36:37], v31
	v_cvt_pk_f32_fp8_sdwa v[30:31], v31 src0_sel:WORD_1
	s_waitcnt vmcnt(1)
	v_mov_b32_e32 v38, v0
	v_mov_b32_e32 v39, v32
	v_mov_b32_e32 v0, v2
	s_waitcnt vmcnt(0)
	v_mov_b32_e32 v2, v6
	v_mov_b32_e32 v6, v8
	v_mov_b32_e32 v32, v1
	v_mov_b32_e32 v1, v34
	v_mov_b32_e32 v34, v3
	v_mov_b32_e32 v3, v36
	v_mov_b32_e32 v36, v7
	v_mov_b32_e32 v7, v30
	v_mov_b32_e32 v30, v9
	v_pk_mul_f32 v[8:9], v[38:39], v[162:163]
	v_pk_mul_f32 v[10:11], v[32:33], v[10:11]
	v_pk_mul_f32 v[0:1], v[0:1], v[12:13]
	v_pk_mul_f32 v[12:13], v[34:35], v[14:15]
	v_pk_mul_f32 v[14:15], v[36:37], v[18:19]
	v_mul_f32_e32 v18, 0xbfb8aa3b, v9
	v_mul_f32_e32 v19, 0xbfb8aa3b, v11
	v_exp_f32_e32 v18, v18
	v_pk_mul_f32 v[6:7], v[6:7], v[20:21]
	v_mul_f32_e32 v20, 0xbfb8aa3b, v1
	v_exp_f32_e32 v19, v19
	v_pk_mul_f32 v[2:3], v[2:3], v[16:17]
	v_mul_f32_e32 v21, 0xbfb8aa3b, v13
	v_exp_f32_e32 v20, v20
	v_pk_mul_f32 v[16:17], v[30:31], v[22:23]
	v_mul_f32_e32 v22, 0xbfb8aa3b, v3
	v_exp_f32_e32 v21, v21
	v_mul_f32_e32 v23, 0xbfb8aa3b, v15
	v_exp_f32_e32 v22, v22
	v_add_f32_e32 v18, 1.0, v18
	v_exp_f32_e32 v23, v23
	v_add_f32_e32 v19, 1.0, v19
	v_div_scale_f32 v32, s[2:3], v18, v18, v9
	v_add_f32_e32 v20, 1.0, v20
	v_div_scale_f32 v34, s[2:3], v19, v19, v11
	v_rcp_f32_e32 v48, v32
	v_mul_f32_e32 v30, 0xbfb8aa3b, v7
	v_add_f32_e32 v21, 1.0, v21
	v_div_scale_f32 v36, s[4:5], v20, v20, v1
	v_rcp_f32_e32 v49, v34
	v_mul_f32_e32 v31, 0xbfb8aa3b, v17
	v_exp_f32_e32 v30, v30
	v_add_f32_e32 v22, 1.0, v22
	v_div_scale_f32 v38, s[6:7], v21, v21, v13
	v_rcp_f32_e32 v50, v36
	v_exp_f32_e32 v31, v31
	v_add_f32_e32 v23, 1.0, v23
	v_div_scale_f32 v40, s[8:9], v22, v22, v3
	v_rcp_f32_e32 v51, v38
	v_div_scale_f32 v42, s[10:11], v23, v23, v15
	v_rcp_f32_e32 v52, v40
	v_fma_f32 v56, -v32, v48, 1.0
	v_div_scale_f32 v33, vcc, v9, v18, v9
	v_rcp_f32_e32 v53, v42
	v_fma_f32 v57, -v34, v49, 1.0
	v_fmac_f32_e32 v48, v56, v48
	v_add_f32_e32 v30, 1.0, v30
	v_div_scale_f32 v35, s[2:3], v11, v19, v11
	v_fma_f32 v58, -v36, v50, 1.0
	v_fmac_f32_e32 v49, v57, v49
	v_mul_f32_e32 v56, v33, v48
	v_add_f32_e32 v31, 1.0, v31
	v_div_scale_f32 v37, s[4:5], v1, v20, v1
	v_div_scale_f32 v44, s[12:13], v30, v30, v7
	v_fma_f32 v59, -v38, v51, 1.0
	v_fmac_f32_e32 v50, v58, v50
	v_mul_f32_e32 v57, v35, v49
	v_fma_f32 v64, -v32, v56, v33
	v_div_scale_f32 v39, s[6:7], v13, v21, v13
	v_div_scale_f32 v46, s[14:15], v31, v31, v17
	v_rcp_f32_e32 v54, v44
	v_fma_f32 v60, -v40, v52, 1.0
	v_fmac_f32_e32 v51, v59, v51
	v_mul_f32_e32 v58, v37, v50
	v_fma_f32 v65, -v34, v57, v35
	v_fmac_f32_e32 v56, v64, v48
	v_div_scale_f32 v41, s[8:9], v3, v22, v3
	v_rcp_f32_e32 v55, v46
	v_fma_f32 v61, -v42, v53, 1.0
	v_fmac_f32_e32 v52, v60, v52
	v_mul_f32_e32 v59, v39, v51
	v_fma_f32 v66, -v36, v58, v37
	v_fmac_f32_e32 v57, v65, v49
	v_fma_f32 v32, -v32, v56, v33
	v_div_scale_f32 v43, s[10:11], v15, v23, v15
	v_fmac_f32_e32 v53, v61, v53
	v_mul_f32_e32 v60, v41, v52
	v_fma_f32 v67, -v38, v59, v39
	v_fmac_f32_e32 v58, v66, v50
	v_fma_f32 v33, -v34, v57, v35
	v_div_fmas_f32 v32, v32, v48, v56
	s_mov_b64 vcc, s[2:3]
	v_mul_f32_e32 v61, v43, v53
	v_fma_f32 v68, -v40, v60, v41
	v_fmac_f32_e32 v59, v67, v51
	v_fma_f32 v34, -v36, v58, v37
	v_div_fixup_f32 v9, v32, v18, v9
	v_div_fmas_f32 v18, v33, v49, v57
	s_mov_b64 vcc, s[4:5]
	v_fma_f32 v62, -v44, v54, 1.0
	v_fma_f32 v69, -v42, v61, v43
	v_fmac_f32_e32 v60, v68, v52
	v_fma_f32 v35, -v38, v59, v39
	v_mul_f32_e32 v8, v8, v9
	v_div_fixup_f32 v9, v18, v19, v11
	v_div_fmas_f32 v11, v34, v50, v58
	s_mov_b64 vcc, s[6:7]
	v_div_scale_f32 v45, s[12:13], v7, v30, v7
	v_fma_f32 v63, -v46, v55, 1.0
	v_fmac_f32_e32 v54, v62, v54
	v_fmac_f32_e32 v61, v69, v53
	v_fma_f32 v36, -v40, v60, v41
	v_mul_f32_e32 v9, v10, v9
	v_div_fixup_f32 v1, v11, v20, v1
	v_div_fmas_f32 v10, v35, v51, v59
	s_mov_b64 vcc, s[8:9]
	v_div_scale_f32 v47, s[14:15], v17, v31, v17
	v_fmac_f32_e32 v55, v63, v55
	v_mul_f32_e32 v62, v45, v54
	v_fma_f32 v37, -v42, v61, v43
	v_mul_f32_e32 v0, v0, v1
	v_div_fixup_f32 v1, v10, v21, v13
	v_div_fmas_f32 v10, v36, v52, v60
	s_mov_b64 vcc, s[10:11]
	v_mul_f32_e32 v63, v47, v55
	v_fma_f32 v70, -v44, v62, v45
	v_div_fixup_f32 v3, v10, v22, v3
	v_div_fmas_f32 v10, v37, v53, v61
	v_fma_f32 v71, -v46, v63, v47
	v_fmac_f32_e32 v62, v70, v54
	v_mul_f32_e32 v8, 0x41800000, v8
	v_mul_f32_e32 v9, 0x41800000, v9
	v_mul_f32_e32 v2, v2, v3
	v_div_fixup_f32 v3, v10, v23, v15
	v_fmac_f32_e32 v63, v71, v55
	v_fma_f32 v38, -v44, v62, v45
	v_med3_f32 v8, v8, s91, v231
	v_med3_f32 v9, v9, s91, v231
	s_mov_b64 vcc, s[12:13]
	v_mul_f32_e32 v3, v14, v3
	v_fma_f32 v39, -v46, v63, v47
	v_div_fmas_f32 v10, v38, v54, v62
	v_cvt_pk_fp8_f32 v24, v8, v9
	s_mov_b64 vcc, s[14:15]
	v_mul_f32_e32 v2, 0x41800000, v2
	v_mul_f32_e32 v3, 0x41800000, v3
	v_mul_f32_e32 v1, v12, v1
	v_div_fixup_f32 v7, v10, v30, v7
	v_div_fmas_f32 v8, v39, v55, v63
	v_med3_f32 v2, v2, s91, v231
	v_med3_f32 v3, v3, s91, v231
	v_mul_f32_e32 v0, 0x41800000, v0
	v_mul_f32_e32 v1, 0x41800000, v1
	v_mul_f32_e32 v6, v6, v7
	v_div_fixup_f32 v7, v8, v31, v17
	v_cvt_pk_fp8_f32 v25, v2, v3
	v_med3_f32 v0, v0, s91, v231
	v_med3_f32 v1, v1, s91, v231
	v_mul_f32_e32 v7, v16, v7
	v_mul_f32_e32 v6, 0x41800000, v6
	v_cvt_pk_fp8_f32 v24, v0, v1 op_sel:[0,0,1]
	v_mul_f32_e32 v0, 0x41800000, v7
	v_med3_f32 v1, v6, s91, v231
	v_med3_f32 v0, v0, s91, v231
	v_cvt_pk_fp8_f32 v25, v1, v0 op_sel:[0,0,1]
	v_lshl_add_u64 v[0:1], s[44:45], 0, v[28:29]
	v_lshl_add_u64 v[0:1], v[0:1], 0, v[26:27]
	global_store_dwordx2 v[0:1], v[24:25], off
	s_andn2_b64 exec, exec, s[46:47]
	s_cbranch_execnz .LBB0_1840
	s_branch .LBB0_1826

; #define LAS __attribute__((address_space(3)))
; __device__ __forceinline__ void finishSM(f32x16& p0, f32x16& p1, float& l_reg, bf16x8& pa0, bf16x8& pa1, bf16x8& pa2, bf16x8& pa3) {
;   for (int r = 0; r < 16; ++r) p1[r] = __builtin_amdgcn_exp2f(p1[r]);
;   float ps = 0; for (int r = 0; r < 16; ++r) ps += p0[r]; for (int r = 0; r < 16; ++r) ps += p1[r];
;   { auto rr = __builtin_amdgcn_permlane32_swap(__float_as_uint(ps), __float_as_uint(ps), false, false);
;     ps = __uint_as_float(rr[0]) + __uint_as_float(rr[1]); }
;   l_reg += ps;
;     ...
;   PK4(p0, 0, pa0); PK4(p0, 8, pa1); PK4(p1, 0, pa2); PK4(p1, 8, pa3);
;     ...
; }
; __device__ __forceinline__ void qkt(f32x16& p0, f32x16& p1, const LAS char* Ks, const bf16x8* qr, int r32, int hi, float nm) {
; #pragma unroll
;   for (int r = 0; r < 16; ++r) { p0[r] = nm; p1[r] = nm; }
; #pragma unroll
;   for (int d0 = 0; d0 < DQK / 16; ++d0) { int cb = (d0 * 16 + hi * 8) * 2;
;     bf16x8 b0 = *reinterpret_cast<const LAS bf16x8*>(Ks + KSWZ(r32, cb));
;     bf16x8 b1 = *reinterpret_cast<const LAS bf16x8*>(Ks + KSWZ(32 + r32, cb));
;     __builtin_amdgcn_s_setprio(1);
;     p0 = __builtin_amdgcn_mfma_f32_32x32x16_bf16(b0, qr[d0], p0, 0, 0, 0);
;     p1 = __builtin_amdgcn_mfma_f32_32x32x16_bf16(b1, qr[d0], p1, 0, 0, 0);
;     __builtin_amdgcn_s_setprio(0); }
.LBB0_3144:
	s_mov_b32 s74, s4
	s_lshl_b32 s4, s72, 14
	s_add_i32 s75, s4, 0
	v_add_u32_e32 v242, s75, v192
	v_add_u32_e32 v238, v242, v198
	ds_read_b128 v[234:237], v238 offset:24576
	ds_read_b128 v[238:241], v238 offset:32768
	v_add_f32_e32 v33, 0, v80
	v_add_f32_e32 v33, v81, v33
	v_add_f32_e32 v33, v82, v33
	v_add_f32_e32 v33, v83, v33
	v_add_f32_e32 v33, v84, v33
	s_setprio 1
	s_waitcnt lgkmcnt(1)
	v_mfma_f32_32x32x16_bf16 v[112:127], v[234:237], v[128:131], v[48:63]
	v_add_f32_e32 v33, v85, v33
	v_add_f32_e32 v33, v86, v33
	v_add_f32_e32 v33, v87, v33
	v_add_f32_e32 v33, v88, v33
	s_waitcnt lgkmcnt(0)
	v_mfma_f32_32x32x16_bf16 v[96:111], v[238:241], v[128:131], v[48:63]
	s_setprio 0
	v_add_f32_e32 v33, v89, v33
	v_add_f32_e32 v33, v90, v33
	v_add_f32_e32 v33, v91, v33
	v_add_u32_e32 v238, v242, v199
	ds_read_b128 v[234:237], v238 offset:24576
	ds_read_b128 v[238:241], v238 offset:32768
	v_exp_f32_e32 v64, v64
	v_add_f32_e32 v33, v92, v33
	v_exp_f32_e32 v65, v65
	v_add_f32_e32 v33, v93, v33
	v_exp_f32_e32 v66, v66
	s_setprio 1
	s_waitcnt lgkmcnt(1)
	v_mfma_f32_32x32x16_bf16 v[112:127], v[234:237], v[132:135], v[112:127]
	v_add_f32_e32 v33, v94, v33
	v_exp_f32_e32 v67, v67
	v_add_f32_e32 v33, v95, v33
	v_exp_f32_e32 v68, v68
	s_waitcnt lgkmcnt(0)
	v_mfma_f32_32x32x16_bf16 v[96:111], v[238:241], v[132:135], v[96:111]
	s_setprio 0
	v_add_f32_e32 v33, v64, v33
	v_exp_f32_e32 v69, v69
	v_add_f32_e32 v33, v65, v33
	v_add_u32_e32 v238, v242, v200
	ds_read_b128 v[234:237], v238 offset:24576
	ds_read_b128 v[238:241], v238 offset:32768
	v_exp_f32_e32 v70, v70
	v_add_f32_e32 v33, v66, v33
	v_exp_f32_e32 v71, v71
	v_add_f32_e32 v33, v67, v33
	v_exp_f32_e32 v72, v72
	s_setprio 1
	s_waitcnt lgkmcnt(1)
	v_mfma_f32_32x32x16_bf16 v[112:127], v[234:237], v[136:139], v[112:127]
	v_add_f32_e32 v33, v68, v33
	v_exp_f32_e32 v73, v73
	v_add_f32_e32 v33, v69, v33
	v_exp_f32_e32 v74, v74
	s_waitcnt lgkmcnt(0)
	v_mfma_f32_32x32x16_bf16 v[96:111], v[238:241], v[136:139], v[96:111]
	s_setprio 0
	v_add_f32_e32 v33, v70, v33
	v_exp_f32_e32 v75, v75
	v_add_f32_e32 v33, v71, v33
	v_add_u32_e32 v238, v242, v201
	ds_read_b128 v[234:237], v238 offset:24576
	ds_read_b128 v[238:241], v238 offset:32768
	v_exp_f32_e32 v76, v76
	v_add_f32_e32 v33, v72, v33
	v_exp_f32_e32 v77, v77
	v_add_f32_e32 v33, v73, v33
	v_exp_f32_e32 v78, v78
	s_setprio 1
	s_waitcnt lgkmcnt(1)
	v_mfma_f32_32x32x16_bf16 v[112:127], v[234:237], v[140:143], v[112:127]
	v_add_f32_e32 v33, v74, v33
	v_exp_f32_e32 v79, v79
	v_add_f32_e32 v33, v75, v33
	v_add_f32_e32 v33, v76, v33
	s_waitcnt lgkmcnt(0)
	v_mfma_f32_32x32x16_bf16 v[96:111], v[238:241], v[140:143], v[96:111]
	s_setprio 0
	v_add_f32_e32 v33, v77, v33
	v_add_f32_e32 v33, v78, v33
	v_add_f32_e32 v204, v79, v33
	v_add_u32_e32 v238, v242, v202
	ds_read_b128 v[234:237], v238 offset:24576
	ds_read_b128 v[238:241], v238 offset:32768
	v_mov_b32_e32 v205, v204
	v_cvt_pk_bf16_f32 v34, v80, v81
	v_cvt_pk_bf16_f32 v35, v82, v83
	v_cvt_pk_bf16_f32 v36, v84, v85
	v_cvt_pk_bf16_f32 v37, v86, v87
	s_setprio 1
	s_waitcnt lgkmcnt(1)
	v_mfma_f32_32x32x16_bf16 v[112:127], v[234:237], v[148:151], v[112:127]
	v_cvt_pk_bf16_f32 v38, v88, v89
	v_cvt_pk_bf16_f32 v39, v90, v91
	v_cvt_pk_bf16_f32 v40, v92, v93
	v_cvt_pk_bf16_f32 v41, v94, v95
	s_waitcnt lgkmcnt(0)
	v_mfma_f32_32x32x16_bf16 v[96:111], v[238:241], v[148:151], v[96:111]
	s_setprio 0
	v_cvt_pk_bf16_f32 v42, v64, v65
	v_cvt_pk_bf16_f32 v43, v66, v67
	v_cvt_pk_bf16_f32 v44, v68, v69
	v_add_u32_e32 v242, v242, v203
	ds_read_b128 v[234:237], v242 offset:24576
	ds_read_b128 v[238:241], v242 offset:32768
	v_cvt_pk_bf16_f32 v45, v70, v71
	v_cvt_pk_bf16_f32 v164, v72, v73
	v_cvt_pk_bf16_f32 v165, v74, v75
	v_cvt_pk_bf16_f32 v166, v76, v77
	v_cvt_pk_bf16_f32 v167, v78, v79
	s_setprio 1
	s_waitcnt lgkmcnt(1)
	v_mfma_f32_32x32x16_bf16 v[112:127], v[234:237], v[144:147], v[112:127]
	s_nop 1
	v_permlane32_swap_b32_e32 v204, v205
	v_permlane32_swap_b32_e32 v34, v36
	v_permlane32_swap_b32_e32 v35, v37
	s_waitcnt lgkmcnt(0)
	v_mfma_f32_32x32x16_bf16 v[96:111], v[238:241], v[144:147], v[96:111]
	s_setprio 0
	v_permlane32_swap_b32_e32 v38, v40
	v_permlane32_swap_b32_e32 v39, v41
	v_permlane32_swap_b32_e32 v42, v44
	v_permlane32_swap_b32_e32 v43, v45
	v_permlane32_swap_b32_e32 v164, v166
	v_permlane32_swap_b32_e32 v165, v167
	s_cmp_lt_u32 s73, 61
	s_cselect_b64 s[4:5], -1, 0
	s_cmp_gt_u32 s73, 60
	v_lshl_add_u64 v[180:181], s[22:23], 0, v[176:177]
	v_lshl_add_u64 v[178:179], s[22:23], 0, v[174:175]
	s_cbranch_scc1 .LBB0_3146
	v_add_co_u32_e32 v46, vcc, 0x66006000, v180
	s_nop 1
	v_addc_co_u32_e32 v47, vcc, 0, v181, vcc
	s_waitcnt vmcnt(1)
	v_add_co_u32_e32 v156, vcc, 0x6200c000, v178
	s_nop 1
	v_addc_co_u32_e32 v157, vcc, 0, v179, vcc
	global_load_dwordx4 v[152:155], v[46:47], off
	s_nop 0
	global_load_dwordx4 v[156:159], v[156:157], off
	v_add_co_u32_e32 v46, vcc, 0x6200e000, v178
	s_nop 1
	v_addc_co_u32_e32 v47, vcc, 0, v179, vcc
	global_load_dwordx4 v[160:163], v[46:47], off

; #define LAS __attribute__((address_space(3)))
; __device__ __forceinline__ void finishSM(f32x16& p0, f32x16& p1, float& l_reg, bf16x8& pa0, bf16x8& pa1, bf16x8& pa2, bf16x8& pa3) {
;   for (int r = 0; r < 16; ++r) p1[r] = __builtin_amdgcn_exp2f(p1[r]);
;   float ps = 0; for (int r = 0; r < 16; ++r) ps += p0[r]; for (int r = 0; r < 16; ++r) ps += p1[r];
;   { auto rr = __builtin_amdgcn_permlane32_swap(__float_as_uint(ps), __float_as_uint(ps), false, false);
;     ps = __uint_as_float(rr[0]) + __uint_as_float(rr[1]); }
;   l_reg += ps;
;     ...
;   PK4(p0, 0, pa0); PK4(p0, 8, pa1); PK4(p1, 0, pa2); PK4(p1, 8, pa3);
;     ...
; }
; __device__ __forceinline__ void qkt(f32x16& p0, f32x16& p1, const LAS char* Ks, const bf16x8* qr, int r32, int hi, float nm) {
; #pragma unroll
;   for (int r = 0; r < 16; ++r) { p0[r] = nm; p1[r] = nm; }
; #pragma unroll
;   for (int d0 = 0; d0 < DQK / 16; ++d0) { int cb = (d0 * 16 + hi * 8) * 2;
;     bf16x8 b0 = *reinterpret_cast<const LAS bf16x8*>(Ks + KSWZ(r32, cb));
;     bf16x8 b1 = *reinterpret_cast<const LAS bf16x8*>(Ks + KSWZ(32 + r32, cb));
;     __builtin_amdgcn_s_setprio(1);
;     p0 = __builtin_amdgcn_mfma_f32_32x32x16_bf16(b0, qr[d0], p0, 0, 0, 0);
;     p1 = __builtin_amdgcn_mfma_f32_32x32x16_bf16(b1, qr[d0], p1, 0, 0, 0);
;     __builtin_amdgcn_s_setprio(0); }
.LBB0_3148:
	s_cmp_lt_u32 s73, 62
	s_cselect_b64 s[14:15], -1, 0
	s_cmp_gt_u32 s73, 61
	s_cselect_b64 s[4:5], -1, 0
	s_and_b64 vcc, exec, s[4:5]
	s_cbranch_vccnz .Lattn1_s2only
	v_lshl_add_u32 v243, s74, 14, v193
	v_add_u32_e32 v238, v243, v198
	ds_read_b128 v[234:237], v238 offset:24576
	ds_read_b128 v[238:241], v238 offset:32768
	v_exp_f32_e32 v34, v112
	v_exp_f32_e32 v35, v113
	v_exp_f32_e32 v36, v114
	v_exp_f32_e32 v37, v115
	v_exp_f32_e32 v38, v116
	v_add_f32_e32 v33, 0, v34
	v_exp_f32_e32 v39, v117
	s_setprio 1
	s_waitcnt lgkmcnt(1)
	v_mfma_f32_32x32x16_bf16 v[80:95], v[234:237], v[128:131], v[48:63]
	v_add_f32_e32 v33, v35, v33
	v_exp_f32_e32 v40, v118
	v_add_f32_e32 v33, v36, v33
	v_exp_f32_e32 v41, v119
	v_add_f32_e32 v33, v37, v33
	s_waitcnt lgkmcnt(0)
	v_mfma_f32_32x32x16_bf16 v[64:79], v[238:241], v[128:131], v[48:63]
	s_setprio 0
	v_exp_f32_e32 v42, v120
	v_add_f32_e32 v33, v38, v33
	v_exp_f32_e32 v43, v121
	v_add_f32_e32 v33, v39, v33
	v_add_u32_e32 v238, v243, v199
	ds_read_b128 v[234:237], v238 offset:24576
	ds_read_b128 v[238:241], v238 offset:32768
	v_exp_f32_e32 v44, v122
	v_add_f32_e32 v33, v40, v33
	v_exp_f32_e32 v45, v123
	v_add_f32_e32 v33, v41, v33
	v_exp_f32_e32 v47, v124
	v_add_f32_e32 v33, v42, v33
	v_exp_f32_e32 v112, v125
	s_setprio 1
	s_waitcnt lgkmcnt(1)
	v_mfma_f32_32x32x16_bf16 v[80:95], v[234:237], v[132:135], v[80:95]
	v_add_f32_e32 v33, v43, v33
	v_exp_f32_e32 v113, v126
	v_add_f32_e32 v33, v44, v33
	v_exp_f32_e32 v114, v127
	v_add_f32_e32 v33, v45, v33
	s_waitcnt lgkmcnt(0)
	v_mfma_f32_32x32x16_bf16 v[64:79], v[238:241], v[132:135], v[64:79]
	s_setprio 0
	v_exp_f32_e32 v96, v96
	v_add_f32_e32 v33, v47, v33
	v_exp_f32_e32 v97, v97
	v_add_f32_e32 v33, v112, v33
	v_add_u32_e32 v238, v243, v200
	ds_read_b128 v[234:237], v238 offset:24576
	ds_read_b128 v[238:241], v238 offset:32768
	v_exp_f32_e32 v98, v98
	v_add_f32_e32 v33, v113, v33
	v_exp_f32_e32 v99, v99
	v_add_f32_e32 v33, v114, v33
	v_exp_f32_e32 v100, v100
	v_add_f32_e32 v33, v96, v33
	v_exp_f32_e32 v101, v101
	s_setprio 1
	s_waitcnt lgkmcnt(1)
	v_mfma_f32_32x32x16_bf16 v[80:95], v[234:237], v[136:139], v[80:95]
	v_add_f32_e32 v33, v97, v33
	v_exp_f32_e32 v102, v102
	v_add_f32_e32 v33, v98, v33
	v_exp_f32_e32 v103, v103
	v_add_f32_e32 v33, v99, v33
	s_waitcnt lgkmcnt(0)
	v_mfma_f32_32x32x16_bf16 v[64:79], v[238:241], v[136:139], v[64:79]
	s_setprio 0
	v_exp_f32_e32 v104, v104
	v_add_f32_e32 v33, v100, v33
	v_exp_f32_e32 v105, v105
	v_add_f32_e32 v33, v101, v33
	v_add_u32_e32 v238, v243, v201
	ds_read_b128 v[234:237], v238 offset:24576
	ds_read_b128 v[238:241], v238 offset:32768
	v_exp_f32_e32 v106, v106
	v_add_f32_e32 v33, v102, v33
	v_exp_f32_e32 v107, v107
	v_add_f32_e32 v33, v103, v33
	v_exp_f32_e32 v108, v108
	v_add_f32_e32 v33, v104, v33
	v_exp_f32_e32 v109, v109
	s_setprio 1
	s_waitcnt lgkmcnt(1)
	v_mfma_f32_32x32x16_bf16 v[80:95], v[234:237], v[140:143], v[80:95]
	v_add_f32_e32 v33, v105, v33
	v_exp_f32_e32 v110, v110
	v_add_f32_e32 v33, v106, v33
	v_exp_f32_e32 v111, v111
	v_add_f32_e32 v33, v107, v33
	s_waitcnt lgkmcnt(0)
	v_mfma_f32_32x32x16_bf16 v[64:79], v[238:241], v[140:143], v[64:79]
	s_setprio 0
	v_add_f32_e32 v33, v108, v33
	v_add_f32_e32 v33, v109, v33
	v_add_f32_e32 v33, v110, v33
	v_add_f32_e32 v33, v111, v33
	v_add_u32_e32 v238, v243, v202
	ds_read_b128 v[234:237], v238 offset:24576
	ds_read_b128 v[238:241], v238 offset:32768
	v_mov_b32_e32 v46, v33
	v_cvt_pk_bf16_f32 v34, v34, v35
	v_cvt_pk_bf16_f32 v35, v36, v37
	v_cvt_pk_bf16_f32 v36, v38, v39
	v_cvt_pk_bf16_f32 v37, v40, v41
	v_cvt_pk_bf16_f32 v38, v42, v43
	v_cvt_pk_bf16_f32 v39, v44, v45
	s_setprio 1
	s_waitcnt lgkmcnt(1)
	v_mfma_f32_32x32x16_bf16 v[80:95], v[234:237], v[148:151], v[80:95]
	v_cvt_pk_bf16_f32 v40, v47, v112
	v_cvt_pk_bf16_f32 v41, v113, v114
	v_cvt_pk_bf16_f32 v42, v96, v97
	v_cvt_pk_bf16_f32 v43, v98, v99
	v_cvt_pk_bf16_f32 v44, v100, v101
	s_waitcnt lgkmcnt(0)
	v_mfma_f32_32x32x16_bf16 v[64:79], v[238:241], v[148:151], v[64:79]
	s_setprio 0
	v_cvt_pk_bf16_f32 v45, v102, v103
	v_cvt_pk_bf16_f32 v96, v104, v105
	v_cvt_pk_bf16_f32 v97, v106, v107
	v_cvt_pk_bf16_f32 v98, v108, v109
	v_add_u32_e32 v238, v243, v203
	ds_read_b128 v[234:237], v238 offset:24576
	ds_read_b128 v[238:241], v238 offset:32768
	v_cvt_pk_bf16_f32 v99, v110, v111
	s_nop 1
	v_permlane32_swap_b32_e32 v33, v46
	v_permlane32_swap_b32_e32 v34, v36
	v_permlane32_swap_b32_e32 v35, v37
	v_permlane32_swap_b32_e32 v38, v40
	v_permlane32_swap_b32_e32 v39, v41
	s_setprio 1
	s_waitcnt lgkmcnt(1)
	v_mfma_f32_32x32x16_bf16 v[80:95], v[234:237], v[144:147], v[80:95]
	v_permlane32_swap_b32_e32 v42, v44
	v_permlane32_swap_b32_e32 v43, v45
	v_permlane32_swap_b32_e32 v96, v98
	v_permlane32_swap_b32_e32 v97, v99
	s_waitcnt lgkmcnt(0)
	v_mfma_f32_32x32x16_bf16 v[64:79], v[238:241], v[144:147], v[64:79]
	s_setprio 0
	s_branch .Lattn1_join

; #define SBAR() __builtin_amdgcn_sched_barrier(0)
; #define SLOAD(k0) do { sr_.vs0 = *reinterpret_cast<const bf16x8*>(&Vh[(long)((k0) + vr) * DVV + vc]); \
;     sr_.ks0 = *reinterpret_cast<const bf16x8*>(&Kh[(long)((k0) + sr) * KROW + sc]); sr_.ks1 = *reinterpret_cast<const bf16x8*>(&Kh[(long)((k0) + 32 + sr) * KROW + sc]); } while (0)
; template <int D0> __device__ __forceinline__ void pv_one(f32x16& od, int vb, bf16x8 pa0, bf16x8 pa1, bf16x8 pa2, bf16x8 pa3) {
;   const s16x4 l0 = tr_read<v_rd_off(D0, 0, 0)>(vb), h0 = tr_read<v_rd_off(D0, 0, 1)>(vb), l1 = tr_read<v_rd_off(D0, 1, 0)>(vb), h1 = tr_read<v_rd_off(D0, 1, 1)>(vb);
;   const s16x4 l2 = tr_read<v_rd_off(D0, 2, 0)>(vb), h2 = tr_read<v_rd_off(D0, 2, 1)>(vb), l3 = tr_read<v_rd_off(D0, 3, 0)>(vb), h3 = tr_read<v_rd_off(D0, 3, 1)>(vb);
;   asm volatile("s_waitcnt lgkmcnt(0)" ::: "memory"); SBAR();
;     ...
;   __builtin_amdgcn_s_setprio(1);
;   od = __builtin_amdgcn_mfma_f32_32x32x16_bf16(pa0, PK(l0, h0), od, 0, 0, 0);
;   od = __builtin_amdgcn_mfma_f32_32x32x16_bf16(pa1, PK(l1, h1), od, 0, 0, 0);
;   od = __builtin_amdgcn_mfma_f32_32x32x16_bf16(pa2, PK(l2, h2), od, 0, 0, 0);
;   od = __builtin_amdgcn_mfma_f32_32x32x16_bf16(pa3, PK(l3, h3), od, 0, 0, 0);
;   __builtin_amdgcn_s_setprio(0);
;     ...
; }
; __device__ __forceinline__ void pv_d0(f32x16* o, int vb, bf16x8 pa0, bf16x8 pa1, bf16x8 pa2, bf16x8 pa3) {
;   pv_one<0>(o[0], vb, pa0, pa1, pa2, pa3); pv_one<1>(o[1], vb, pa0, pa1, pa2, pa3);
; }
; __device__ __forceinline__ void attn_body(const bf16_t* __restrict__ Qb, const bf16_t* __restrict__ Kh, const bf16_t* __restrict__ Vh, unsigned char* __restrict__ Ob, int ldo, int seq, LAS char* lds, const int wv, const float kbound, const float oscale) {
;     ...
;     if (j + 4 < NT) SLOAD((j + 4) * KVBLK); SBAR();
;     pv_d0(o, vb0 + b1 * (int)SHM_V, pa0, pa1, pa2, pa3); if (j + 2 < NT) partialSM(pA0, pA1);
.Lattn1_join:
	s_cmp_lt_u32 s73, 60
	s_cselect_b64 s[16:17], -1, 0
	s_cmp_gt_u32 s73, 59
	s_cbranch_scc1 .LBB0_3152
	v_add_co_u32_e32 v100, vcc, 0x66008000, v180
	s_nop 1
	v_addc_co_u32_e32 v101, vcc, 0, v181, vcc
	v_add_co_u32_e32 v102, vcc, 0x62010000, v178
	s_nop 1
	v_addc_co_u32_e32 v103, vcc, 0, v179, vcc
	global_load_dwordx4 v[152:155], v[100:101], off
	global_load_dwordx4 v[156:159], v[102:103], off
	v_add_co_u32_e32 v100, vcc, 0x62012000, v178
	s_nop 1
	v_addc_co_u32_e32 v101, vcc, 0, v179, vcc
	global_load_dwordx4 v[160:163], v[100:101], off
.LBB0_3152:
	s_lshl_b32 s76, s72, 13
	v_add_u32_e32 v47, s76, v188
	ds_read_b64_tr_b16 v[100:101], v47 offset:0
	ds_read_b64_tr_b16 v[102:103], v47 offset:0x400
	ds_read_b64_tr_b16 v[104:105], v47 offset:0x800
	ds_read_b64_tr_b16 v[106:107], v47 offset:0xc00
	ds_read_b64_tr_b16 v[108:109], v47 offset:0x1000
	ds_read_b64_tr_b16 v[110:111], v47 offset:0x1400
	ds_read_b64_tr_b16 v[112:113], v47 offset:0x1800
	ds_read_b64_tr_b16 v[114:115], v47 offset:0x1c00
	s_waitcnt lgkmcnt(0)
	s_setprio 1
	v_mfma_f32_32x32x16_bf16 v[0:15], v[34:37], v[100:103], v[0:15]
	v_exp_f32_e32 v80, v80
	v_exp_f32_e32 v81, v81
	v_mfma_f32_32x32x16_bf16 v[0:15], v[38:41], v[104:107], v[0:15]
	v_exp_f32_e32 v82, v82
	v_exp_f32_e32 v83, v83
	v_mfma_f32_32x32x16_bf16 v[0:15], v[42:45], v[108:111], v[0:15]
	v_exp_f32_e32 v84, v84
	v_exp_f32_e32 v85, v85
	v_mfma_f32_32x32x16_bf16 v[0:15], v[96:99], v[112:115], v[0:15]
	v_exp_f32_e32 v86, v86
	v_exp_f32_e32 v87, v87
	s_setprio 0
	ds_read_b64_tr_b16 v[100:101], v47 offset:0x200
	ds_read_b64_tr_b16 v[102:103], v47 offset:0x600
	ds_read_b64_tr_b16 v[104:105], v47 offset:0xa00
	ds_read_b64_tr_b16 v[106:107], v47 offset:0xe00
	ds_read_b64_tr_b16 v[108:109], v47 offset:0x1200
	ds_read_b64_tr_b16 v[110:111], v47 offset:0x1600
	ds_read_b64_tr_b16 v[112:113], v47 offset:0x1a00
	ds_read_b64_tr_b16 v[114:115], v47 offset:0x1e00
	s_waitcnt lgkmcnt(0)
	s_setprio 1
	v_mfma_f32_32x32x16_bf16 v[16:31], v[34:37], v[100:103], v[16:31]
	v_exp_f32_e32 v88, v88
	v_exp_f32_e32 v89, v89
	v_mfma_f32_32x32x16_bf16 v[16:31], v[38:41], v[104:107], v[16:31]
	v_exp_f32_e32 v90, v90
	v_exp_f32_e32 v91, v91
	v_mfma_f32_32x32x16_bf16 v[16:31], v[42:45], v[108:111], v[16:31]
	v_exp_f32_e32 v92, v92
	v_exp_f32_e32 v93, v93
	v_mfma_f32_32x32x16_bf16 v[16:31], v[96:99], v[112:115], v[16:31]
	v_exp_f32_e32 v94, v94
	v_exp_f32_e32 v95, v95
	s_setprio 0

; #define LAS __attribute__((address_space(3)))
; __device__ __forceinline__ bf16_t f2bf(float f) { unsigned u = __builtin_bit_cast(unsigned, f); return (bf16_t)((u + 0x7fffu + ((u >> 16) & 1u)) >> 16); }
; __device__ __forceinline__ int crow(int r, int hi) { return (r & 3) + 8 * (r >> 2) + 4 * hi; }
; __device__ __forceinline__ int crow(int r, int hi) { return (r & 3) + 8 * (r >> 2) + 4 * hi; }
; template <int DK, int DV, bool MLSTM>
; __device__ __forceinline__ void out_unit2(LAS unsigned char* lds, LAS unsigned char* ldstab, const OutArgs a, const int wv) {
;     ...
;     for (int r = 0; r < 16; ++r) {
;         const int row = 32 * rb + crow(r, hi);
;         const float t1 = s1[r] + exch[((1 - dh) * 128 + row) * 2], t2 = s2[r] + exch[((1 - dh) * 128 + row) * 2 + 1];
;         float mean, inv;
;         if (MLSTM) { mean = 0.f; inv = rsqrtf(t2 * (1.f / DV) + EPS); }
;         else { mean = t1 * (1.f / DV); inv = rsqrtf(fmaxf(t2 * (1.f / DV) - mean * mean, 0.f) + EPS); }
; #pragma unroll
;         for (int nb = 0; nb < NB; ++nb) { const int col = dh * (DV / 2) + 32 * nb + r32;
;             *(LAS bf16_t*)(lds + row * TP + col * 2) = f2bf((o[nb][r] - mean) * inv); }
.LBB0_4313:
	s_or_b64 exec, exec, s[4:5]
	v_lshlrev_b32_e32 v164, 1, v219
	v_subrev_u32_e32 v164, s6, v164
	s_add_i32 s4, 0, 0x22100
	v_lshl_add_u32 v164, v164, 2, s4
	s_waitcnt vmcnt(0) lgkmcnt(0)
	s_barrier
	ds_read_b128 v[164:167], v164 offset:1024
	v_lshlrev_b32_e32 v168, 1, v217
	v_subrev_u32_e32 v168, s6, v168
	v_lshl_add_u32 v168, v168, 2, s4
	ds_read2_b64 v[168:171], v168 offset0:128 offset1:129
	s_waitcnt lgkmcnt(1)
	v_pk_add_f32 v[156:157], v[156:157], v[164:165]
	s_nop 0
	v_pk_mul_f32 v[156:157], v[156:157], s[26:27] op_sel_hi:[1,0]
	s_nop 0
	v_fma_f32 v157, -v156, v156, v157
	v_max_f32_e32 v157, 0, v157
	v_add_f32_e32 v157, 0x358637bd, v157
	v_mul_f32_e32 v164, 0x4b800000, v157
	v_cmp_gt_f32_e32 vcc, s89, v157
	v_sub_f32_e32 v16, v16, v156
	v_sub_f32_e32 v0, v0, v156
	v_cndmask_b32_e32 v157, v157, v164, vcc
	v_rsq_f32_e32 v157, v157
	v_or_b32_e32 v164, s6, v233
	v_mul_f32_e32 v165, 0x45800000, v157
	v_cndmask_b32_e32 v157, v157, v165, vcc
	v_mul_f32_e32 v16, v16, v157
	v_bfe_u32 v172, v16, 16, 1
	v_lshlrev_b32_e32 v165, 10, v219
	v_add3_u32 v172, v16, v172, s90
	v_lshlrev_b32_e32 v16, 1, v164
	v_mul_f32_e32 v0, v0, v157
	v_add3_u32 v164, 0, v165, v16
	v_bfe_u32 v165, v0, 16, 1
	v_add3_u32 v0, v0, v165, s90
	ds_write_b16_d16_hi v164, v0 offset:64
	v_sub_f32_e32 v0, v32, v156
	v_mul_f32_e32 v0, v0, v157
	v_bfe_u32 v32, v0, 16, 1
	v_add3_u32 v0, v0, v32, s90
	ds_write_b16_d16_hi v164, v0 offset:128
	v_sub_f32_e32 v0, v48, v156
	v_mul_f32_e32 v0, v0, v157
	v_bfe_u32 v32, v0, 16, 1
	v_add3_u32 v0, v0, v32, s90
	ds_write_b16_d16_hi v164, v0 offset:192
	v_sub_f32_e32 v0, v96, v156
	v_mul_f32_e32 v0, v0, v157
	v_bfe_u32 v32, v0, 16, 1
	v_add3_u32 v0, v0, v32, s90
	ds_write_b16_d16_hi v164, v0 offset:256
	v_sub_f32_e32 v0, v112, v156
	v_mul_f32_e32 v0, v0, v157
	v_bfe_u32 v32, v0, 16, 1
	v_add3_u32 v0, v0, v32, s90
	ds_write_b16_d16_hi v164, v0 offset:320
	v_sub_f32_e32 v0, v80, v156
	v_mul_f32_e32 v0, v0, v157
	v_bfe_u32 v32, v0, 16, 1
	v_add3_u32 v0, v0, v32, s90
	ds_write_b16_d16_hi v164, v0 offset:384
	v_sub_f32_e32 v0, v64, v156
	v_mul_f32_e32 v0, v0, v157
	v_pk_add_f32 v[156:157], v[158:159], v[166:167]
	ds_write_b16_d16_hi v164, v172
	v_pk_mul_f32 v[156:157], v[156:157], s[26:27] op_sel_hi:[1,0]
	s_nop 0
	v_fma_f32 v32, -v156, v156, v157
	v_max_f32_e32 v32, 0, v32
	v_add_f32_e32 v32, 0x358637bd, v32
	v_mul_f32_e32 v48, 0x4b800000, v32
	v_cmp_gt_f32_e32 vcc, s89, v32
	v_sub_f32_e32 v17, v17, v156
	v_sub_f32_e32 v1, v1, v156
	v_cndmask_b32_e32 v32, v32, v48, vcc
	v_rsq_f32_e32 v32, v32
	v_bfe_u32 v48, v0, 16, 1
	v_add3_u32 v0, v0, v48, s90
	ds_write_b16_d16_hi v164, v0 offset:448
	v_mul_f32_e32 v0, 0x45800000, v32
	v_cndmask_b32_e32 v0, v32, v0, vcc
	v_mul_f32_e32 v17, v17, v0
	v_lshlrev_b32_e32 v32, 10, v218
	v_bfe_u32 v48, v17, 16, 1
	v_add3_u32 v17, v17, v48, s90
	v_add3_u32 v32, 0, v32, v16
	v_mul_f32_e32 v1, v1, v0
	ds_write_b16_d16_hi v32, v17
	v_bfe_u32 v17, v1, 16, 1
	v_add3_u32 v1, v1, v17, s90
	ds_write_b16_d16_hi v32, v1 offset:64
	v_sub_f32_e32 v1, v33, v156
	v_mul_f32_e32 v1, v1, v0
	v_bfe_u32 v17, v1, 16, 1
	v_add3_u32 v1, v1, v17, s90
	ds_write_b16_d16_hi v32, v1 offset:128
	v_sub_f32_e32 v1, v49, v156
	v_mul_f32_e32 v1, v1, v0
	v_bfe_u32 v17, v1, 16, 1
	v_add3_u32 v1, v1, v17, s90
	ds_write_b16_d16_hi v32, v1 offset:192
	v_sub_f32_e32 v1, v97, v156
	v_mul_f32_e32 v1, v1, v0
	v_bfe_u32 v17, v1, 16, 1
	v_add3_u32 v1, v1, v17, s90
	ds_write_b16_d16_hi v32, v1 offset:256
	v_sub_f32_e32 v1, v113, v156
	v_mul_f32_e32 v1, v1, v0
	v_bfe_u32 v17, v1, 16, 1
	v_add3_u32 v1, v1, v17, s90
	ds_write_b16_d16_hi v32, v1 offset:320
	v_sub_f32_e32 v1, v81, v156
	v_mul_f32_e32 v1, v1, v0
	v_bfe_u32 v17, v1, 16, 1
	v_add3_u32 v1, v1, v17, s90
	ds_write_b16_d16_hi v32, v1 offset:384
	v_sub_f32_e32 v1, v65, v156
	v_mul_f32_e32 v17, v1, v0
	s_waitcnt lgkmcnt(14)
	v_pk_add_f32 v[0:1], v[152:153], v[168:169]
	s_nop 0
	v_pk_mul_f32 v[0:1], v[0:1], s[26:27] op_sel_hi:[1,0]
	s_nop 0
	v_fma_f32 v1, -v0, v0, v1
	v_max_f32_e32 v1, 0, v1
	v_add_f32_e32 v1, 0x358637bd, v1
	v_mul_f32_e32 v33, 0x4b800000, v1
	v_cmp_gt_f32_e32 vcc, s89, v1
	v_sub_f32_e32 v18, v18, v0
	v_sub_f32_e32 v2, v2, v0
	v_cndmask_b32_e32 v1, v1, v33, vcc
	v_rsq_f32_e32 v1, v1
	v_bfe_u32 v33, v17, 16, 1
	v_add3_u32 v17, v17, v33, s90
	ds_write_b16_d16_hi v32, v17 offset:448
	v_mul_f32_e32 v17, 0x45800000, v1
	v_cndmask_b32_e32 v1, v1, v17, vcc
	v_mul_f32_e32 v18, v18, v1
	v_lshlrev_b32_e32 v17, 10, v217
	v_bfe_u32 v32, v18, 16, 1
	v_add3_u32 v18, v18, v32, s90
	v_add3_u32 v17, 0, v17, v16
	v_mul_f32_e32 v2, v2, v1
	ds_write_b16_d16_hi v17, v18
	v_bfe_u32 v18, v2, 16, 1
	v_add3_u32 v2, v2, v18, s90
	ds_write_b16_d16_hi v17, v2 offset:64
	v_sub_f32_e32 v2, v34, v0
	v_mul_f32_e32 v2, v2, v1
	v_bfe_u32 v18, v2, 16, 1
	v_add3_u32 v2, v2, v18, s90
	ds_write_b16_d16_hi v17, v2 offset:128
	v_sub_f32_e32 v2, v50, v0
	v_mul_f32_e32 v2, v2, v1
	v_bfe_u32 v18, v2, 16, 1
	v_add3_u32 v2, v2, v18, s90
	ds_write_b16_d16_hi v17, v2 offset:192
	v_sub_f32_e32 v2, v98, v0
	v_mul_f32_e32 v2, v2, v1
	v_bfe_u32 v18, v2, 16, 1
	v_add3_u32 v2, v2, v18, s90
	ds_write_b16_d16_hi v17, v2 offset:256
	v_sub_f32_e32 v2, v114, v0
	v_mul_f32_e32 v2, v2, v1
	v_bfe_u32 v18, v2, 16, 1
	v_add3_u32 v2, v2, v18, s90
	ds_write_b16_d16_hi v17, v2 offset:320
	v_sub_f32_e32 v2, v82, v0
	v_mul_f32_e32 v2, v2, v1
	v_bfe_u32 v18, v2, 16, 1
	v_add3_u32 v2, v2, v18, s90
	v_sub_f32_e32 v0, v66, v0
	ds_write_b16_d16_hi v17, v2 offset:384
	v_mul_f32_e32 v2, v0, v1
	v_pk_add_f32 v[0:1], v[154:155], v[170:171]
	s_nop 0
	v_pk_mul_f32 v[0:1], v[0:1], s[26:27] op_sel_hi:[1,0]
	s_nop 0
	v_fma_f32 v1, -v0, v0, v1
	v_max_f32_e32 v1, 0, v1
; #define LAS __attribute__((address_space(3)))
; __device__ __forceinline__ bf16_t f2bf(float f) { unsigned u = __builtin_bit_cast(unsigned, f); return (bf16_t)((u + 0x7fffu + ((u >> 16) & 1u)) >> 16); }
; __device__ __forceinline__ int crow(int r, int hi) { return (r & 3) + 8 * (r >> 2) + 4 * hi; }
; __device__ __forceinline__ int crow(int r, int hi) { return (r & 3) + 8 * (r >> 2) + 4 * hi; }
; template <int DK, int DV, bool MLSTM>
; __device__ __forceinline__ void out_unit2(LAS unsigned char* lds, LAS unsigned char* ldstab, const OutArgs a, const int wv) {
;     ...
;     for (int r = 0; r < 16; ++r) {
;         const int row = 32 * rb + crow(r, hi);
;         const float t1 = s1[r] + exch[((1 - dh) * 128 + row) * 2], t2 = s2[r] + exch[((1 - dh) * 128 + row) * 2 + 1];
;         float mean, inv;
;         if (MLSTM) { mean = 0.f; inv = rsqrtf(t2 * (1.f / DV) + EPS); }
;         else { mean = t1 * (1.f / DV); inv = rsqrtf(fmaxf(t2 * (1.f / DV) - mean * mean, 0.f) + EPS); }
; #pragma unroll
;         for (int nb = 0; nb < NB; ++nb) { const int col = dh * (DV / 2) + 32 * nb + r32;
;             *(LAS bf16_t*)(lds + row * TP + col * 2) = f2bf((o[nb][r] - mean) * inv); }
	v_add_f32_e32 v1, 0x358637bd, v1
	v_mul_f32_e32 v18, 0x4b800000, v1
	v_cmp_gt_f32_e32 vcc, s89, v1
	s_nop 1
	v_cndmask_b32_e32 v1, v1, v18, vcc
	v_rsq_f32_e32 v1, v1
	v_bfe_u32 v18, v2, 16, 1
	v_add3_u32 v2, v2, v18, s90
	ds_write_b16_d16_hi v17, v2 offset:448
	v_mul_f32_e32 v2, 0x45800000, v1
	v_cndmask_b32_e32 v1, v1, v2, vcc
	v_sub_f32_e32 v17, v19, v0
	v_mul_f32_e32 v17, v17, v1
	v_lshlrev_b32_e32 v2, 10, v216
	v_bfe_u32 v18, v17, 16, 1
	v_add3_u32 v17, v17, v18, s90
	v_add3_u32 v18, 0, v2, v16
	v_sub_f32_e32 v2, v3, v0
	v_mul_f32_e32 v2, v2, v1
	v_bfe_u32 v3, v2, 16, 1
	v_add3_u32 v2, v2, v3, s90
	ds_write_b16_d16_hi v18, v2 offset:64
	v_sub_f32_e32 v2, v35, v0
	v_mul_f32_e32 v2, v2, v1
	v_bfe_u32 v3, v2, 16, 1
	v_add3_u32 v2, v2, v3, s90
	ds_write_b16_d16_hi v18, v2 offset:128
	v_sub_f32_e32 v2, v51, v0
	v_mul_f32_e32 v2, v2, v1
	v_bfe_u32 v3, v2, 16, 1
	v_add3_u32 v2, v2, v3, s90
	ds_write_b16_d16_hi v18, v2 offset:192
	v_sub_f32_e32 v2, v99, v0
	v_mul_f32_e32 v2, v2, v1
	v_bfe_u32 v3, v2, 16, 1
	v_add3_u32 v2, v2, v3, s90
	ds_write_b16_d16_hi v18, v2 offset:256
	v_sub_f32_e32 v2, v115, v0
	v_mul_f32_e32 v2, v2, v1
	v_bfe_u32 v3, v2, 16, 1
	v_add3_u32 v2, v2, v3, s90
	ds_write_b16_d16_hi v18, v2 offset:320
	v_sub_f32_e32 v2, v83, v0
	v_sub_f32_e32 v0, v67, v0
	ds_write_b16_d16_hi v18, v17
	v_mul_f32_e32 v2, v2, v1
	v_mul_f32_e32 v17, v0, v1
	v_lshlrev_b32_e32 v0, 1, v215
	v_bfe_u32 v3, v2, 16, 1
	v_subrev_u32_e32 v0, s6, v0
	v_add3_u32 v2, v2, v3, s90
	v_lshl_add_u32 v0, v0, 2, s4
	ds_write_b16_d16_hi v18, v2 offset:384
	ds_read2_b64 v[0:3], v0 offset0:128 offset1:129
	v_lshlrev_b32_e32 v19, 1, v213
	v_subrev_u32_e32 v19, s6, v19
	v_lshl_add_u32 v19, v19, 2, s4
	ds_read2_b64 v[32:35], v19 offset0:128 offset1:129
	s_waitcnt lgkmcnt(1)
	v_pk_add_f32 v[0:1], v[148:149], v[0:1]
	s_nop 0
	v_pk_mul_f32 v[0:1], v[0:1], s[26:27] op_sel_hi:[1,0]
	s_nop 0
	v_fma_f32 v1, -v0, v0, v1
	v_max_f32_e32 v1, 0, v1
	v_add_f32_e32 v1, 0x358637bd, v1
	v_mul_f32_e32 v19, 0x4b800000, v1
	v_cmp_gt_f32_e32 vcc, s89, v1
	v_sub_f32_e32 v4, v4, v0
	s_nop 0
	v_cndmask_b32_e32 v1, v1, v19, vcc
	v_rsq_f32_e32 v1, v1
	v_bfe_u32 v19, v17, 16, 1
	v_add3_u32 v17, v17, v19, s90
	ds_write_b16_d16_hi v18, v17 offset:448
	v_mul_f32_e32 v17, 0x45800000, v1
	v_cndmask_b32_e32 v1, v1, v17, vcc
	v_sub_f32_e32 v18, v20, v0
	v_mul_f32_e32 v18, v18, v1
	v_lshlrev_b32_e32 v17, 10, v215
	v_bfe_u32 v19, v18, 16, 1
	v_add3_u32 v18, v18, v19, s90
	v_add3_u32 v17, 0, v17, v16
	v_mul_f32_e32 v4, v4, v1
	ds_write_b16_d16_hi v17, v18
	v_bfe_u32 v18, v4, 16, 1
	v_add3_u32 v4, v4, v18, s90
	ds_write_b16_d16_hi v17, v4 offset:64
	v_sub_f32_e32 v4, v36, v0
	v_mul_f32_e32 v4, v4, v1
	v_bfe_u32 v18, v4, 16, 1
	v_add3_u32 v4, v4, v18, s90
	ds_write_b16_d16_hi v17, v4 offset:128
	v_sub_f32_e32 v4, v52, v0
	v_mul_f32_e32 v4, v4, v1
	v_bfe_u32 v18, v4, 16, 1
	v_add3_u32 v4, v4, v18, s90
	ds_write_b16_d16_hi v17, v4 offset:192
	v_sub_f32_e32 v4, v100, v0
	v_mul_f32_e32 v4, v4, v1
	v_bfe_u32 v18, v4, 16, 1
	v_add3_u32 v4, v4, v18, s90
	ds_write_b16_d16_hi v17, v4 offset:256
	v_sub_f32_e32 v4, v116, v0
	v_mul_f32_e32 v4, v4, v1
	v_bfe_u32 v18, v4, 16, 1
	v_add3_u32 v4, v4, v18, s90
	ds_write_b16_d16_hi v17, v4 offset:320
	v_sub_f32_e32 v4, v84, v0
	v_mul_f32_e32 v4, v4, v1
	v_bfe_u32 v18, v4, 16, 1
	v_add3_u32 v4, v4, v18, s90
	v_sub_f32_e32 v0, v68, v0
	ds_write_b16_d16_hi v17, v4 offset:384
	v_mul_f32_e32 v4, v0, v1
	v_pk_add_f32 v[0:1], v[150:151], v[2:3]
	s_nop 0
	v_pk_mul_f32 v[0:1], v[0:1], s[26:27] op_sel_hi:[1,0]
	s_nop 0
	v_fma_f32 v1, -v0, v0, v1
	v_max_f32_e32 v1, 0, v1
	v_add_f32_e32 v1, 0x358637bd, v1
	v_mul_f32_e32 v2, 0x4b800000, v1
	v_cmp_gt_f32_e32 vcc, s89, v1
	v_sub_f32_e32 v3, v21, v0
	s_nop 0
	v_cndmask_b32_e32 v1, v1, v2, vcc
	v_rsq_f32_e32 v1, v1
	v_bfe_u32 v2, v4, 16, 1
	v_add3_u32 v2, v4, v2, s90
	ds_write_b16_d16_hi v17, v2 offset:448
	v_mul_f32_e32 v2, 0x45800000, v1
	v_cndmask_b32_e32 v1, v1, v2, vcc
	v_mul_f32_e32 v3, v3, v1
	v_lshlrev_b32_e32 v2, 10, v214
	v_bfe_u32 v4, v3, 16, 1
	v_add3_u32 v3, v3, v4, s90
	v_add3_u32 v2, 0, v2, v16
	ds_write_b16_d16_hi v2, v3
	v_sub_f32_e32 v3, v5, v0
	v_mul_f32_e32 v3, v3, v1
	v_bfe_u32 v4, v3, 16, 1
	v_add3_u32 v3, v3, v4, s90
	ds_write_b16_d16_hi v2, v3 offset:64
	v_sub_f32_e32 v3, v37, v0
	v_mul_f32_e32 v3, v3, v1
	v_bfe_u32 v4, v3, 16, 1
	v_add3_u32 v3, v3, v4, s90
	ds_write_b16_d16_hi v2, v3 offset:128
	v_sub_f32_e32 v3, v53, v0
	v_mul_f32_e32 v3, v3, v1
	v_bfe_u32 v4, v3, 16, 1
	v_add3_u32 v3, v3, v4, s90
	ds_write_b16_d16_hi v2, v3 offset:192
	v_sub_f32_e32 v3, v101, v0
	v_mul_f32_e32 v3, v3, v1
	v_bfe_u32 v4, v3, 16, 1
	v_add3_u32 v3, v3, v4, s90
	ds_write_b16_d16_hi v2, v3 offset:256
	v_sub_f32_e32 v3, v117, v0
	v_mul_f32_e32 v3, v3, v1
	v_bfe_u32 v4, v3, 16, 1
	v_add3_u32 v3, v3, v4, s90
	ds_write_b16_d16_hi v2, v3 offset:320
	v_sub_f32_e32 v3, v85, v0
	v_mul_f32_e32 v3, v3, v1
	v_bfe_u32 v4, v3, 16, 1
	v_add3_u32 v3, v3, v4, s90
	v_sub_f32_e32 v0, v69, v0
	ds_write_b16_d16_hi v2, v3 offset:384
	v_mul_f32_e32 v3, v0, v1
	s_waitcnt lgkmcnt(14)
; #define LAS __attribute__((address_space(3)))
; __device__ __forceinline__ bf16_t f2bf(float f) { unsigned u = __builtin_bit_cast(unsigned, f); return (bf16_t)((u + 0x7fffu + ((u >> 16) & 1u)) >> 16); }
; __device__ __forceinline__ int crow(int r, int hi) { return (r & 3) + 8 * (r >> 2) + 4 * hi; }
; __device__ __forceinline__ int crow(int r, int hi) { return (r & 3) + 8 * (r >> 2) + 4 * hi; }
; template <int DK, int DV, bool MLSTM>
; __device__ __forceinline__ void out_unit2(LAS unsigned char* lds, LAS unsigned char* ldstab, const OutArgs a, const int wv) {
;     ...
;     for (int r = 0; r < 16; ++r) {
;         const int row = 32 * rb + crow(r, hi);
;         const float t1 = s1[r] + exch[((1 - dh) * 128 + row) * 2], t2 = s2[r] + exch[((1 - dh) * 128 + row) * 2 + 1];
;         float mean, inv;
;         if (MLSTM) { mean = 0.f; inv = rsqrtf(t2 * (1.f / DV) + EPS); }
;         else { mean = t1 * (1.f / DV); inv = rsqrtf(fmaxf(t2 * (1.f / DV) - mean * mean, 0.f) + EPS); }
; #pragma unroll
;         for (int nb = 0; nb < NB; ++nb) { const int col = dh * (DV / 2) + 32 * nb + r32;
;             *(LAS bf16_t*)(lds + row * TP + col * 2) = f2bf((o[nb][r] - mean) * inv); }
	v_pk_add_f32 v[0:1], v[144:145], v[32:33]
	s_nop 0
	v_pk_mul_f32 v[0:1], v[0:1], s[26:27] op_sel_hi:[1,0]
	s_nop 0
	v_fma_f32 v1, -v0, v0, v1
	v_max_f32_e32 v1, 0, v1
	v_add_f32_e32 v1, 0x358637bd, v1
	v_mul_f32_e32 v4, 0x4b800000, v1
	v_cmp_gt_f32_e32 vcc, s89, v1
	s_nop 1
	v_cndmask_b32_e32 v1, v1, v4, vcc
	v_rsq_f32_e32 v1, v1
	v_bfe_u32 v4, v3, 16, 1
	v_add3_u32 v3, v3, v4, s90
	ds_write_b16_d16_hi v2, v3 offset:448
	v_mul_f32_e32 v2, 0x45800000, v1
	v_cndmask_b32_e32 v1, v1, v2, vcc
	v_sub_f32_e32 v3, v22, v0
	v_mul_f32_e32 v3, v3, v1
	v_lshlrev_b32_e32 v2, 10, v213
	v_bfe_u32 v4, v3, 16, 1
	v_add3_u32 v3, v3, v4, s90
	v_add3_u32 v2, 0, v2, v16
	ds_write_b16_d16_hi v2, v3
	v_sub_f32_e32 v3, v6, v0
	v_mul_f32_e32 v3, v3, v1
	v_bfe_u32 v4, v3, 16, 1
	v_add3_u32 v3, v3, v4, s90
	ds_write_b16_d16_hi v2, v3 offset:64
	v_sub_f32_e32 v3, v38, v0
	v_mul_f32_e32 v3, v3, v1
	v_bfe_u32 v4, v3, 16, 1
	v_add3_u32 v3, v3, v4, s90
	ds_write_b16_d16_hi v2, v3 offset:128
	v_sub_f32_e32 v3, v54, v0
	v_mul_f32_e32 v3, v3, v1
	v_bfe_u32 v4, v3, 16, 1
	v_add3_u32 v3, v3, v4, s90
	ds_write_b16_d16_hi v2, v3 offset:192
	v_sub_f32_e32 v3, v102, v0
	v_mul_f32_e32 v3, v3, v1
	v_bfe_u32 v4, v3, 16, 1
	v_add3_u32 v3, v3, v4, s90
	ds_write_b16_d16_hi v2, v3 offset:256
	v_sub_f32_e32 v3, v118, v0
	v_mul_f32_e32 v3, v3, v1
	v_bfe_u32 v4, v3, 16, 1
	v_add3_u32 v3, v3, v4, s90
	ds_write_b16_d16_hi v2, v3 offset:320
	v_sub_f32_e32 v3, v86, v0
	v_mul_f32_e32 v3, v3, v1
	v_bfe_u32 v4, v3, 16, 1
	v_add3_u32 v3, v3, v4, s90
	v_sub_f32_e32 v0, v70, v0
	ds_write_b16_d16_hi v2, v3 offset:384
	v_mul_f32_e32 v3, v0, v1
	v_pk_add_f32 v[0:1], v[146:147], v[34:35]
	s_nop 0
	v_pk_mul_f32 v[0:1], v[0:1], s[26:27] op_sel_hi:[1,0]
	s_nop 0
	v_fma_f32 v1, -v0, v0, v1
	v_max_f32_e32 v1, 0, v1
	v_add_f32_e32 v1, 0x358637bd, v1
	v_mul_f32_e32 v4, 0x4b800000, v1
	v_cmp_gt_f32_e32 vcc, s89, v1
	s_nop 1
	v_cndmask_b32_e32 v1, v1, v4, vcc
	v_rsq_f32_e32 v1, v1
	v_bfe_u32 v4, v3, 16, 1
	v_add3_u32 v3, v3, v4, s90
	ds_write_b16_d16_hi v2, v3 offset:448
	v_mul_f32_e32 v2, 0x45800000, v1
	v_cndmask_b32_e32 v1, v1, v2, vcc
	v_sub_f32_e32 v3, v23, v0
	v_lshlrev_b32_e32 v2, 10, v212
	v_mul_f32_e32 v3, v3, v1
	v_bfe_u32 v4, v3, 16, 1
	v_add3_u32 v17, 0, v2, v16
	v_sub_f32_e32 v2, v7, v0
	v_add3_u32 v3, v3, v4, s90
	v_mul_f32_e32 v2, v2, v1
	ds_write_b16_d16_hi v17, v3
	v_bfe_u32 v3, v2, 16, 1
	v_add3_u32 v2, v2, v3, s90
	ds_write_b16_d16_hi v17, v2 offset:64
	v_sub_f32_e32 v2, v39, v0
	v_mul_f32_e32 v2, v2, v1
	v_bfe_u32 v3, v2, 16, 1
	v_add3_u32 v2, v2, v3, s90
	ds_write_b16_d16_hi v17, v2 offset:128
	v_sub_f32_e32 v2, v55, v0
	v_mul_f32_e32 v2, v2, v1
	v_bfe_u32 v3, v2, 16, 1
	v_add3_u32 v2, v2, v3, s90
	ds_write_b16_d16_hi v17, v2 offset:192
	v_sub_f32_e32 v2, v103, v0
	v_mul_f32_e32 v2, v2, v1
	v_bfe_u32 v3, v2, 16, 1
	v_add3_u32 v2, v2, v3, s90
	ds_write_b16_d16_hi v17, v2 offset:256
	v_sub_f32_e32 v2, v119, v0
	v_mul_f32_e32 v2, v2, v1
	v_bfe_u32 v3, v2, 16, 1
	v_add3_u32 v2, v2, v3, s90
	ds_write_b16_d16_hi v17, v2 offset:320
	v_sub_f32_e32 v2, v87, v0
	v_sub_f32_e32 v0, v71, v0
	v_mul_f32_e32 v2, v2, v1
	v_mul_f32_e32 v18, v0, v1
	v_lshlrev_b32_e32 v0, 1, v211
	v_bfe_u32 v3, v2, 16, 1
	v_subrev_u32_e32 v0, s6, v0
	v_add3_u32 v2, v2, v3, s90
	v_lshl_add_u32 v0, v0, 2, s4
	ds_write_b16_d16_hi v17, v2 offset:384
	ds_read2_b64 v[0:3], v0 offset0:128 offset1:129
	v_lshlrev_b32_e32 v4, 1, v209
	v_subrev_u32_e32 v4, s6, v4
	v_lshl_add_u32 v4, v4, 2, s4
	ds_read2_b64 v[4:7], v4 offset0:128 offset1:129
	s_waitcnt lgkmcnt(1)
	v_pk_add_f32 v[0:1], v[140:141], v[0:1]
	s_nop 0
	v_pk_mul_f32 v[0:1], v[0:1], s[26:27] op_sel_hi:[1,0]
	s_nop 0
	v_fma_f32 v1, -v0, v0, v1
	v_max_f32_e32 v1, 0, v1
	v_add_f32_e32 v1, 0x358637bd, v1
	v_mul_f32_e32 v19, 0x4b800000, v1
	v_cmp_gt_f32_e32 vcc, s89, v1
	v_sub_f32_e32 v8, v8, v0
	s_nop 0
	v_cndmask_b32_e32 v1, v1, v19, vcc
	v_rsq_f32_e32 v1, v1
	v_bfe_u32 v19, v18, 16, 1
	v_add3_u32 v18, v18, v19, s90
	ds_write_b16_d16_hi v17, v18 offset:448
	v_mul_f32_e32 v17, 0x45800000, v1
	v_cndmask_b32_e32 v1, v1, v17, vcc
	v_sub_f32_e32 v18, v24, v0
	v_mul_f32_e32 v18, v18, v1
	v_lshlrev_b32_e32 v17, 10, v211
	v_bfe_u32 v19, v18, 16, 1
	v_add3_u32 v18, v18, v19, s90
	v_add3_u32 v17, 0, v17, v16
	v_mul_f32_e32 v8, v8, v1
	ds_write_b16_d16_hi v17, v18
	v_bfe_u32 v18, v8, 16, 1
	v_add3_u32 v8, v8, v18, s90
	ds_write_b16_d16_hi v17, v8 offset:64
	v_sub_f32_e32 v8, v40, v0
	v_mul_f32_e32 v8, v8, v1
	v_bfe_u32 v18, v8, 16, 1
	v_add3_u32 v8, v8, v18, s90
	ds_write_b16_d16_hi v17, v8 offset:128
	v_sub_f32_e32 v8, v56, v0
	v_mul_f32_e32 v8, v8, v1
	v_bfe_u32 v18, v8, 16, 1
	v_add3_u32 v8, v8, v18, s90
	ds_write_b16_d16_hi v17, v8 offset:192
	v_sub_f32_e32 v8, v104, v0
	v_mul_f32_e32 v8, v8, v1
	v_bfe_u32 v18, v8, 16, 1
	v_add3_u32 v8, v8, v18, s90
	ds_write_b16_d16_hi v17, v8 offset:256
	v_sub_f32_e32 v8, v120, v0
	v_mul_f32_e32 v8, v8, v1
	v_bfe_u32 v18, v8, 16, 1
	v_add3_u32 v8, v8, v18, s90
	ds_write_b16_d16_hi v17, v8 offset:320
	v_sub_f32_e32 v8, v88, v0
	v_mul_f32_e32 v8, v8, v1
	v_bfe_u32 v18, v8, 16, 1
	v_add3_u32 v8, v8, v18, s90
	v_sub_f32_e32 v0, v72, v0
	ds_write_b16_d16_hi v17, v8 offset:384
	v_mul_f32_e32 v8, v0, v1
	v_pk_add_f32 v[0:1], v[142:143], v[2:3]
	s_nop 0
	v_pk_mul_f32 v[0:1], v[0:1], s[26:27] op_sel_hi:[1,0]
	s_nop 0
	v_fma_f32 v1, -v0, v0, v1
	v_max_f32_e32 v1, 0, v1
	v_add_f32_e32 v1, 0x358637bd, v1
	v_mul_f32_e32 v2, 0x4b800000, v1
	v_cmp_gt_f32_e32 vcc, s89, v1
	v_sub_f32_e32 v3, v25, v0
	s_nop 0
	v_cndmask_b32_e32 v1, v1, v2, vcc
	v_rsq_f32_e32 v1, v1
	v_bfe_u32 v2, v8, 16, 1
	v_add3_u32 v2, v8, v2, s90
	ds_write_b16_d16_hi v17, v2 offset:448
	v_mul_f32_e32 v2, 0x45800000, v1
	v_cndmask_b32_e32 v1, v1, v2, vcc
	v_mul_f32_e32 v3, v3, v1
	v_lshlrev_b32_e32 v2, 10, v210
	v_bfe_u32 v8, v3, 16, 1
	v_add3_u32 v3, v3, v8, s90
	v_add3_u32 v2, 0, v2, v16
	ds_write_b16_d16_hi v2, v3
	v_sub_f32_e32 v3, v9, v0
	v_mul_f32_e32 v3, v3, v1
	v_bfe_u32 v8, v3, 16, 1
	v_add3_u32 v3, v3, v8, s90
	ds_write_b16_d16_hi v2, v3 offset:64
	v_sub_f32_e32 v3, v41, v0
	v_mul_f32_e32 v3, v3, v1
	v_bfe_u32 v8, v3, 16, 1
	v_add3_u32 v3, v3, v8, s90
	ds_write_b16_d16_hi v2, v3 offset:128
	v_sub_f32_e32 v3, v57, v0
	v_mul_f32_e32 v3, v3, v1
	v_bfe_u32 v8, v3, 16, 1
	v_add3_u32 v3, v3, v8, s90
	ds_write_b16_d16_hi v2, v3 offset:192
	v_sub_f32_e32 v3, v105, v0
	v_mul_f32_e32 v3, v3, v1
	v_bfe_u32 v8, v3, 16, 1
	v_add3_u32 v3, v3, v8, s90
	ds_write_b16_d16_hi v2, v3 offset:256
	v_sub_f32_e32 v3, v121, v0
	v_mul_f32_e32 v3, v3, v1
	v_bfe_u32 v8, v3, 16, 1
	v_add3_u32 v3, v3, v8, s90
	ds_write_b16_d16_hi v2, v3 offset:320
	v_sub_f32_e32 v3, v89, v0
	v_mul_f32_e32 v3, v3, v1
	v_bfe_u32 v8, v3, 16, 1
	v_add3_u32 v3, v3, v8, s90
	v_sub_f32_e32 v0, v73, v0
	ds_write_b16_d16_hi v2, v3 offset:384
	v_mul_f32_e32 v3, v0, v1
	s_waitcnt lgkmcnt(14)
; #define LAS __attribute__((address_space(3)))
; __device__ __forceinline__ bf16_t f2bf(float f) { unsigned u = __builtin_bit_cast(unsigned, f); return (bf16_t)((u + 0x7fffu + ((u >> 16) & 1u)) >> 16); }
; __device__ __forceinline__ int crow(int r, int hi) { return (r & 3) + 8 * (r >> 2) + 4 * hi; }
; __device__ __forceinline__ int crow(int r, int hi) { return (r & 3) + 8 * (r >> 2) + 4 * hi; }
; template <int DK, int DV, bool MLSTM>
; __device__ __forceinline__ void out_unit2(LAS unsigned char* lds, LAS unsigned char* ldstab, const OutArgs a, const int wv) {
;     ...
;     for (int r = 0; r < 16; ++r) {
;         const int row = 32 * rb + crow(r, hi);
;         const float t1 = s1[r] + exch[((1 - dh) * 128 + row) * 2], t2 = s2[r] + exch[((1 - dh) * 128 + row) * 2 + 1];
;         float mean, inv;
;         if (MLSTM) { mean = 0.f; inv = rsqrtf(t2 * (1.f / DV) + EPS); }
;         else { mean = t1 * (1.f / DV); inv = rsqrtf(fmaxf(t2 * (1.f / DV) - mean * mean, 0.f) + EPS); }
; #pragma unroll
;         for (int nb = 0; nb < NB; ++nb) { const int col = dh * (DV / 2) + 32 * nb + r32;
;             *(LAS bf16_t*)(lds + row * TP + col * 2) = f2bf((o[nb][r] - mean) * inv); }
	v_pk_add_f32 v[0:1], v[136:137], v[4:5]
	s_nop 0
	v_pk_mul_f32 v[0:1], v[0:1], s[26:27] op_sel_hi:[1,0]
	s_nop 0
	v_fma_f32 v1, -v0, v0, v1
	v_max_f32_e32 v1, 0, v1
	v_add_f32_e32 v1, 0x358637bd, v1
	v_mul_f32_e32 v4, 0x4b800000, v1
	v_cmp_gt_f32_e32 vcc, s89, v1
	s_nop 1
	v_cndmask_b32_e32 v1, v1, v4, vcc
	v_rsq_f32_e32 v1, v1
	v_bfe_u32 v4, v3, 16, 1
	v_add3_u32 v3, v3, v4, s90
	ds_write_b16_d16_hi v2, v3 offset:448
	v_mul_f32_e32 v2, 0x45800000, v1
	v_cndmask_b32_e32 v1, v1, v2, vcc
	v_sub_f32_e32 v3, v26, v0
	v_mul_f32_e32 v3, v3, v1
	v_lshlrev_b32_e32 v2, 10, v209
	v_bfe_u32 v4, v3, 16, 1
	v_add3_u32 v3, v3, v4, s90
	v_add3_u32 v2, 0, v2, v16
	ds_write_b16_d16_hi v2, v3
	v_sub_f32_e32 v3, v10, v0
	v_mul_f32_e32 v3, v3, v1
	v_bfe_u32 v4, v3, 16, 1
	v_add3_u32 v3, v3, v4, s90
	ds_write_b16_d16_hi v2, v3 offset:64
	v_sub_f32_e32 v3, v42, v0
	v_mul_f32_e32 v3, v3, v1
	v_bfe_u32 v4, v3, 16, 1
	v_add3_u32 v3, v3, v4, s90
	ds_write_b16_d16_hi v2, v3 offset:128
	v_sub_f32_e32 v3, v58, v0
	v_mul_f32_e32 v3, v3, v1
	v_bfe_u32 v4, v3, 16, 1
	v_add3_u32 v3, v3, v4, s90
	ds_write_b16_d16_hi v2, v3 offset:192
	v_sub_f32_e32 v3, v106, v0
	v_mul_f32_e32 v3, v3, v1
	v_bfe_u32 v4, v3, 16, 1
	v_add3_u32 v3, v3, v4, s90
	ds_write_b16_d16_hi v2, v3 offset:256
	v_sub_f32_e32 v3, v122, v0
	v_mul_f32_e32 v3, v3, v1
	v_bfe_u32 v4, v3, 16, 1
	v_add3_u32 v3, v3, v4, s90
	ds_write_b16_d16_hi v2, v3 offset:320
	v_sub_f32_e32 v3, v90, v0
	v_mul_f32_e32 v3, v3, v1
	v_bfe_u32 v4, v3, 16, 1
	v_add3_u32 v3, v3, v4, s90
	v_sub_f32_e32 v0, v74, v0
	ds_write_b16_d16_hi v2, v3 offset:384
	v_mul_f32_e32 v3, v0, v1
	v_pk_add_f32 v[0:1], v[138:139], v[6:7]
	s_nop 0
	v_pk_mul_f32 v[0:1], v[0:1], s[26:27] op_sel_hi:[1,0]
	s_nop 0
	v_fma_f32 v1, -v0, v0, v1
	v_max_f32_e32 v1, 0, v1
	v_add_f32_e32 v1, 0x358637bd, v1
	v_mul_f32_e32 v4, 0x4b800000, v1
	v_cmp_gt_f32_e32 vcc, s89, v1
	s_nop 1
	v_cndmask_b32_e32 v1, v1, v4, vcc
	v_rsq_f32_e32 v1, v1
	v_bfe_u32 v4, v3, 16, 1
	v_add3_u32 v3, v3, v4, s90
	ds_write_b16_d16_hi v2, v3 offset:448
	v_mul_f32_e32 v2, 0x45800000, v1
	v_cndmask_b32_e32 v1, v1, v2, vcc
	v_sub_f32_e32 v3, v27, v0
	v_lshlrev_b32_e32 v2, 10, v208
	v_mul_f32_e32 v3, v3, v1
	v_bfe_u32 v4, v3, 16, 1
	v_add3_u32 v8, 0, v2, v16
	v_sub_f32_e32 v2, v11, v0
	v_add3_u32 v3, v3, v4, s90
	v_mul_f32_e32 v2, v2, v1
	ds_write_b16_d16_hi v8, v3
	v_bfe_u32 v3, v2, 16, 1
	v_add3_u32 v2, v2, v3, s90
	ds_write_b16_d16_hi v8, v2 offset:64
	v_sub_f32_e32 v2, v43, v0
	v_mul_f32_e32 v2, v2, v1
	v_bfe_u32 v3, v2, 16, 1
	v_add3_u32 v2, v2, v3, s90
	ds_write_b16_d16_hi v8, v2 offset:128
	v_sub_f32_e32 v2, v59, v0
	v_mul_f32_e32 v2, v2, v1
	v_bfe_u32 v3, v2, 16, 1
	v_add3_u32 v2, v2, v3, s90
	ds_write_b16_d16_hi v8, v2 offset:192
	v_sub_f32_e32 v2, v107, v0
	v_mul_f32_e32 v2, v2, v1
	v_bfe_u32 v3, v2, 16, 1
	v_add3_u32 v2, v2, v3, s90
	ds_write_b16_d16_hi v8, v2 offset:256
	v_sub_f32_e32 v2, v123, v0
	v_mul_f32_e32 v2, v2, v1
	v_bfe_u32 v3, v2, 16, 1
	v_add3_u32 v2, v2, v3, s90
	ds_write_b16_d16_hi v8, v2 offset:320
	v_sub_f32_e32 v2, v91, v0
	v_sub_f32_e32 v0, v75, v0
	v_mul_f32_e32 v2, v2, v1
	v_mul_f32_e32 v9, v0, v1
	v_lshlrev_b32_e32 v0, 1, v207
	v_bfe_u32 v3, v2, 16, 1
	v_subrev_u32_e32 v0, s6, v0
	v_add3_u32 v2, v2, v3, s90
	v_lshl_add_u32 v0, v0, 2, s4
	ds_write_b16_d16_hi v8, v2 offset:384
	ds_read2_b64 v[0:3], v0 offset0:128 offset1:129
	v_lshlrev_b32_e32 v4, 1, v162
	v_subrev_u32_e32 v4, s6, v4
	v_lshl_add_u32 v4, v4, 2, s4
	ds_read2_b64 v[4:7], v4 offset0:128 offset1:129
	s_waitcnt lgkmcnt(1)
	v_pk_add_f32 v[0:1], v[132:133], v[0:1]
	s_nop 0
	v_pk_mul_f32 v[0:1], v[0:1], s[26:27] op_sel_hi:[1,0]
	s_nop 0
	v_fma_f32 v1, -v0, v0, v1
	v_max_f32_e32 v1, 0, v1
	v_add_f32_e32 v1, 0x358637bd, v1
	v_mul_f32_e32 v10, 0x4b800000, v1
	v_cmp_gt_f32_e32 vcc, s89, v1
	s_nop 1
	v_cndmask_b32_e32 v1, v1, v10, vcc
	v_rsq_f32_e32 v1, v1
	v_bfe_u32 v10, v9, 16, 1
	v_add3_u32 v9, v9, v10, s90
	ds_write_b16_d16_hi v8, v9 offset:448
	v_mul_f32_e32 v8, 0x45800000, v1
	v_cndmask_b32_e32 v1, v1, v8, vcc
	v_sub_f32_e32 v9, v28, v0
	v_mul_f32_e32 v9, v9, v1
	v_lshlrev_b32_e32 v8, 10, v207
	v_bfe_u32 v10, v9, 16, 1
	v_add3_u32 v9, v9, v10, s90
	v_add3_u32 v8, 0, v8, v16
	ds_write_b16_d16_hi v8, v9
	v_sub_f32_e32 v9, v12, v0
	v_mul_f32_e32 v9, v9, v1
	v_bfe_u32 v10, v9, 16, 1
	v_add3_u32 v9, v9, v10, s90
	ds_write_b16_d16_hi v8, v9 offset:64
	v_sub_f32_e32 v9, v44, v0
	v_mul_f32_e32 v9, v9, v1
	v_bfe_u32 v10, v9, 16, 1
	v_add3_u32 v9, v9, v10, s90
	ds_write_b16_d16_hi v8, v9 offset:128
	v_sub_f32_e32 v9, v60, v0
	v_mul_f32_e32 v9, v9, v1
	v_bfe_u32 v10, v9, 16, 1
	v_add3_u32 v9, v9, v10, s90
	ds_write_b16_d16_hi v8, v9 offset:192
	v_sub_f32_e32 v9, v108, v0
	v_mul_f32_e32 v9, v9, v1
	v_bfe_u32 v10, v9, 16, 1
	v_add3_u32 v9, v9, v10, s90
	ds_write_b16_d16_hi v8, v9 offset:256
	v_sub_f32_e32 v9, v124, v0
	v_mul_f32_e32 v9, v9, v1
	v_bfe_u32 v10, v9, 16, 1
	v_add3_u32 v9, v9, v10, s90
	ds_write_b16_d16_hi v8, v9 offset:320
	v_sub_f32_e32 v9, v92, v0
	v_mul_f32_e32 v9, v9, v1
	v_bfe_u32 v10, v9, 16, 1
	v_add3_u32 v9, v9, v10, s90
	v_sub_f32_e32 v0, v76, v0
	ds_write_b16_d16_hi v8, v9 offset:384
	v_mul_f32_e32 v9, v0, v1
	v_pk_add_f32 v[0:1], v[134:135], v[2:3]
	s_nop 0
	v_pk_mul_f32 v[0:1], v[0:1], s[26:27] op_sel_hi:[1,0]
	s_nop 0
	v_fma_f32 v1, -v0, v0, v1
	v_max_f32_e32 v1, 0, v1
	v_add_f32_e32 v1, 0x358637bd, v1
	v_mul_f32_e32 v2, 0x4b800000, v1
	v_cmp_gt_f32_e32 vcc, s89, v1
	v_sub_f32_e32 v3, v29, v0
	s_nop 0
	v_cndmask_b32_e32 v1, v1, v2, vcc
	v_rsq_f32_e32 v1, v1
	v_bfe_u32 v2, v9, 16, 1
	v_add3_u32 v2, v9, v2, s90
	ds_write_b16_d16_hi v8, v2 offset:448
	v_mul_f32_e32 v2, 0x45800000, v1
	v_cndmask_b32_e32 v1, v1, v2, vcc
	v_mul_f32_e32 v3, v3, v1
	v_lshlrev_b32_e32 v2, 10, v206
	v_bfe_u32 v8, v3, 16, 1
	v_add3_u32 v3, v3, v8, s90
	v_add3_u32 v2, 0, v2, v16
	ds_write_b16_d16_hi v2, v3
	v_sub_f32_e32 v3, v13, v0
	v_mul_f32_e32 v3, v3, v1
	v_bfe_u32 v8, v3, 16, 1
	v_add3_u32 v3, v3, v8, s90
	ds_write_b16_d16_hi v2, v3 offset:64
	v_sub_f32_e32 v3, v45, v0
	v_mul_f32_e32 v3, v3, v1
	v_bfe_u32 v8, v3, 16, 1
	v_add3_u32 v3, v3, v8, s90
	ds_write_b16_d16_hi v2, v3 offset:128
	v_sub_f32_e32 v3, v61, v0
	v_mul_f32_e32 v3, v3, v1
	v_bfe_u32 v8, v3, 16, 1
	v_add3_u32 v3, v3, v8, s90
	ds_write_b16_d16_hi v2, v3 offset:192
	v_sub_f32_e32 v3, v109, v0
	v_mul_f32_e32 v3, v3, v1
	v_bfe_u32 v8, v3, 16, 1
	v_add3_u32 v3, v3, v8, s90
	ds_write_b16_d16_hi v2, v3 offset:256
	v_sub_f32_e32 v3, v125, v0
	v_mul_f32_e32 v3, v3, v1
	v_bfe_u32 v8, v3, 16, 1
	v_add3_u32 v3, v3, v8, s90
	ds_write_b16_d16_hi v2, v3 offset:320
	v_sub_f32_e32 v3, v93, v0
	v_mul_f32_e32 v3, v3, v1
	v_bfe_u32 v8, v3, 16, 1
	v_add3_u32 v3, v3, v8, s90
	v_sub_f32_e32 v0, v77, v0
	ds_write_b16_d16_hi v2, v3 offset:384
	v_mul_f32_e32 v3, v0, v1
	s_waitcnt lgkmcnt(14)
; #define LAS __attribute__((address_space(3)))
; __device__ __forceinline__ bf16_t f2bf(float f) { unsigned u = __builtin_bit_cast(unsigned, f); return (bf16_t)((u + 0x7fffu + ((u >> 16) & 1u)) >> 16); }
; __device__ __forceinline__ int crow(int r, int hi) { return (r & 3) + 8 * (r >> 2) + 4 * hi; }
; __device__ __forceinline__ int crow(int r, int hi) { return (r & 3) + 8 * (r >> 2) + 4 * hi; }
; template <int DK, int DV, bool MLSTM>
; __device__ __forceinline__ void out_unit2(LAS unsigned char* lds, LAS unsigned char* ldstab, const OutArgs a, const int wv) {
;     ...
;     for (int r = 0; r < 16; ++r) {
;         const int row = 32 * rb + crow(r, hi);
;         const float t1 = s1[r] + exch[((1 - dh) * 128 + row) * 2], t2 = s2[r] + exch[((1 - dh) * 128 + row) * 2 + 1];
;         float mean, inv;
;         if (MLSTM) { mean = 0.f; inv = rsqrtf(t2 * (1.f / DV) + EPS); }
;         else { mean = t1 * (1.f / DV); inv = rsqrtf(fmaxf(t2 * (1.f / DV) - mean * mean, 0.f) + EPS); }
; #pragma unroll
;         for (int nb = 0; nb < NB; ++nb) { const int col = dh * (DV / 2) + 32 * nb + r32;
;             *(LAS bf16_t*)(lds + row * TP + col * 2) = f2bf((o[nb][r] - mean) * inv); }
;     }
;     __syncthreads();
;     constexpr int CPR = DV / 8;
; #pragma unroll 1
;     for (int id = tid; id < 128 * CPR; id += 512) { const int row = id / CPR, ch = id % CPR;
;         const u32x4 y = *(const LAS u32x4*)(lds + row * TP + ch * 16);
;         const f32x4 g0 = *(const f32x4*)(a.gain + 8 * ch), g1 = *(const f32x4*)(a.gain + 8 * ch + 4);
	v_pk_add_f32 v[0:1], v[128:129], v[4:5]
	s_nop 0
	v_pk_mul_f32 v[0:1], v[0:1], s[26:27] op_sel_hi:[1,0]
	s_nop 0
	v_fma_f32 v1, -v0, v0, v1
	v_max_f32_e32 v1, 0, v1
	v_add_f32_e32 v1, 0x358637bd, v1
	v_mul_f32_e32 v4, 0x4b800000, v1
	v_cmp_gt_f32_e32 vcc, s89, v1
	s_nop 1
	v_cndmask_b32_e32 v1, v1, v4, vcc
	v_rsq_f32_e32 v1, v1
	v_bfe_u32 v4, v3, 16, 1
	v_add3_u32 v3, v3, v4, s90
	ds_write_b16_d16_hi v2, v3 offset:448
	v_mul_f32_e32 v2, 0x45800000, v1
	v_cndmask_b32_e32 v1, v1, v2, vcc
	v_sub_f32_e32 v3, v30, v0
	v_mul_f32_e32 v3, v3, v1
	v_lshlrev_b32_e32 v2, 10, v162
	v_bfe_u32 v4, v3, 16, 1
	v_add3_u32 v3, v3, v4, s90
	v_add3_u32 v2, 0, v2, v16
	ds_write_b16_d16_hi v2, v3
	v_sub_f32_e32 v3, v14, v0
	v_mul_f32_e32 v3, v3, v1
	v_bfe_u32 v4, v3, 16, 1
	v_add3_u32 v3, v3, v4, s90
	ds_write_b16_d16_hi v2, v3 offset:64
	v_sub_f32_e32 v3, v46, v0
	v_mul_f32_e32 v3, v3, v1
	v_bfe_u32 v4, v3, 16, 1
	v_add3_u32 v3, v3, v4, s90
	ds_write_b16_d16_hi v2, v3 offset:128
	v_sub_f32_e32 v3, v62, v0
	v_mul_f32_e32 v3, v3, v1
	v_bfe_u32 v4, v3, 16, 1
	v_add3_u32 v3, v3, v4, s90
	ds_write_b16_d16_hi v2, v3 offset:192
	v_sub_f32_e32 v3, v110, v0
	v_mul_f32_e32 v3, v3, v1
	v_bfe_u32 v4, v3, 16, 1
	v_add3_u32 v3, v3, v4, s90
	ds_write_b16_d16_hi v2, v3 offset:256
	v_sub_f32_e32 v3, v126, v0
	v_mul_f32_e32 v3, v3, v1
	v_bfe_u32 v4, v3, 16, 1
	v_add3_u32 v3, v3, v4, s90
	ds_write_b16_d16_hi v2, v3 offset:320
	v_sub_f32_e32 v3, v94, v0
	v_mul_f32_e32 v3, v3, v1
	v_bfe_u32 v4, v3, 16, 1
	v_add3_u32 v3, v3, v4, s90
	v_sub_f32_e32 v0, v78, v0
	ds_write_b16_d16_hi v2, v3 offset:384
	v_mul_f32_e32 v3, v0, v1
	v_pk_add_f32 v[0:1], v[130:131], v[6:7]
	s_nop 0
	v_pk_mul_f32 v[0:1], v[0:1], s[26:27] op_sel_hi:[1,0]
	s_nop 0
	v_fma_f32 v1, -v0, v0, v1
	v_max_f32_e32 v1, 0, v1
	v_add_f32_e32 v1, 0x358637bd, v1
	v_mul_f32_e32 v4, 0x4b800000, v1
	v_cmp_gt_f32_e32 vcc, s89, v1
	s_nop 1
	v_cndmask_b32_e32 v1, v1, v4, vcc
	v_rsq_f32_e32 v1, v1
	v_bfe_u32 v4, v3, 16, 1
	v_add3_u32 v3, v3, v4, s90
	ds_write_b16_d16_hi v2, v3 offset:448
	v_mul_f32_e32 v2, 0x45800000, v1
	v_cndmask_b32_e32 v1, v1, v2, vcc
	v_sub_f32_e32 v3, v31, v0
	v_mul_f32_e32 v3, v3, v1
	v_lshlrev_b32_e32 v2, 10, v160
	v_bfe_u32 v4, v3, 16, 1
	v_add3_u32 v3, v3, v4, s90
	v_add3_u32 v2, 0, v2, v16
	ds_write_b16_d16_hi v2, v3
	v_sub_f32_e32 v3, v15, v0
	v_mul_f32_e32 v3, v3, v1
	v_bfe_u32 v4, v3, 16, 1
	v_add3_u32 v3, v3, v4, s90
	ds_write_b16_d16_hi v2, v3 offset:64
	v_sub_f32_e32 v3, v47, v0
	v_mul_f32_e32 v3, v3, v1
	v_bfe_u32 v4, v3, 16, 1
	v_add3_u32 v3, v3, v4, s90
	ds_write_b16_d16_hi v2, v3 offset:128
	v_sub_f32_e32 v3, v63, v0
	v_mul_f32_e32 v3, v3, v1
	v_bfe_u32 v4, v3, 16, 1
	v_add3_u32 v3, v3, v4, s90
	ds_write_b16_d16_hi v2, v3 offset:192
	v_sub_f32_e32 v3, v111, v0
	v_mul_f32_e32 v3, v3, v1
	v_bfe_u32 v4, v3, 16, 1
	v_add3_u32 v3, v3, v4, s90
	ds_write_b16_d16_hi v2, v3 offset:256
	v_sub_f32_e32 v3, v127, v0
	v_mul_f32_e32 v3, v3, v1
	v_bfe_u32 v4, v3, 16, 1
	v_add3_u32 v3, v3, v4, s90
	ds_write_b16_d16_hi v2, v3 offset:320
	v_sub_f32_e32 v3, v95, v0
	v_sub_f32_e32 v0, v79, v0
	v_mul_f32_e32 v3, v3, v1
	v_mul_f32_e32 v0, v0, v1
	v_bfe_u32 v4, v3, 16, 1
	v_bfe_u32 v1, v0, 16, 1
	v_add3_u32 v3, v3, v4, s90
	v_add3_u32 v0, v0, v1, s90
	v_cmp_gt_i32_e32 vcc, s88, v232
	ds_write_b16_d16_hi v2, v3 offset:384
	ds_write_b16_d16_hi v2, v0 offset:448
	s_waitcnt lgkmcnt(0)
	s_barrier
	s_and_saveexec_b64 s[36:37], vcc
	s_cbranch_execz .LBB0_4301
	s_lshl_b32 s4, s8, 2
	s_add_u32 s38, s51, s4
	s_addc_u32 s39, s52, 0
	s_lshl_b64 s[2:3], s[2:3], 11
	s_add_u32 s4, s53, s2
	s_addc_u32 s5, s54, s3
	s_add_u32 s40, s4, s8
	s_addc_u32 s41, s5, 0
	s_add_u32 s2, s55, s2
	s_addc_u32 s3, s56, s3
	s_add_u32 s42, s2, s8
	s_addc_u32 s43, s3, 0
	v_lshl_add_u32 v4, v232, 4, 0
	v_lshlrev_b32_e32 v5, 3, v232
	s_mov_b64 s[44:45], 0
; #define LAS __attribute__((address_space(3)))
; __device__ __forceinline__ float sigmoidf_(float x) { return 1.f / (1.f + __expf(-x)); }
; __device__ __forceinline__ float siluf_(float x) { return x / (1.f + __expf(-x)); }
; __device__ __forceinline__ unsigned pk4_fp8c(float a, float b, float c, float d) { return pk4_fp8(__builtin_amdgcn_fmed3f(a, -448.f, 448.f), __builtin_amdgcn_fmed3f(b, -448.f, 448.f), __builtin_amdgcn_fmed3f(c, -448.f, 448.f), __builtin_amdgcn_fmed3f(d, -448.f, 448.f)); }
; template <int DK, int DV, bool MLSTM>
; __device__ __forceinline__ void out_unit2(LAS unsigned char* lds, LAS unsigned char* ldstab, const OutArgs a, const int wv) {
;     ...
;     for (int id = tid; id < 128 * CPR; id += 512) { const int row = id / CPR, ch = id % CPR;
;         const u32x4 y = *(const LAS u32x4*)(lds + row * TP + ch * 16);
;         const f32x4 g0 = *(const f32x4*)(a.gain + 8 * ch), g1 = *(const f32x4*)(a.gain + 8 * ch + 4);
;         float yv[8] = {bf_lo(y.x), bf_hi(y.x), bf_lo(y.y), bf_hi(y.y), bf_lo(y.z), bf_hi(y.z), bf_lo(y.w), bf_hi(y.w)};
;         float gv[8];
;         if (MLSTM) { const u32x4 g = *(const u32x4*)(a.G + (size_t)row * a.ldg + 8 * ch);
;             gv[0] = bf_lo(g.x); gv[1] = bf_hi(g.x); gv[2] = bf_lo(g.y); gv[3] = bf_hi(g.y); gv[4] = bf_lo(g.z); gv[5] = bf_hi(g.z); gv[6] = bf_lo(g.w); gv[7] = bf_hi(g.w); }
;         else { const u32x2 g = *(const u32x2*)(a.G8 + (size_t)row * a.ldg8 + 8 * ch);
;             const f32x2 e0 = __builtin_amdgcn_cvt_pk_f32_fp8((int)g.x, false), e1 = __builtin_amdgcn_cvt_pk_f32_fp8((int)g.x, true), e2 = __builtin_amdgcn_cvt_pk_f32_fp8((int)g.y, false), e3 = __builtin_amdgcn_cvt_pk_f32_fp8((int)g.y, true);
;             gv[0] = e0[0] * a.g8inv; gv[1] = e0[1] * a.g8inv; gv[2] = e1[0] * a.g8inv; gv[3] = e1[1] * a.g8inv; gv[4] = e2[0] * a.g8inv; gv[5] = e2[1] * a.g8inv; gv[6] = e3[0] * a.g8inv; gv[7] = e3[1] * a.g8inv; }
;         float gn[8] = {g0[0], g0[1], g0[2], g0[3], g1[0], g1[1], g1[2], g1[3]};
;         float ov[8];
; #pragma unroll
;         for (int i = 0; i < 8; ++i) ov[i] = yv[i] * gn[i] * (MLSTM ? sigmoidf_(gv[i]) : siluf_(gv[i]));
;         u32x2 w; w.x = pg8::pk4_fp8c(ov[0] * a.oscale, ov[1] * a.oscale, ov[2] * a.oscale, ov[3] * a.oscale); w.y = pg8::pk4_fp8c(ov[4] * a.oscale, ov[5] * a.oscale, ov[6] * a.oscale, ov[7] * a.oscale);
;         *(u32x2*)(a.Out + (size_t)row * a.ldo + 8 * ch) = w; }
.LBB0_4315:
	v_ashrrev_i32_e32 v6, 31, v232
	ds_read_b128 v[0:3], v4
	v_lshrrev_b32_e32 v6, 26, v6
	v_add_u32_e32 v6, v232, v6
	v_add_u32_e32 v7, 0x200, v232
	v_ashrrev_i32_e32 v6, 6, v6
	v_cmp_lt_i32_e32 vcc, s92, v232
	v_mov_b32_e32 v232, v7
	v_lshlrev_b32_e32 v8, 9, v6
	v_ashrrev_i32_e32 v7, 31, v6
	v_sub_u32_e32 v26, v5, v8
	v_lshlrev_b64 v[28:29], 11, v[6:7]
	s_waitcnt lgkmcnt(0)
	v_lshlrev_b32_e32 v162, 16, v0
	v_and_b32_e32 v10, 0xffff0000, v0
	v_lshlrev_b32_e32 v12, 16, v1
	v_and_b32_e32 v14, 0xffff0000, v1
	v_ashrrev_i32_e32 v27, 31, v26
	v_lshl_add_u64 v[0:1], s[40:41], 0, v[28:29]
	v_lshl_add_u64 v[6:7], v[26:27], 2, s[38:39]
	v_lshl_add_u64 v[0:1], v[0:1], 0, v[26:27]
	v_lshlrev_b32_e32 v16, 16, v2
	v_and_b32_e32 v18, 0xffff0000, v2
	v_lshlrev_b32_e32 v20, 16, v3
	v_and_b32_e32 v22, 0xffff0000, v3
	global_load_dwordx2 v[30:31], v[0:1], off
	s_nop 0
	global_load_dwordx4 v[0:3], v[6:7], off
	s_nop 0
	global_load_dwordx4 v[6:9], v[6:7], off offset:16
	v_mov_b32_e32 v11, v163
	v_mov_b32_e32 v13, v163
	v_mov_b32_e32 v15, v163
	v_mov_b32_e32 v19, v163
	v_mov_b32_e32 v21, v163
	v_mov_b32_e32 v17, v163
	v_mov_b32_e32 v23, v163
	s_or_b64 s[44:45], vcc, s[44:45]
	v_mov_b32_e32 v24, 0
	v_mov_b32_e32 v25, 0
	v_add_u32_e32 v4, 0x2000, v4
	v_add_u32_e32 v5, 0x1000, v5
	s_waitcnt vmcnt(2)
	v_cvt_pk_f32_fp8_e32 v[32:33], v30
	v_cvt_pk_f32_fp8_sdwa v[34:35], v30 src0_sel:WORD_1
	v_cvt_pk_f32_fp8_e32 v[36:37], v31
	v_cvt_pk_f32_fp8_sdwa v[30:31], v31 src0_sel:WORD_1
	s_waitcnt vmcnt(1)
	v_mov_b32_e32 v38, v0
	v_mov_b32_e32 v39, v32
	v_mov_b32_e32 v0, v2
	s_waitcnt vmcnt(0)
	v_mov_b32_e32 v2, v6
	v_mov_b32_e32 v6, v8
	v_mov_b32_e32 v32, v1
	v_mov_b32_e32 v1, v34
	v_mov_b32_e32 v34, v3
	v_mov_b32_e32 v3, v36
	v_mov_b32_e32 v36, v7
	v_mov_b32_e32 v7, v30
	v_mov_b32_e32 v30, v9
	v_pk_mul_f32 v[8:9], v[38:39], v[162:163]
	v_pk_mul_f32 v[10:11], v[32:33], v[10:11]
	v_pk_mul_f32 v[0:1], v[0:1], v[12:13]
	v_pk_mul_f32 v[12:13], v[34:35], v[14:15]
	v_pk_mul_f32 v[14:15], v[36:37], v[18:19]
	v_mul_f32_e32 v18, 0xbfb8aa3b, v9
	v_mul_f32_e32 v19, 0xbfb8aa3b, v11
	v_exp_f32_e32 v18, v18
	v_pk_mul_f32 v[6:7], v[6:7], v[20:21]
	v_mul_f32_e32 v20, 0xbfb8aa3b, v1
	v_exp_f32_e32 v19, v19
	v_pk_mul_f32 v[2:3], v[2:3], v[16:17]
	v_mul_f32_e32 v21, 0xbfb8aa3b, v13
	v_exp_f32_e32 v20, v20
	v_pk_mul_f32 v[16:17], v[30:31], v[22:23]
	v_mul_f32_e32 v22, 0xbfb8aa3b, v3
	v_exp_f32_e32 v21, v21
	v_mul_f32_e32 v23, 0xbfb8aa3b, v15
	v_exp_f32_e32 v22, v22
	v_add_f32_e32 v18, 1.0, v18
	v_exp_f32_e32 v23, v23
	v_add_f32_e32 v19, 1.0, v19
	v_div_scale_f32 v32, s[2:3], v18, v18, v9
	v_add_f32_e32 v20, 1.0, v20
	v_div_scale_f32 v34, s[2:3], v19, v19, v11
	v_rcp_f32_e32 v48, v32
	v_mul_f32_e32 v30, 0xbfb8aa3b, v7
	v_add_f32_e32 v21, 1.0, v21
	v_div_scale_f32 v36, s[4:5], v20, v20, v1
	v_rcp_f32_e32 v49, v34
	v_mul_f32_e32 v31, 0xbfb8aa3b, v17
	v_exp_f32_e32 v30, v30
	v_add_f32_e32 v22, 1.0, v22
	v_div_scale_f32 v38, s[6:7], v21, v21, v13
	v_rcp_f32_e32 v50, v36
	v_exp_f32_e32 v31, v31
	v_add_f32_e32 v23, 1.0, v23
	v_div_scale_f32 v40, s[8:9], v22, v22, v3
	v_rcp_f32_e32 v51, v38
	v_div_scale_f32 v42, s[10:11], v23, v23, v15
	v_rcp_f32_e32 v52, v40
	v_fma_f32 v56, -v32, v48, 1.0
	v_div_scale_f32 v33, vcc, v9, v18, v9
	v_rcp_f32_e32 v53, v42
	v_fma_f32 v57, -v34, v49, 1.0
	v_fmac_f32_e32 v48, v56, v48
	v_add_f32_e32 v30, 1.0, v30
	v_div_scale_f32 v35, s[2:3], v11, v19, v11
	v_fma_f32 v58, -v36, v50, 1.0
	v_fmac_f32_e32 v49, v57, v49
	v_mul_f32_e32 v56, v33, v48
	v_add_f32_e32 v31, 1.0, v31
	v_div_scale_f32 v37, s[4:5], v1, v20, v1
	v_div_scale_f32 v44, s[12:13], v30, v30, v7
	v_fma_f32 v59, -v38, v51, 1.0
	v_fmac_f32_e32 v50, v58, v50
	v_mul_f32_e32 v57, v35, v49
	v_fma_f32 v64, -v32, v56, v33
	v_div_scale_f32 v39, s[6:7], v13, v21, v13
	v_div_scale_f32 v46, s[14:15], v31, v31, v17
	v_rcp_f32_e32 v54, v44
	v_fma_f32 v60, -v40, v52, 1.0
	v_fmac_f32_e32 v51, v59, v51
	v_mul_f32_e32 v58, v37, v50
	v_fma_f32 v65, -v34, v57, v35
	v_fmac_f32_e32 v56, v64, v48
	v_div_scale_f32 v41, s[8:9], v3, v22, v3
	v_rcp_f32_e32 v55, v46
	v_fma_f32 v61, -v42, v53, 1.0
	v_fmac_f32_e32 v52, v60, v52
	v_mul_f32_e32 v59, v39, v51
	v_fma_f32 v66, -v36, v58, v37
	v_fmac_f32_e32 v57, v65, v49
	v_fma_f32 v32, -v32, v56, v33
	v_div_scale_f32 v43, s[10:11], v15, v23, v15
	v_fmac_f32_e32 v53, v61, v53
	v_mul_f32_e32 v60, v41, v52
	v_fma_f32 v67, -v38, v59, v39
	v_fmac_f32_e32 v58, v66, v50
	v_fma_f32 v33, -v34, v57, v35
	v_div_fmas_f32 v32, v32, v48, v56
	s_mov_b64 vcc, s[2:3]
	v_mul_f32_e32 v61, v43, v53
	v_fma_f32 v68, -v40, v60, v41
	v_fmac_f32_e32 v59, v67, v51
	v_fma_f32 v34, -v36, v58, v37
	v_div_fixup_f32 v9, v32, v18, v9
	v_div_fmas_f32 v18, v33, v49, v57
	s_mov_b64 vcc, s[4:5]
	v_fma_f32 v62, -v44, v54, 1.0
	v_fma_f32 v69, -v42, v61, v43
	v_fmac_f32_e32 v60, v68, v52
	v_fma_f32 v35, -v38, v59, v39
	v_mul_f32_e32 v8, v8, v9
	v_div_fixup_f32 v9, v18, v19, v11
	v_div_fmas_f32 v11, v34, v50, v58
	s_mov_b64 vcc, s[6:7]
	v_div_scale_f32 v45, s[12:13], v7, v30, v7
	v_fma_f32 v63, -v46, v55, 1.0
	v_fmac_f32_e32 v54, v62, v54
	v_fmac_f32_e32 v61, v69, v53
	v_fma_f32 v36, -v40, v60, v41
	v_mul_f32_e32 v9, v10, v9
	v_div_fixup_f32 v1, v11, v20, v1
	v_div_fmas_f32 v10, v35, v51, v59
	s_mov_b64 vcc, s[8:9]
	v_div_scale_f32 v47, s[14:15], v17, v31, v17
	v_fmac_f32_e32 v55, v63, v55
	v_mul_f32_e32 v62, v45, v54
	v_fma_f32 v37, -v42, v61, v43
	v_mul_f32_e32 v0, v0, v1
	v_div_fixup_f32 v1, v10, v21, v13
	v_div_fmas_f32 v10, v36, v52, v60
	s_mov_b64 vcc, s[10:11]
	v_mul_f32_e32 v63, v47, v55
	v_fma_f32 v70, -v44, v62, v45
	v_div_fixup_f32 v3, v10, v22, v3
	v_div_fmas_f32 v10, v37, v53, v61
	v_fma_f32 v71, -v46, v63, v47
	v_fmac_f32_e32 v62, v70, v54
	v_mul_f32_e32 v8, 0x41800000, v8
	v_mul_f32_e32 v9, 0x41800000, v9
	v_mul_f32_e32 v2, v2, v3
	v_div_fixup_f32 v3, v10, v23, v15
	v_fmac_f32_e32 v63, v71, v55
	v_fma_f32 v38, -v44, v62, v45
	v_med3_f32 v8, v8, s91, v231
	v_med3_f32 v9, v9, s91, v231
	s_mov_b64 vcc, s[12:13]
	v_mul_f32_e32 v3, v14, v3
	v_fma_f32 v39, -v46, v63, v47
	v_div_fmas_f32 v10, v38, v54, v62
	v_cvt_pk_fp8_f32 v24, v8, v9
	s_mov_b64 vcc, s[14:15]
	v_mul_f32_e32 v2, 0x41800000, v2
	v_mul_f32_e32 v3, 0x41800000, v3
	v_mul_f32_e32 v1, v12, v1
	v_div_fixup_f32 v7, v10, v30, v7
	v_div_fmas_f32 v8, v39, v55, v63
	v_med3_f32 v2, v2, s91, v231
	v_med3_f32 v3, v3, s91, v231
	v_mul_f32_e32 v0, 0x41800000, v0
	v_mul_f32_e32 v1, 0x41800000, v1
	v_mul_f32_e32 v6, v6, v7
	v_div_fixup_f32 v7, v8, v31, v17
	v_cvt_pk_fp8_f32 v25, v2, v3
	v_med3_f32 v0, v0, s91, v231
	v_med3_f32 v1, v1, s91, v231
	v_mul_f32_e32 v7, v16, v7
	v_mul_f32_e32 v6, 0x41800000, v6
	v_cvt_pk_fp8_f32 v24, v0, v1 op_sel:[0,0,1]
	v_mul_f32_e32 v0, 0x41800000, v7
	v_med3_f32 v1, v6, s91, v231
	v_med3_f32 v0, v0, s91, v231
	v_cvt_pk_fp8_f32 v25, v1, v0 op_sel:[0,0,1]
	v_lshl_add_u64 v[0:1], s[42:43], 0, v[28:29]
	v_lshl_add_u64 v[0:1], v[0:1], 0, v[26:27]
	global_store_dwordx2 v[0:1], v[24:25], off
	s_andn2_b64 exec, exec, s[44:45]
	s_cbranch_execnz .LBB0_4315
	s_branch .LBB0_4301

; #define LAS __attribute__((address_space(3)))
; #define TIDX(wv) (((wv) << 6) | lane_id())
; __device__ __forceinline__ const Args& fresh_args() { unsigned long long p = (unsigned long long)__builtin_amdgcn_kernarg_segment_ptr(); asm volatile("" : "+s"(p)); return *(const Args*)(CArgsP)p; }
; #define REP(k) for (int rep_ = 0; rep_ < ((PROBE_MASK >> (k)) & 1) + 1; ++rep_)
; #define GRID_BAR() do { if (fused) { for (int br_ = 0; br_ < (((PROBE_MASK >> 13) & 1) + 1); ++br_) xcd_barrier((gbar_t)(fresh_args().ws + WS_CTL) + CW_BAR, (volatile LAS unsigned*)((LAS unsigned char*)lds_raw + LT_MISC) + 8, wv); } } while (0)
; __global__ void __launch_bounds__(512, 2) fwd_kernel(Args a_kernarg) {
;     const Args& a0 = fresh_args();
;     LAS unsigned char* lds0 = (LAS unsigned char*)lds_raw;
;     const int wv = __builtin_amdgcn_readfirstlane((int)threadIdx.x >> 6);
;     for (int u = TIDX(wv); u < 64; u += 512) ((LAS unsigned*)(lds0 + LT_MISC))[u] = 0u;
;     __syncthreads();
;     const int lo = a0.ph_lo, hi = a0.ph_hi; const bool fused = (hi - lo) > 1;
;     if (fused) xcd_barrier_post((gbar_t)(a0.ws + WS_CTL) + CW_BAR, wv);
;     REP(12) if (IN(0)) { p0_prologue(fresh_args(), wv); GRID_BAR(); }
;     layer_body<0>(lo, hi, fused, wv); layer_body<1>(lo, hi, fused, wv); layer_body<2>(lo, hi, fused, wv); layer_body<3>(lo, hi, fused, wv);
;     if (IN(49)) n1_phase(fresh_args(), DEPTH, true, wv);
; }
	.amdhsa_kernel _Z10fwd_kernel4Args
		.amdhsa_group_segment_fixed_size 0
		.amdhsa_private_segment_fixed_size 0
		.amdhsa_kernarg_size 520
		.amdhsa_user_sgpr_count 2
		.amdhsa_user_sgpr_dispatch_ptr 0
		.amdhsa_user_sgpr_queue_ptr 0
		.amdhsa_user_sgpr_kernarg_segment_ptr 1
		.amdhsa_user_sgpr_dispatch_id 0
		.amdhsa_user_sgpr_kernarg_preload_length 0
		.amdhsa_user_sgpr_kernarg_preload_offset 0
		.amdhsa_user_sgpr_private_segment_size 0
		.amdhsa_uses_dynamic_stack 0
		.amdhsa_enable_private_segment 0
		.amdhsa_system_sgpr_workgroup_id_x 1
		.amdhsa_system_sgpr_workgroup_id_y 0
		.amdhsa_system_sgpr_workgroup_id_z 0
		.amdhsa_system_sgpr_workgroup_info 0
		.amdhsa_system_vgpr_workitem_id 0
		.amdhsa_next_free_vgpr 256
		.amdhsa_next_free_sgpr 98
		.amdhsa_accum_offset 256
		.amdhsa_reserve_vcc 1
		.amdhsa_float_round_mode_32 0
		.amdhsa_float_round_mode_16_64 0
		.amdhsa_float_denorm_mode_32 3
		.amdhsa_float_denorm_mode_16_64 3
		.amdhsa_dx10_clamp 1
		.amdhsa_ieee_mode 1
		.amdhsa_fp16_overflow 0
		.amdhsa_tg_split 0
		.amdhsa_exception_fp_ieee_invalid_op 0
		.amdhsa_exception_fp_denorm_src 0
		.amdhsa_exception_fp_ieee_div_zero 0
		.amdhsa_exception_fp_ieee_overflow 0
		.amdhsa_exception_fp_ieee_underflow 0
		.amdhsa_exception_fp_ieee_inexact 0
		.amdhsa_exception_int_div_zero 0
	.end_amdhsa_kernel

; #define LAS __attribute__((address_space(3)))
; #define TIDX(wv) (((wv) << 6) | lane_id())
; __device__ __forceinline__ const Args& fresh_args() { unsigned long long p = (unsigned long long)__builtin_amdgcn_kernarg_segment_ptr(); asm volatile("" : "+s"(p)); return *(const Args*)(CArgsP)p; }
; #define REP(k) for (int rep_ = 0; rep_ < ((PROBE_MASK >> (k)) & 1) + 1; ++rep_)
; #define GRID_BAR() do { if (fused) { for (int br_ = 0; br_ < (((PROBE_MASK >> 13) & 1) + 1); ++br_) xcd_barrier((gbar_t)(fresh_args().ws + WS_CTL) + CW_BAR, (volatile LAS unsigned*)((LAS unsigned char*)lds_raw + LT_MISC) + 8, wv); } } while (0)
; __global__ void __launch_bounds__(512, 2) fwd_kernel(Args a_kernarg) {
;     const Args& a0 = fresh_args();
;     LAS unsigned char* lds0 = (LAS unsigned char*)lds_raw;
;     const int wv = __builtin_amdgcn_readfirstlane((int)threadIdx.x >> 6);
;     for (int u = TIDX(wv); u < 64; u += 512) ((LAS unsigned*)(lds0 + LT_MISC))[u] = 0u;
;     __syncthreads();
;     const int lo = a0.ph_lo, hi = a0.ph_hi; const bool fused = (hi - lo) > 1;
;     if (fused) xcd_barrier_post((gbar_t)(a0.ws + WS_CTL) + CW_BAR, wv);
;     REP(12) if (IN(0)) { p0_prologue(fresh_args(), wv); GRID_BAR(); }
;     layer_body<0>(lo, hi, fused, wv); layer_body<1>(lo, hi, fused, wv); layer_body<2>(lo, hi, fused, wv); layer_body<3>(lo, hi, fused, wv);
;     if (IN(49)) n1_phase(fresh_args(), DEPTH, true, wv);
; }
amdhsa.kernels:
  - .agpr_count:     0
    .args:
      - .offset:         0
        .size:           264
        .value_kind:     by_value
      - .offset:         264
        .size:           4
        .value_kind:     hidden_block_count_x
      - .offset:         268
        .size:           4
        .value_kind:     hidden_block_count_y
      - .offset:         272
        .size:           4
        .value_kind:     hidden_block_count_z
      - .offset:         276
        .size:           2
        .value_kind:     hidden_group_size_x
      - .offset:         278
        .size:           2
        .value_kind:     hidden_group_size_y
      - .offset:         280
        .size:           2
        .value_kind:     hidden_group_size_z
      - .offset:         282
        .size:           2
        .value_kind:     hidden_remainder_x
      - .offset:         284
        .size:           2
        .value_kind:     hidden_remainder_y
      - .offset:         286
        .size:           2
        .value_kind:     hidden_remainder_z
      - .offset:         304
        .size:           8
        .value_kind:     hidden_global_offset_x
      - .offset:         312
        .size:           8
        .value_kind:     hidden_global_offset_y
      - .offset:         320
        .size:           8
        .value_kind:     hidden_global_offset_z
      - .offset:         328
        .size:           2
        .value_kind:     hidden_grid_dims
      - .offset:         384
        .size:           4
        .value_kind:     hidden_dynamic_lds_size
    .group_segment_fixed_size: 0
    .kernarg_segment_align: 8
    .kernarg_segment_size: 520
    .language:       OpenCL C
    .language_version:
      - 2
      - 0
    .max_flat_workgroup_size: 512
    .name:           _Z10fwd_kernel4Args
    .private_segment_fixed_size: 0
    .sgpr_count:     104
    .sgpr_spill_count: 0
    .symbol:         _Z10fwd_kernel4Args.kd
    .uniform_work_group_size: 1
    .uses_dynamic_stack: false
    .vgpr_count:     256
    .vgpr_spill_count: 0
    .wavefront_size: 64
